# v23 + LDS-DMA offset v_mov copies removed in GEMM load phases + epilogue s_nop pad trimmed
# baseline (speedup 1.0000x reference)
.LBB0_134:
	s_lshr_b32 s84, s26, 2
	s_mov_b32 s27, s83
	s_mov_b64 s[2:3], s[78:79]
	s_waitcnt vmcnt(0) lgkmcnt(0)
	v_mov_b32_e32 v2, v0
	s_cmp_ge_i32 s27, s84
	v_readfirstlane_b32 s10, v2
	s_cbranch_scc1 .LBB0_150
	v_bfe_i32 v4, v2, 27, 1
	v_lshlrev_b32_e32 v3, 4, v2
	v_lshrrev_b32_e32 v4, 22, v4
	v_add_u32_e32 v4, v3, v4
	v_and_b32_e32 v4, 0xfffffc00, v4
	v_sub_u32_e32 v4, v3, v4
	v_ashrrev_i32_e32 v1, 31, v2
	v_lshrrev_b32_e32 v5, 4, v4
	v_lshrrev_b32_e32 v1, 26, v1
	v_bitop3_b32 v5, v5, v4, 32 bitop3:0x6c
	v_ashrrev_i32_e32 v4, 31, v4
	v_add_u32_e32 v1, v2, v1
	v_lshrrev_b32_e32 v4, 26, v4
	v_ashrrev_i32_e32 v1, 6, v1
	v_add_u32_e32 v4, v5, v4
	v_lshlrev_b32_e32 v6, 3, v1
	v_ashrrev_i32_e32 v4, 6, v4
	v_and_b32_e32 v6, -16, v6
	v_mul_i32_i24_e32 v7, 64, v4
	s_lshr_b32 s28, s26, 5
	v_add_u32_e32 v6, v4, v6
	v_sub_u32_e32 v5, v5, v7
	s_add_u32 s29, s2, 0x6200000
	v_lshlrev_b32_e32 v1, 5, v1
	v_ashrrev_i16_sdwa v5, v188, sext(v5) dst_sel:DWORD dst_unused:UNUSED_PAD src0_sel:DWORD src1_sel:BYTE_0
	v_lshlrev_b32_e32 v7, 1, v6
	v_lshrrev_b32_e32 v8, 2, v6
	v_and_b32_e32 v4, 3, v4
	s_mov_b32 s2, 0x1fffe0
	v_and_b32_e32 v1, 32, v1
	v_bfe_i32 v5, v5, 0, 16
	v_and_b32_e32 v7, 24, v7
	v_and_b32_e32 v8, 4, v8
	v_and_or_b32 v4, v6, s2, v4
	v_or3_b32 v4, v4, v8, v7
	v_add_lshl_u32 v5, v1, v5, 1
	v_add_u32_e32 v3, 0x2000, v3
	v_lshl_add_u32 v132, v4, 11, v5
	v_ashrrev_i32_e32 v4, 31, v3
	v_lshrrev_b32_e32 v4, 22, v4
	v_add_u32_e32 v4, v3, v4
	v_ashrrev_i32_e32 v4, 10, v4
	v_lshl_add_u32 v1, v6, 11, v5
	v_mul_i32_i24_e32 v5, 0x400, v4
	v_sub_u32_e32 v3, v3, v5
	v_lshrrev_b32_e32 v5, 4, v3
	v_bitop3_b32 v3, v5, v3, 32 bitop3:0x6c
	v_ashrrev_i32_e32 v6, 31, v3
	v_lshrrev_b32_e32 v6, 26, v6
	v_lshlrev_b32_e32 v5, 3, v4
	v_add_u32_e32 v6, v3, v6
	v_and_b32_e32 v5, -16, v5
	v_ashrrev_i32_e32 v7, 6, v6
	v_and_b32_e32 v6, 0xc0, v6
	v_add_u32_e32 v5, v7, v5
	v_sub_u32_e32 v3, v3, v6
	v_lshlrev_b32_e32 v4, 5, v4
	v_ashrrev_i16_sdwa v3, v188, sext(v3) dst_sel:DWORD dst_unused:UNUSED_PAD src0_sel:DWORD src1_sel:BYTE_0
	v_lshlrev_b32_e32 v6, 1, v5
	v_lshrrev_b32_e32 v8, 2, v5
	v_and_b32_e32 v7, 3, v7
	v_and_b32_e32 v4, 32, v4
	v_bfe_i32 v3, v3, 0, 16
	v_and_b32_e32 v6, 24, v6
	v_and_b32_e32 v8, 4, v8
	v_and_or_b32 v7, v5, s2, v7
	v_or3_b32 v6, v7, v8, v6
	v_add_lshl_u32 v3, v4, v3, 1
	v_lshl_add_u32 v133, v5, 11, v3
	v_lshl_add_u32 v134, v6, 11, v3
	v_cvt_f32_u32_e32 v3, s28
	s_addc_u32 s30, s3, 0
	s_ashr_i32 s34, s27, 31
	s_lshr_b32 s2, s34, 29
	v_rcp_iflag_f32_e32 v3, v3
	s_add_i32 s2, s27, s2
	s_ashr_i32 s3, s10, 6
	s_ashr_i32 s6, s2, 3
	v_mul_f32_e32 v3, 0x4f7ffffe, v3
	v_cvt_u32_f32_e32 v3, v3
	s_and_b32 s2, s2, -8
	s_ashr_i32 s11, s10, 8
	s_lshl_b32 s31, s3, 10
	s_sub_i32 s2, s27, s2
	s_or_b32 s35, s28, 1
	s_cmp_lt_i32 s2, 0
	s_cselect_b32 s7, s35, s28
	s_sub_i32 s8, 0, s28
	v_readfirstlane_b32 s36, v3
	s_mul_i32 s2, s2, s7
	s_mul_i32 s8, s8, s36
	s_add_i32 s2, s2, s6
	s_mul_hi_u32 s8, s36, s8
	s_abs_i32 s7, s2
	s_add_i32 s36, s36, s8
	s_mul_hi_u32 s8, s7, s36
	s_mul_i32 s9, s8, s28
	s_sub_i32 s7, s7, s9
	s_ashr_i32 s6, s2, 31
	s_add_i32 s9, s8, 1
	s_sub_i32 s12, s7, s28
	s_cmp_ge_u32 s7, s28
	s_cselect_b32 s8, s9, s8
	s_cselect_b32 s7, s12, s7
	s_add_i32 s9, s8, 1
	s_cmp_ge_u32 s7, s28
	s_cselect_b32 s7, s9, s8
	s_xor_b32 s7, s7, s6
	s_sub_i32 s6, s7, s6
	s_lshl_b32 s8, s6, 3
	s_sub_i32 s7, 64, s8
	s_min_i32 s9, s7, 8
	s_sext_i32_i16 s7, s9
	v_cvt_f32_i32_e32 v3, s7
	s_mul_i32 s6, s6, s28
	s_sub_i32 s12, s2, s6
	s_sext_i32_i16 s2, s12
	v_cvt_f32_i32_e32 v4, s2
	v_rcp_iflag_f32_e32 v5, v3
	s_xor_b32 s2, s2, s7
	s_ashr_i32 s2, s2, 30
	s_or_b32 s2, s2, 1
	v_mul_f32_e32 v5, v4, v5
	v_trunc_f32_e32 v5, v5
	v_fma_f32 v4, -v5, v3, v4
	v_cvt_i32_f32_e32 v5, v5
	v_cmp_ge_f32_e64 s[6:7], |v4|, |v3|
	s_and_b64 s[6:7], s[6:7], exec
	s_cselect_b32 s2, s2, 0
	v_readfirstlane_b32 s6, v5
	s_add_i32 s2, s6, s2
	s_mul_i32 s6, s2, s9
	s_sub_i32 s6, s12, s6
	s_sext_i32_i16 s6, s6
	s_add_i32 s8, s8, s6
	s_bfe_i64 s[6:7], s[2:3], 0x100000
	s_lshl_b32 s16, s8, 8
	s_lshl_b64 s[6:7], s[6:7], 19
	s_add_u32 s20, s4, s6
	s_addc_u32 s21, s5, s7
	s_ashr_i32 s17, s16, 31
	s_lshl_b64 s[6:7], s[16:17], 11
	s_add_i32 s17, s31, 0
	s_add_i32 m0, s17, 0x10000
	s_nop 0
	global_load_lds_dwordx4 v132, s[20:21]
	s_add_i32 m0, s17, 0x12000
	s_add_u32 s8, s20, 0x40000
	global_load_lds_dwordx4 v134, s[20:21]
	s_addc_u32 s9, s21, 0
	s_add_i32 m0, s17, 0x14000
	s_nop 0
	global_load_lds_dwordx4 v132, s[8:9]
	s_add_i32 m0, s17, 0x16000
	s_add_u32 s22, s29, s6
	global_load_lds_dwordx4 v134, s[8:9]
	s_addc_u32 s23, s30, s7
	s_mov_b32 m0, s17
	s_add_i32 s37, s17, 0x2000
	global_load_lds_dwordx4 v1, s[22:23]
	s_mov_b32 m0, s37
	s_add_u32 s6, s22, 0x40000
	global_load_lds_dwordx4 v133, s[22:23]
	s_addc_u32 s7, s23, 0
	s_add_i32 s40, s17, 0x4000
	s_mov_b32 m0, s40
	s_add_i32 s41, s17, 0x6000
	global_load_lds_dwordx4 v1, s[6:7]
	v_mov_b32_e32 v3, v133
	s_mov_b32 m0, s41
	s_cmp_eq_u32 s11, 1
	global_load_lds_dwordx4 v3, s[6:7]
	s_cselect_b64 s[6:7], -1, 0
	s_cmp_lg_u32 s11, 1
	s_cbranch_scc1 .LBB0_137
	s_barrier

.LBB0_143:
	s_add_u32 s22, s20, 0xfffc0080
	s_addc_u32 s23, s21, -1
	s_add_i32 s51, 0, 0x10000
	s_cmp_eq_u32 s50, 12
	s_cselect_b32 s23, s13, s23
	s_cselect_b32 s22, s47, s22
	v_add_u32_e32 v139, s51, v136
	s_cselect_b32 s25, s15, s49
	s_cselect_b32 s24, s14, s48
	s_add_i32 s54, 0, 0x14000
	ds_read_b128 v[140:143], v139
	ds_read_b128 v[144:147], v139 offset:1024
	ds_read_b128 v[148:151], v139 offset:2048
	ds_read_b128 v[152:155], v139 offset:3072
	v_add_u32_e32 v139, s54, v136
	ds_read_b128 v[156:159], v139
	ds_read_b128 v[160:163], v139 offset:1024
	ds_read_b128 v[172:175], v139 offset:2048
	ds_read_b128 v[176:179], v139 offset:3072
	v_mov_b32_e32 v139, v1
	ds_read_b128 v[180:183], v138
	ds_read_b128 v[200:203], v138 offset:1024
	ds_read_b128 v[204:207], v138 offset:2048
	ds_read_b128 v[208:211], v138 offset:3072
	ds_read_b128 v[212:215], v138 offset:4096
	ds_read_b128 v[216:219], v138 offset:5120
	ds_read_b128 v[220:223], v138 offset:6144
	ds_read_b128 v[224:227], v138 offset:7168
	s_add_i32 m0, s17, 0xc000
	s_nop 0
	global_load_lds_dwordx4 v139, s[20:21]
	s_add_i32 m0, s17, 0xe000
	s_nop 0
	global_load_lds_dwordx4 v133, s[20:21]
	s_waitcnt vmcnt(8)
	s_waitcnt lgkmcnt(0)
	s_barrier
	s_setprio 1
	s_waitcnt lgkmcnt(0)
	v_mfma_f32_16x16x32_bf16 v[126:129], v[140:143], v[180:183], v[126:129]
	v_mfma_f32_16x16x32_bf16 v[122:125], v[148:151], v[180:183], v[122:125]
	v_mfma_f32_16x16x32_bf16 v[118:121], v[140:143], v[204:207], v[118:121]
	v_mfma_f32_16x16x32_bf16 v[110:113], v[148:151], v[204:207], v[110:113]
	v_mfma_f32_16x16x32_bf16 v[102:105], v[140:143], v[212:215], v[102:105]
	v_mfma_f32_16x16x32_bf16 v[94:97], v[148:151], v[212:215], v[94:97]
	v_mfma_f32_16x16x32_bf16 v[86:89], v[140:143], v[220:223], v[86:89]
	v_mfma_f32_16x16x32_bf16 v[78:81], v[148:151], v[220:223], v[78:81]
	v_mfma_f32_16x16x32_bf16 v[126:129], v[144:147], v[200:203], v[126:129]
	v_mfma_f32_16x16x32_bf16 v[122:125], v[152:155], v[200:203], v[122:125]
	v_mfma_f32_16x16x32_bf16 v[118:121], v[144:147], v[208:211], v[118:121]
	v_mfma_f32_16x16x32_bf16 v[110:113], v[152:155], v[208:211], v[110:113]
	v_mfma_f32_16x16x32_bf16 v[102:105], v[144:147], v[216:219], v[102:105]
	v_mfma_f32_16x16x32_bf16 v[94:97], v[152:155], v[216:219], v[94:97]
	v_mfma_f32_16x16x32_bf16 v[86:89], v[144:147], v[224:227], v[86:89]
	v_mfma_f32_16x16x32_bf16 v[78:81], v[152:155], v[224:227], v[78:81]
	s_setprio 0
	s_setprio 1
	v_mfma_f32_16x16x32_bf16 v[114:117], v[156:159], v[180:183], v[114:117]
	v_mfma_f32_16x16x32_bf16 v[106:109], v[172:175], v[180:183], v[106:109]
	v_mfma_f32_16x16x32_bf16 v[98:101], v[156:159], v[204:207], v[98:101]
	v_mfma_f32_16x16x32_bf16 v[90:93], v[172:175], v[204:207], v[90:93]
	v_mfma_f32_16x16x32_bf16 v[82:85], v[156:159], v[212:215], v[82:85]
	v_mfma_f32_16x16x32_bf16 v[74:77], v[172:175], v[212:215], v[74:77]
	v_mfma_f32_16x16x32_bf16 v[70:73], v[156:159], v[220:223], v[70:73]
	v_mfma_f32_16x16x32_bf16 v[66:69], v[172:175], v[220:223], v[66:69]
	v_mfma_f32_16x16x32_bf16 v[114:117], v[160:163], v[200:203], v[114:117]
	v_mfma_f32_16x16x32_bf16 v[106:109], v[176:179], v[200:203], v[106:109]
	v_mfma_f32_16x16x32_bf16 v[98:101], v[160:163], v[208:211], v[98:101]
	v_mfma_f32_16x16x32_bf16 v[90:93], v[176:179], v[208:211], v[90:93]
	v_mfma_f32_16x16x32_bf16 v[82:85], v[160:163], v[216:219], v[82:85]
	v_mfma_f32_16x16x32_bf16 v[74:77], v[176:179], v[216:219], v[74:77]
	v_mfma_f32_16x16x32_bf16 v[70:73], v[160:163], v[224:227], v[70:73]
	v_mfma_f32_16x16x32_bf16 v[66:69], v[176:179], v[224:227], v[66:69]
	s_setprio 0
	s_barrier
	v_mov_b32_e32 v139, v132
	s_add_i32 s51, s51, s31
	ds_read_b128 v[180:183], v138 offset:16384
	ds_read_b128 v[200:203], v138 offset:17408
	ds_read_b128 v[204:207], v138 offset:18432
	ds_read_b128 v[208:211], v138 offset:19456
	ds_read_b128 v[212:215], v138 offset:20480
	ds_read_b128 v[216:219], v138 offset:21504
	ds_read_b128 v[220:223], v138 offset:22528
	ds_read_b128 v[224:227], v138 offset:23552
	s_mov_b32 m0, s51
	s_nop 0
	global_load_lds_dwordx4 v139, s[24:25]
	s_add_i32 m0, s51, 0x2000
	s_add_u32 s52, s24, 0x40000
	global_load_lds_dwordx4 v134, s[24:25]
	s_addc_u32 s53, s25, 0
	s_add_i32 s51, s54, s31
	s_mov_b32 m0, s51
	s_nop 0
	global_load_lds_dwordx4 v132, s[52:53]
	s_add_i32 m0, s51, 0x2000
	s_nop 0
	global_load_lds_dwordx4 v134, s[52:53]
	s_mov_b32 m0, s17
	s_nop 0
	global_load_lds_dwordx4 v1, s[22:23]
	v_mov_b32_e32 v139, v133
	s_mov_b32 m0, s37
	s_nop 0
	global_load_lds_dwordx4 v139, s[22:23]
	s_waitcnt vmcnt(8)
	s_waitcnt lgkmcnt(0)
	s_barrier
	s_setprio 1
	s_waitcnt lgkmcnt(0)
	v_mfma_f32_16x16x32_bf16 v[62:65], v[140:143], v[180:183], v[62:65]
	v_mfma_f32_16x16x32_bf16 v[58:61], v[148:151], v[180:183], v[58:61]
	v_mfma_f32_16x16x32_bf16 v[54:57], v[140:143], v[204:207], v[54:57]
	v_mfma_f32_16x16x32_bf16 v[46:49], v[148:151], v[204:207], v[46:49]
	v_mfma_f32_16x16x32_bf16 v[38:41], v[140:143], v[212:215], v[38:41]
	v_mfma_f32_16x16x32_bf16 v[30:33], v[148:151], v[212:215], v[30:33]
	v_mfma_f32_16x16x32_bf16 v[22:25], v[140:143], v[220:223], v[22:25]
	v_mfma_f32_16x16x32_bf16 v[14:17], v[148:151], v[220:223], v[14:17]
	v_mfma_f32_16x16x32_bf16 v[62:65], v[144:147], v[200:203], v[62:65]
	v_mfma_f32_16x16x32_bf16 v[58:61], v[152:155], v[200:203], v[58:61]
	v_mfma_f32_16x16x32_bf16 v[54:57], v[144:147], v[208:211], v[54:57]
	v_mfma_f32_16x16x32_bf16 v[46:49], v[152:155], v[208:211], v[46:49]
	v_mfma_f32_16x16x32_bf16 v[38:41], v[144:147], v[216:219], v[38:41]
	v_mfma_f32_16x16x32_bf16 v[30:33], v[152:155], v[216:219], v[30:33]
	v_mfma_f32_16x16x32_bf16 v[22:25], v[144:147], v[224:227], v[22:25]
	v_mfma_f32_16x16x32_bf16 v[14:17], v[152:155], v[224:227], v[14:17]
	s_setprio 0
	s_setprio 1
	v_mfma_f32_16x16x32_bf16 v[50:53], v[156:159], v[180:183], v[50:53]
	v_mfma_f32_16x16x32_bf16 v[42:45], v[172:175], v[180:183], v[42:45]
	v_mfma_f32_16x16x32_bf16 v[34:37], v[156:159], v[204:207], v[34:37]
	v_mfma_f32_16x16x32_bf16 v[26:29], v[172:175], v[204:207], v[26:29]
	v_mfma_f32_16x16x32_bf16 v[18:21], v[156:159], v[212:215], v[18:21]
	v_mfma_f32_16x16x32_bf16 v[10:13], v[172:175], v[212:215], v[10:13]
	v_mfma_f32_16x16x32_bf16 v[6:9], v[156:159], v[220:223], v[6:9]
	v_mfma_f32_16x16x32_bf16 v[2:5], v[172:175], v[220:223], v[2:5]
	v_mfma_f32_16x16x32_bf16 v[50:53], v[160:163], v[200:203], v[50:53]
	v_mfma_f32_16x16x32_bf16 v[42:45], v[176:179], v[200:203], v[42:45]
	v_mfma_f32_16x16x32_bf16 v[34:37], v[160:163], v[208:211], v[34:37]
	v_mfma_f32_16x16x32_bf16 v[26:29], v[176:179], v[208:211], v[26:29]
	v_mfma_f32_16x16x32_bf16 v[18:21], v[160:163], v[216:219], v[18:21]
	v_mfma_f32_16x16x32_bf16 v[10:13], v[176:179], v[216:219], v[10:13]
	v_mfma_f32_16x16x32_bf16 v[6:9], v[160:163], v[224:227], v[6:9]
	v_mfma_f32_16x16x32_bf16 v[2:5], v[176:179], v[224:227], v[2:5]
	s_setprio 0
	s_barrier
	s_add_i32 s51, 0, 0x18000
	v_add_u32_e32 v139, s51, v136
	s_add_i32 s54, 0, 0x1c000
	ds_read_b128 v[140:143], v139
	ds_read_b128 v[144:147], v139 offset:1024
	ds_read_b128 v[148:151], v139 offset:2048
	ds_read_b128 v[152:155], v139 offset:3072
	v_add_u32_e32 v139, s54, v136
	ds_read_b128 v[156:159], v139
	ds_read_b128 v[160:163], v139 offset:1024
	ds_read_b128 v[172:175], v139 offset:2048
	ds_read_b128 v[176:179], v139 offset:3072
	s_add_u32 s52, s22, 0x40000
	v_mov_b32_e32 v139, v1
	s_mov_b32 m0, s40
	ds_read_b128 v[180:183], v138 offset:32768
	ds_read_b128 v[200:203], v138 offset:33792
	ds_read_b128 v[204:207], v138 offset:34816
	ds_read_b128 v[208:211], v138 offset:35840
	ds_read_b128 v[212:215], v138 offset:36864
	ds_read_b128 v[216:219], v138 offset:37888
	ds_read_b128 v[220:223], v138 offset:38912
	ds_read_b128 v[224:227], v138 offset:39936
	s_addc_u32 s53, s23, 0
	s_nop 0
	global_load_lds_dwordx4 v139, s[52:53]
	s_mov_b32 m0, s41
	s_nop 0
	global_load_lds_dwordx4 v133, s[52:53]
	s_waitcnt vmcnt(8)
	s_waitcnt lgkmcnt(0)
	s_barrier
	s_setprio 1
	s_waitcnt lgkmcnt(0)
	v_mfma_f32_16x16x32_bf16 v[126:129], v[140:143], v[180:183], v[126:129]
	v_mfma_f32_16x16x32_bf16 v[122:125], v[148:151], v[180:183], v[122:125]
	v_mfma_f32_16x16x32_bf16 v[118:121], v[140:143], v[204:207], v[118:121]
	v_mfma_f32_16x16x32_bf16 v[110:113], v[148:151], v[204:207], v[110:113]
	v_mfma_f32_16x16x32_bf16 v[102:105], v[140:143], v[212:215], v[102:105]
	v_mfma_f32_16x16x32_bf16 v[94:97], v[148:151], v[212:215], v[94:97]
	v_mfma_f32_16x16x32_bf16 v[86:89], v[140:143], v[220:223], v[86:89]
	v_mfma_f32_16x16x32_bf16 v[78:81], v[148:151], v[220:223], v[78:81]
	v_mfma_f32_16x16x32_bf16 v[126:129], v[144:147], v[200:203], v[126:129]
	v_mfma_f32_16x16x32_bf16 v[122:125], v[152:155], v[200:203], v[122:125]
	v_mfma_f32_16x16x32_bf16 v[118:121], v[144:147], v[208:211], v[118:121]
	v_mfma_f32_16x16x32_bf16 v[110:113], v[152:155], v[208:211], v[110:113]
	v_mfma_f32_16x16x32_bf16 v[102:105], v[144:147], v[216:219], v[102:105]
	v_mfma_f32_16x16x32_bf16 v[94:97], v[152:155], v[216:219], v[94:97]
	v_mfma_f32_16x16x32_bf16 v[86:89], v[144:147], v[224:227], v[86:89]
	v_mfma_f32_16x16x32_bf16 v[78:81], v[152:155], v[224:227], v[78:81]
	s_setprio 0
	s_setprio 1
	v_mfma_f32_16x16x32_bf16 v[114:117], v[156:159], v[180:183], v[114:117]
	v_mfma_f32_16x16x32_bf16 v[106:109], v[172:175], v[180:183], v[106:109]
	v_mfma_f32_16x16x32_bf16 v[98:101], v[156:159], v[204:207], v[98:101]
	v_mfma_f32_16x16x32_bf16 v[90:93], v[172:175], v[204:207], v[90:93]
	v_mfma_f32_16x16x32_bf16 v[82:85], v[156:159], v[212:215], v[82:85]
	v_mfma_f32_16x16x32_bf16 v[74:77], v[172:175], v[212:215], v[74:77]
	v_mfma_f32_16x16x32_bf16 v[70:73], v[156:159], v[220:223], v[70:73]
	v_mfma_f32_16x16x32_bf16 v[66:69], v[172:175], v[220:223], v[66:69]
	v_mfma_f32_16x16x32_bf16 v[114:117], v[160:163], v[200:203], v[114:117]
	v_mfma_f32_16x16x32_bf16 v[106:109], v[176:179], v[200:203], v[106:109]
	v_mfma_f32_16x16x32_bf16 v[98:101], v[160:163], v[208:211], v[98:101]
	v_mfma_f32_16x16x32_bf16 v[90:93], v[176:179], v[208:211], v[90:93]
	v_mfma_f32_16x16x32_bf16 v[82:85], v[160:163], v[216:219], v[82:85]
	v_mfma_f32_16x16x32_bf16 v[74:77], v[176:179], v[216:219], v[74:77]
	v_mfma_f32_16x16x32_bf16 v[70:73], v[160:163], v[224:227], v[70:73]
	v_mfma_f32_16x16x32_bf16 v[66:69], v[176:179], v[224:227], v[66:69]
	s_setprio 0
	s_barrier
	v_mov_b32_e32 v166, v132
	ds_read_b128 v[180:183], v138 offset:49152
	ds_read_b128 v[200:203], v138 offset:50176
	ds_read_b128 v[204:207], v138 offset:51200
	ds_read_b128 v[208:211], v138 offset:52224
	ds_read_b128 v[212:215], v138 offset:53248
	ds_read_b128 v[216:219], v138 offset:54272
	ds_read_b128 v[220:223], v138 offset:55296
	ds_read_b128 v[224:227], v138 offset:56320
	s_add_i32 s51, s51, s31
	v_lshl_add_u64 v[164:165], s[24:25], 0, v[166:167]
	v_lshl_add_u64 v[164:165], v[164:165], 0, s[80:81]
	s_mov_b32 m0, s51
	v_mov_b32_e32 v166, v134
	global_load_lds_dwordx4 v[164:165], off
	s_add_i32 m0, s51, 0x2000
	v_mov_b32_e32 v139, v132
	v_lshl_add_u64 v[164:165], s[24:25], 0, v[166:167]
	s_add_u32 s24, s24, 0x40080
	v_lshl_add_u64 v[164:165], v[164:165], 0, s[80:81]
	s_addc_u32 s25, s25, 0
	s_add_i32 s51, s54, s31
	global_load_lds_dwordx4 v[164:165], off
	s_mov_b32 m0, s51
	v_mov_b32_e32 v166, v1
	global_load_lds_dwordx4 v139, s[24:25]
	v_mov_b32_e32 v139, v134
	s_add_i32 m0, s51, 0x2000
	s_nop 0
	global_load_lds_dwordx4 v139, s[24:25]
	s_mov_b32 m0, s42
	v_lshl_add_u64 v[164:165], s[22:23], 0, v[166:167]
	v_lshl_add_u64 v[164:165], v[164:165], 0, s[80:81]
	v_mov_b32_e32 v166, v133
	global_load_lds_dwordx4 v[164:165], off
	s_mov_b32 m0, s43
	v_lshl_add_u64 v[164:165], s[22:23], 0, v[166:167]
	v_lshl_add_u64 v[164:165], v[164:165], 0, s[80:81]
	global_load_lds_dwordx4 v[164:165], off
	s_waitcnt vmcnt(8)
	s_waitcnt lgkmcnt(0)
	s_barrier
	s_setprio 1
	s_waitcnt lgkmcnt(0)
	v_mfma_f32_16x16x32_bf16 v[62:65], v[140:143], v[180:183], v[62:65]
	v_mfma_f32_16x16x32_bf16 v[58:61], v[148:151], v[180:183], v[58:61]
	v_mfma_f32_16x16x32_bf16 v[54:57], v[140:143], v[204:207], v[54:57]
	v_mfma_f32_16x16x32_bf16 v[46:49], v[148:151], v[204:207], v[46:49]
	v_mfma_f32_16x16x32_bf16 v[38:41], v[140:143], v[212:215], v[38:41]
	v_mfma_f32_16x16x32_bf16 v[30:33], v[148:151], v[212:215], v[30:33]
	v_mfma_f32_16x16x32_bf16 v[22:25], v[140:143], v[220:223], v[22:25]
	v_mfma_f32_16x16x32_bf16 v[14:17], v[148:151], v[220:223], v[14:17]
	v_mfma_f32_16x16x32_bf16 v[62:65], v[144:147], v[200:203], v[62:65]
	v_mfma_f32_16x16x32_bf16 v[58:61], v[152:155], v[200:203], v[58:61]
	v_mfma_f32_16x16x32_bf16 v[54:57], v[144:147], v[208:211], v[54:57]
	v_mfma_f32_16x16x32_bf16 v[46:49], v[152:155], v[208:211], v[46:49]
	v_mfma_f32_16x16x32_bf16 v[38:41], v[144:147], v[216:219], v[38:41]
	v_mfma_f32_16x16x32_bf16 v[30:33], v[152:155], v[216:219], v[30:33]
	v_mfma_f32_16x16x32_bf16 v[22:25], v[144:147], v[224:227], v[22:25]
	v_mfma_f32_16x16x32_bf16 v[14:17], v[152:155], v[224:227], v[14:17]
	s_setprio 0
	s_setprio 1
	v_mfma_f32_16x16x32_bf16 v[50:53], v[156:159], v[180:183], v[50:53]
	v_mfma_f32_16x16x32_bf16 v[42:45], v[172:175], v[180:183], v[42:45]
	v_mfma_f32_16x16x32_bf16 v[34:37], v[156:159], v[204:207], v[34:37]
	v_mfma_f32_16x16x32_bf16 v[26:29], v[172:175], v[204:207], v[26:29]
	v_mfma_f32_16x16x32_bf16 v[18:21], v[156:159], v[212:215], v[18:21]
	v_mfma_f32_16x16x32_bf16 v[10:13], v[172:175], v[212:215], v[10:13]
	v_mfma_f32_16x16x32_bf16 v[6:9], v[156:159], v[220:223], v[6:9]
	v_mfma_f32_16x16x32_bf16 v[2:5], v[172:175], v[220:223], v[2:5]
	v_mfma_f32_16x16x32_bf16 v[50:53], v[160:163], v[200:203], v[50:53]
	v_mfma_f32_16x16x32_bf16 v[42:45], v[176:179], v[200:203], v[42:45]
	v_mfma_f32_16x16x32_bf16 v[34:37], v[160:163], v[208:211], v[34:37]
	v_mfma_f32_16x16x32_bf16 v[26:29], v[176:179], v[208:211], v[26:29]
	v_mfma_f32_16x16x32_bf16 v[18:21], v[160:163], v[216:219], v[18:21]
	v_mfma_f32_16x16x32_bf16 v[10:13], v[176:179], v[216:219], v[10:13]
	v_mfma_f32_16x16x32_bf16 v[6:9], v[160:163], v[224:227], v[6:9]
	v_mfma_f32_16x16x32_bf16 v[2:5], v[176:179], v[224:227], v[2:5]
	s_setprio 0
	s_barrier
	s_add_i32 s50, s50, 2
	s_add_u32 s48, s48, 0x100
	s_addc_u32 s49, s49, 0
	s_add_u32 s20, s20, 0x100
	s_addc_u32 s21, s21, 0
	s_cmp_gt_u32 s50, 13
	s_cbranch_scc0 .LBB0_143
	s_and_b64 vcc, exec, s[10:11]
	s_cbranch_vccz .LBB0_146
	s_barrier

.LBB0_156:
	v_bfe_i32 v4, v2, 27, 1
	v_lshlrev_b32_e32 v3, 4, v2
	v_lshrrev_b32_e32 v4, 22, v4
	v_add_u32_e32 v4, v3, v4
	v_and_b32_e32 v4, 0xfffffc00, v4
	v_sub_u32_e32 v4, v3, v4
	v_ashrrev_i32_e32 v1, 31, v2
	v_lshrrev_b32_e32 v5, 4, v4
	s_and_b64 s[6:7], s[38:39], exec
	v_lshrrev_b32_e32 v1, 26, v1
	v_bitop3_b32 v5, v5, v4, 32 bitop3:0x6c
	v_ashrrev_i32_e32 v4, 31, v4
	s_cselect_b32 s3, 0x600000, 0
	v_add_u32_e32 v1, v2, v1
	v_lshrrev_b32_e32 v4, 26, v4
	s_add_u32 s3, s78, s3
	v_ashrrev_i32_e32 v1, 6, v1
	v_add_u32_e32 v4, v5, v4
	s_addc_u32 s5, s79, 0
	v_lshlrev_b32_e32 v6, 3, v1
	v_ashrrev_i32_e32 v4, 6, v4
	s_add_u32 s24, s3, 0x600000
	v_and_b32_e32 v6, -16, v6
	v_mul_i32_i24_e32 v7, 64, v4
	s_addc_u32 s25, s5, 0
	v_add_u32_e32 v6, v4, v6
	v_sub_u32_e32 v5, v5, v7
	s_add_u32 s26, s0, 0x6200000
	v_lshlrev_b32_e32 v1, 5, v1
	v_ashrrev_i16_sdwa v5, v188, sext(v5) dst_sel:DWORD dst_unused:UNUSED_PAD src0_sel:DWORD src1_sel:BYTE_0
	v_lshlrev_b32_e32 v7, 1, v6
	v_lshrrev_b32_e32 v8, 2, v6
	v_and_b32_e32 v4, 3, v4
	s_mov_b32 s0, 0x1fffe0
	v_and_b32_e32 v1, 32, v1
	v_bfe_i32 v5, v5, 0, 16
	v_and_b32_e32 v7, 24, v7
	v_and_b32_e32 v8, 4, v8
	v_and_or_b32 v4, v6, s0, v4
	v_or3_b32 v4, v4, v8, v7
	v_add_lshl_u32 v5, v1, v5, 1
	v_add_u32_e32 v3, 0x2000, v3
	v_lshl_add_u32 v130, v4, 11, v5
	v_ashrrev_i32_e32 v4, 31, v3
	v_lshrrev_b32_e32 v4, 22, v4
	v_add_u32_e32 v4, v3, v4
	v_ashrrev_i32_e32 v4, 10, v4
	v_lshl_add_u32 v1, v6, 11, v5
	v_mul_i32_i24_e32 v5, 0x400, v4
	v_sub_u32_e32 v3, v3, v5
	v_lshrrev_b32_e32 v5, 4, v3
	v_bitop3_b32 v3, v5, v3, 32 bitop3:0x6c
	v_ashrrev_i32_e32 v6, 31, v3
	v_lshrrev_b32_e32 v6, 26, v6
	v_lshlrev_b32_e32 v5, 3, v4
	v_add_u32_e32 v6, v3, v6
	v_and_b32_e32 v5, -16, v5
	v_ashrrev_i32_e32 v7, 6, v6
	v_add_u32_e32 v5, v7, v5
	v_and_b32_e32 v7, 3, v7
	s_addc_u32 s27, s1, 0
	v_and_or_b32 v7, v5, s0, v7
	s_add_i32 s0, s4, s2
	s_ashr_i32 s1, s0, 31
	s_lshr_b32 s1, s1, 23
	s_add_i32 s1, s0, s1
	v_and_b32_e32 v6, 0xc0, v6
	s_ashr_i32 s2, s1, 9
	v_sub_u32_e32 v3, v3, v6
	s_lshl_b32 s4, s2, 3
	v_lshlrev_b32_e32 v4, 5, v4
	v_ashrrev_i16_sdwa v3, v188, sext(v3) dst_sel:DWORD dst_unused:UNUSED_PAD src0_sel:DWORD src1_sel:BYTE_0
	v_lshlrev_b32_e32 v6, 1, v5
	v_lshrrev_b32_e32 v8, 2, v5
	s_sub_i32 s2, 4, s4
	v_and_b32_e32 v4, 32, v4
	v_bfe_i32 v3, v3, 0, 16
	v_and_b32_e32 v6, 24, v6
	v_and_b32_e32 v8, 4, v8
	s_min_u32 s5, s2, 8
	s_and_b32 s1, s1, 0xfffffe00
	v_or3_b32 v6, v7, v8, v6
	v_add_lshl_u32 v3, v4, v3, 1
	s_sub_i32 s6, s0, s1
	v_cvt_f32_ubyte0_e32 v4, s5
	v_lshl_add_u32 v131, v5, 11, v3
	v_lshl_add_u32 v132, v6, 11, v3
	v_cvt_f32_i32_e32 v3, s6
	v_rcp_iflag_f32_e32 v5, v4
	s_ashr_i32 s3, s8, 6
	s_ashr_i32 s0, s6, 30
	s_ashr_i32 s9, s8, 8
	v_mul_f32_e32 v5, v3, v5
	v_trunc_f32_e32 v5, v5
	v_fma_f32 v3, -v5, v4, v3
	v_cvt_i32_f32_e32 v5, v5
	s_lshl_b32 s28, s3, 10
	s_or_b32 s2, s0, 1
	v_cmp_ge_f32_e64 s[0:1], |v3|, v4
	s_and_b64 s[0:1], s[0:1], exec
	s_cselect_b32 s0, s2, 0
	v_readfirstlane_b32 s1, v5
	s_add_i32 s2, s1, s0
	s_mul_i32 s0, s2, s5
	s_sub_i32 s0, s6, s0
	s_sext_i32_i16 s0, s0
	s_add_i32 s4, s4, s0
	s_bfe_i64 s[0:1], s[2:3], 0x100000
	s_lshl_b32 s6, s4, 8
	s_lshl_b64 s[0:1], s[0:1], 19
	s_add_u32 s16, s26, s0
	s_addc_u32 s17, s27, s1
	s_ashr_i32 s7, s6, 31
	s_lshl_b64 s[0:1], s[6:7], 11
	s_add_i32 s7, s28, 0
	s_add_i32 m0, s7, 0x10000
	s_nop 0
	global_load_lds_dwordx4 v130, s[16:17]
	s_add_i32 m0, s7, 0x12000
	s_add_u32 s4, s16, 0x40000
	global_load_lds_dwordx4 v132, s[16:17]
	s_addc_u32 s5, s17, 0
	s_add_i32 m0, s7, 0x14000
	s_nop 0
	global_load_lds_dwordx4 v130, s[4:5]
	s_add_i32 m0, s7, 0x16000
	s_add_u32 s18, s24, s0
	global_load_lds_dwordx4 v132, s[4:5]
	s_addc_u32 s19, s25, s1
	s_mov_b32 m0, s7
	s_add_i32 s29, s7, 0x2000
	global_load_lds_dwordx4 v1, s[18:19]
	s_mov_b32 m0, s29
	s_add_u32 s0, s18, 0x40000
	global_load_lds_dwordx4 v131, s[18:19]
	s_addc_u32 s1, s19, 0
	s_add_i32 s30, s7, 0x4000
	s_mov_b32 m0, s30
	s_add_i32 s31, s7, 0x6000
	global_load_lds_dwordx4 v1, s[0:1]
	v_mov_b32_e32 v3, v131
	s_mov_b32 m0, s31
	s_cmp_eq_u32 s9, 1
	global_load_lds_dwordx4 v3, s[0:1]
	s_cselect_b64 s[0:1], -1, 0
	s_cmp_lg_u32 s9, 1
	s_cbranch_scc1 .LBB0_158
	s_barrier

.LBB0_168:
	s_add_u32 s18, s16, 0xfffc0080
	s_addc_u32 s19, s17, -1
	s_add_i32 s45, 0, 0x10000
	s_cmp_eq_u32 s44, 12
	s_cselect_b32 s19, s11, s19
	s_cselect_b32 s18, s41, s18
	v_add_u32_e32 v137, s45, v134
	s_cselect_b32 s21, s13, s43
	s_cselect_b32 s20, s12, s42
	s_add_i32 s48, 0, 0x14000
	ds_read_b128 v[138:141], v137
	ds_read_b128 v[142:145], v137 offset:1024
	ds_read_b128 v[146:149], v137 offset:2048
	ds_read_b128 v[150:153], v137 offset:3072
	v_add_u32_e32 v137, s48, v134
	ds_read_b128 v[154:157], v137
	ds_read_b128 v[158:161], v137 offset:1024
	ds_read_b128 v[162:165], v137 offset:2048
	ds_read_b128 v[172:175], v137 offset:3072
	v_mov_b32_e32 v137, v1
	ds_read_b128 v[176:179], v136
	ds_read_b128 v[180:183], v136 offset:1024
	ds_read_b128 v[200:203], v136 offset:2048
	ds_read_b128 v[204:207], v136 offset:3072
	ds_read_b128 v[208:211], v136 offset:4096
	ds_read_b128 v[212:215], v136 offset:5120
	ds_read_b128 v[216:219], v136 offset:6144
	ds_read_b128 v[220:223], v136 offset:7168
	s_add_i32 m0, s7, 0xc000
	s_nop 0
	global_load_lds_dwordx4 v137, s[16:17]
	s_add_i32 m0, s7, 0xe000
	s_nop 0
	global_load_lds_dwordx4 v131, s[16:17]
	s_waitcnt vmcnt(8)
	s_waitcnt lgkmcnt(0)
	s_barrier
	s_setprio 1
	s_waitcnt lgkmcnt(0)
	v_mfma_f32_16x16x32_bf16 v[126:129], v[138:141], v[176:179], v[126:129]
	v_mfma_f32_16x16x32_bf16 v[122:125], v[146:149], v[176:179], v[122:125]
	v_mfma_f32_16x16x32_bf16 v[118:121], v[138:141], v[200:203], v[118:121]
	v_mfma_f32_16x16x32_bf16 v[114:117], v[146:149], v[200:203], v[114:117]
	v_mfma_f32_16x16x32_bf16 v[102:105], v[138:141], v[208:211], v[102:105]
	v_mfma_f32_16x16x32_bf16 v[98:101], v[146:149], v[208:211], v[98:101]
	v_mfma_f32_16x16x32_bf16 v[86:89], v[138:141], v[216:219], v[86:89]
	v_mfma_f32_16x16x32_bf16 v[82:85], v[146:149], v[216:219], v[82:85]
	v_mfma_f32_16x16x32_bf16 v[126:129], v[142:145], v[180:183], v[126:129]
	v_mfma_f32_16x16x32_bf16 v[122:125], v[150:153], v[180:183], v[122:125]
	v_mfma_f32_16x16x32_bf16 v[118:121], v[142:145], v[204:207], v[118:121]
	v_mfma_f32_16x16x32_bf16 v[114:117], v[150:153], v[204:207], v[114:117]
	v_mfma_f32_16x16x32_bf16 v[102:105], v[142:145], v[212:215], v[102:105]
	v_mfma_f32_16x16x32_bf16 v[98:101], v[150:153], v[212:215], v[98:101]
	v_mfma_f32_16x16x32_bf16 v[86:89], v[142:145], v[220:223], v[86:89]
	v_mfma_f32_16x16x32_bf16 v[82:85], v[150:153], v[220:223], v[82:85]
	s_setprio 0
	s_setprio 1
	v_mfma_f32_16x16x32_bf16 v[110:113], v[154:157], v[176:179], v[110:113]
	v_mfma_f32_16x16x32_bf16 v[106:109], v[162:165], v[176:179], v[106:109]
	v_mfma_f32_16x16x32_bf16 v[94:97], v[154:157], v[200:203], v[94:97]
	v_mfma_f32_16x16x32_bf16 v[90:93], v[162:165], v[200:203], v[90:93]
	v_mfma_f32_16x16x32_bf16 v[78:81], v[154:157], v[208:211], v[78:81]
	v_mfma_f32_16x16x32_bf16 v[74:77], v[162:165], v[208:211], v[74:77]
	v_mfma_f32_16x16x32_bf16 v[70:73], v[154:157], v[216:219], v[70:73]
	v_mfma_f32_16x16x32_bf16 v[62:65], v[162:165], v[216:219], v[62:65]
	v_mfma_f32_16x16x32_bf16 v[110:113], v[158:161], v[180:183], v[110:113]
	v_mfma_f32_16x16x32_bf16 v[106:109], v[172:175], v[180:183], v[106:109]
	v_mfma_f32_16x16x32_bf16 v[94:97], v[158:161], v[204:207], v[94:97]
	v_mfma_f32_16x16x32_bf16 v[90:93], v[172:175], v[204:207], v[90:93]
	v_mfma_f32_16x16x32_bf16 v[78:81], v[158:161], v[212:215], v[78:81]
	v_mfma_f32_16x16x32_bf16 v[74:77], v[172:175], v[212:215], v[74:77]
	v_mfma_f32_16x16x32_bf16 v[70:73], v[158:161], v[220:223], v[70:73]
	v_mfma_f32_16x16x32_bf16 v[62:65], v[172:175], v[220:223], v[62:65]
	s_setprio 0
	s_barrier
	v_mov_b32_e32 v137, v130
	s_add_i32 s45, s45, s28
	ds_read_b128 v[176:179], v136 offset:16384
	ds_read_b128 v[180:183], v136 offset:17408
	ds_read_b128 v[200:203], v136 offset:18432
	ds_read_b128 v[204:207], v136 offset:19456
	ds_read_b128 v[208:211], v136 offset:20480
	ds_read_b128 v[212:215], v136 offset:21504
	ds_read_b128 v[216:219], v136 offset:22528
	ds_read_b128 v[220:223], v136 offset:23552
	s_mov_b32 m0, s45
	s_nop 0
	global_load_lds_dwordx4 v137, s[20:21]
	s_add_i32 m0, s45, 0x2000
	s_add_u32 s46, s20, 0x40000
	global_load_lds_dwordx4 v132, s[20:21]
	s_addc_u32 s47, s21, 0
	s_add_i32 s45, s48, s28
	s_mov_b32 m0, s45
	s_nop 0
	global_load_lds_dwordx4 v130, s[46:47]
	s_add_i32 m0, s45, 0x2000
	s_nop 0
	global_load_lds_dwordx4 v132, s[46:47]
	s_mov_b32 m0, s7
	s_nop 0
	global_load_lds_dwordx4 v1, s[18:19]
	v_mov_b32_e32 v137, v131
	s_mov_b32 m0, s29
	s_nop 0
	global_load_lds_dwordx4 v137, s[18:19]
	s_waitcnt vmcnt(8)
	s_waitcnt lgkmcnt(0)
	s_barrier
	s_setprio 1
	s_waitcnt lgkmcnt(0)
	v_mfma_f32_16x16x32_bf16 v[66:69], v[138:141], v[176:179], v[66:69]
	v_mfma_f32_16x16x32_bf16 v[58:61], v[146:149], v[176:179], v[58:61]
	v_mfma_f32_16x16x32_bf16 v[54:57], v[138:141], v[200:203], v[54:57]
	v_mfma_f32_16x16x32_bf16 v[50:53], v[146:149], v[200:203], v[50:53]
	v_mfma_f32_16x16x32_bf16 v[38:41], v[138:141], v[208:211], v[38:41]
	v_mfma_f32_16x16x32_bf16 v[34:37], v[146:149], v[208:211], v[34:37]
	v_mfma_f32_16x16x32_bf16 v[22:25], v[138:141], v[216:219], v[22:25]
	v_mfma_f32_16x16x32_bf16 v[18:21], v[146:149], v[216:219], v[18:21]
	v_mfma_f32_16x16x32_bf16 v[66:69], v[142:145], v[180:183], v[66:69]
	v_mfma_f32_16x16x32_bf16 v[58:61], v[150:153], v[180:183], v[58:61]
	v_mfma_f32_16x16x32_bf16 v[54:57], v[142:145], v[204:207], v[54:57]
	v_mfma_f32_16x16x32_bf16 v[50:53], v[150:153], v[204:207], v[50:53]
	v_mfma_f32_16x16x32_bf16 v[38:41], v[142:145], v[212:215], v[38:41]
	v_mfma_f32_16x16x32_bf16 v[34:37], v[150:153], v[212:215], v[34:37]
	v_mfma_f32_16x16x32_bf16 v[22:25], v[142:145], v[220:223], v[22:25]
	v_mfma_f32_16x16x32_bf16 v[18:21], v[150:153], v[220:223], v[18:21]
	s_setprio 0
	s_setprio 1
	v_mfma_f32_16x16x32_bf16 v[46:49], v[154:157], v[176:179], v[46:49]
	v_mfma_f32_16x16x32_bf16 v[42:45], v[162:165], v[176:179], v[42:45]
	v_mfma_f32_16x16x32_bf16 v[30:33], v[154:157], v[200:203], v[30:33]
	v_mfma_f32_16x16x32_bf16 v[26:29], v[162:165], v[200:203], v[26:29]
	v_mfma_f32_16x16x32_bf16 v[14:17], v[154:157], v[208:211], v[14:17]
	v_mfma_f32_16x16x32_bf16 v[10:13], v[162:165], v[208:211], v[10:13]
	v_mfma_f32_16x16x32_bf16 v[6:9], v[154:157], v[216:219], v[6:9]
	v_mfma_f32_16x16x32_bf16 v[2:5], v[162:165], v[216:219], v[2:5]
	v_mfma_f32_16x16x32_bf16 v[46:49], v[158:161], v[180:183], v[46:49]
	v_mfma_f32_16x16x32_bf16 v[42:45], v[172:175], v[180:183], v[42:45]
	v_mfma_f32_16x16x32_bf16 v[30:33], v[158:161], v[204:207], v[30:33]
	v_mfma_f32_16x16x32_bf16 v[26:29], v[172:175], v[204:207], v[26:29]
	v_mfma_f32_16x16x32_bf16 v[14:17], v[158:161], v[212:215], v[14:17]
	v_mfma_f32_16x16x32_bf16 v[10:13], v[172:175], v[212:215], v[10:13]
	v_mfma_f32_16x16x32_bf16 v[6:9], v[158:161], v[220:223], v[6:9]
	v_mfma_f32_16x16x32_bf16 v[2:5], v[172:175], v[220:223], v[2:5]
	s_setprio 0
	s_barrier
	s_add_i32 s45, 0, 0x18000
	v_add_u32_e32 v137, s45, v134
	s_add_i32 s48, 0, 0x1c000
	ds_read_b128 v[138:141], v137
	ds_read_b128 v[142:145], v137 offset:1024
	ds_read_b128 v[146:149], v137 offset:2048
	ds_read_b128 v[150:153], v137 offset:3072
	v_add_u32_e32 v137, s48, v134
	ds_read_b128 v[154:157], v137
	ds_read_b128 v[158:161], v137 offset:1024
	ds_read_b128 v[162:165], v137 offset:2048
	ds_read_b128 v[172:175], v137 offset:3072
	s_add_u32 s46, s18, 0x40000
	v_mov_b32_e32 v137, v1
	s_mov_b32 m0, s30
	ds_read_b128 v[176:179], v136 offset:32768
	ds_read_b128 v[180:183], v136 offset:33792
	ds_read_b128 v[200:203], v136 offset:34816
	ds_read_b128 v[204:207], v136 offset:35840
	ds_read_b128 v[208:211], v136 offset:36864
	ds_read_b128 v[212:215], v136 offset:37888
	ds_read_b128 v[216:219], v136 offset:38912
	ds_read_b128 v[220:223], v136 offset:39936
	s_addc_u32 s47, s19, 0
	s_nop 0
	global_load_lds_dwordx4 v137, s[46:47]
	s_mov_b32 m0, s31
	s_nop 0
	global_load_lds_dwordx4 v131, s[46:47]
	s_waitcnt vmcnt(8)
	s_waitcnt lgkmcnt(0)
	s_barrier
	s_setprio 1
	s_waitcnt lgkmcnt(0)
	v_mfma_f32_16x16x32_bf16 v[126:129], v[138:141], v[176:179], v[126:129]
	v_mfma_f32_16x16x32_bf16 v[122:125], v[146:149], v[176:179], v[122:125]
	v_mfma_f32_16x16x32_bf16 v[118:121], v[138:141], v[200:203], v[118:121]
	v_mfma_f32_16x16x32_bf16 v[114:117], v[146:149], v[200:203], v[114:117]
	v_mfma_f32_16x16x32_bf16 v[102:105], v[138:141], v[208:211], v[102:105]
	v_mfma_f32_16x16x32_bf16 v[98:101], v[146:149], v[208:211], v[98:101]
	v_mfma_f32_16x16x32_bf16 v[86:89], v[138:141], v[216:219], v[86:89]
	v_mfma_f32_16x16x32_bf16 v[82:85], v[146:149], v[216:219], v[82:85]
	v_mfma_f32_16x16x32_bf16 v[126:129], v[142:145], v[180:183], v[126:129]
	v_mfma_f32_16x16x32_bf16 v[122:125], v[150:153], v[180:183], v[122:125]
	v_mfma_f32_16x16x32_bf16 v[118:121], v[142:145], v[204:207], v[118:121]
	v_mfma_f32_16x16x32_bf16 v[114:117], v[150:153], v[204:207], v[114:117]
	v_mfma_f32_16x16x32_bf16 v[102:105], v[142:145], v[212:215], v[102:105]
	v_mfma_f32_16x16x32_bf16 v[98:101], v[150:153], v[212:215], v[98:101]
	v_mfma_f32_16x16x32_bf16 v[86:89], v[142:145], v[220:223], v[86:89]
	v_mfma_f32_16x16x32_bf16 v[82:85], v[150:153], v[220:223], v[82:85]
	s_setprio 0
	s_setprio 1
	v_mfma_f32_16x16x32_bf16 v[110:113], v[154:157], v[176:179], v[110:113]
	v_mfma_f32_16x16x32_bf16 v[106:109], v[162:165], v[176:179], v[106:109]
	v_mfma_f32_16x16x32_bf16 v[94:97], v[154:157], v[200:203], v[94:97]
	v_mfma_f32_16x16x32_bf16 v[90:93], v[162:165], v[200:203], v[90:93]
	v_mfma_f32_16x16x32_bf16 v[78:81], v[154:157], v[208:211], v[78:81]
	v_mfma_f32_16x16x32_bf16 v[74:77], v[162:165], v[208:211], v[74:77]
	v_mfma_f32_16x16x32_bf16 v[70:73], v[154:157], v[216:219], v[70:73]
	v_mfma_f32_16x16x32_bf16 v[62:65], v[162:165], v[216:219], v[62:65]
	v_mfma_f32_16x16x32_bf16 v[110:113], v[158:161], v[180:183], v[110:113]
	v_mfma_f32_16x16x32_bf16 v[106:109], v[172:175], v[180:183], v[106:109]
	v_mfma_f32_16x16x32_bf16 v[94:97], v[158:161], v[204:207], v[94:97]
	v_mfma_f32_16x16x32_bf16 v[90:93], v[172:175], v[204:207], v[90:93]
	v_mfma_f32_16x16x32_bf16 v[78:81], v[158:161], v[212:215], v[78:81]
	v_mfma_f32_16x16x32_bf16 v[74:77], v[172:175], v[212:215], v[74:77]
	v_mfma_f32_16x16x32_bf16 v[70:73], v[158:161], v[220:223], v[70:73]
	v_mfma_f32_16x16x32_bf16 v[62:65], v[172:175], v[220:223], v[62:65]
	s_setprio 0
	s_barrier
	v_mov_b32_e32 v166, v130
	ds_read_b128 v[176:179], v136 offset:49152
	ds_read_b128 v[180:183], v136 offset:50176
	ds_read_b128 v[200:203], v136 offset:51200
	ds_read_b128 v[204:207], v136 offset:52224
	ds_read_b128 v[208:211], v136 offset:53248
	ds_read_b128 v[212:215], v136 offset:54272
	ds_read_b128 v[216:219], v136 offset:55296
	ds_read_b128 v[220:223], v136 offset:56320
	s_add_i32 s45, s45, s28
	v_lshl_add_u64 v[184:185], s[20:21], 0, v[166:167]
	v_lshl_add_u64 v[184:185], v[184:185], 0, s[80:81]
	s_mov_b32 m0, s45
	v_mov_b32_e32 v166, v132
	global_load_lds_dwordx4 v[184:185], off
	s_add_i32 m0, s45, 0x2000
	v_mov_b32_e32 v137, v130
	v_lshl_add_u64 v[184:185], s[20:21], 0, v[166:167]
	s_add_u32 s20, s20, 0x40080
	v_lshl_add_u64 v[184:185], v[184:185], 0, s[80:81]
	s_addc_u32 s21, s21, 0
	s_add_i32 s45, s48, s28
	global_load_lds_dwordx4 v[184:185], off
	s_mov_b32 m0, s45
	v_mov_b32_e32 v166, v1
	global_load_lds_dwordx4 v137, s[20:21]
	v_mov_b32_e32 v137, v132
	s_add_i32 m0, s45, 0x2000
	s_nop 0
	global_load_lds_dwordx4 v137, s[20:21]
	s_mov_b32 m0, s34
	v_lshl_add_u64 v[184:185], s[18:19], 0, v[166:167]
	v_lshl_add_u64 v[184:185], v[184:185], 0, s[80:81]
	v_mov_b32_e32 v166, v131
	global_load_lds_dwordx4 v[184:185], off
	s_mov_b32 m0, s35
	v_lshl_add_u64 v[184:185], s[18:19], 0, v[166:167]
	v_lshl_add_u64 v[184:185], v[184:185], 0, s[80:81]
	global_load_lds_dwordx4 v[184:185], off
	s_waitcnt vmcnt(8)
	s_waitcnt lgkmcnt(0)
	s_barrier
	s_setprio 1
	s_waitcnt lgkmcnt(0)
	v_mfma_f32_16x16x32_bf16 v[66:69], v[138:141], v[176:179], v[66:69]
	v_mfma_f32_16x16x32_bf16 v[58:61], v[146:149], v[176:179], v[58:61]
	v_mfma_f32_16x16x32_bf16 v[54:57], v[138:141], v[200:203], v[54:57]
	v_mfma_f32_16x16x32_bf16 v[50:53], v[146:149], v[200:203], v[50:53]
	v_mfma_f32_16x16x32_bf16 v[38:41], v[138:141], v[208:211], v[38:41]
	v_mfma_f32_16x16x32_bf16 v[34:37], v[146:149], v[208:211], v[34:37]
	v_mfma_f32_16x16x32_bf16 v[22:25], v[138:141], v[216:219], v[22:25]
	v_mfma_f32_16x16x32_bf16 v[18:21], v[146:149], v[216:219], v[18:21]
	v_mfma_f32_16x16x32_bf16 v[66:69], v[142:145], v[180:183], v[66:69]
	v_mfma_f32_16x16x32_bf16 v[58:61], v[150:153], v[180:183], v[58:61]
	v_mfma_f32_16x16x32_bf16 v[54:57], v[142:145], v[204:207], v[54:57]
	v_mfma_f32_16x16x32_bf16 v[50:53], v[150:153], v[204:207], v[50:53]
	v_mfma_f32_16x16x32_bf16 v[38:41], v[142:145], v[212:215], v[38:41]
	v_mfma_f32_16x16x32_bf16 v[34:37], v[150:153], v[212:215], v[34:37]
	v_mfma_f32_16x16x32_bf16 v[22:25], v[142:145], v[220:223], v[22:25]
	v_mfma_f32_16x16x32_bf16 v[18:21], v[150:153], v[220:223], v[18:21]
	s_setprio 0
	s_setprio 1
	v_mfma_f32_16x16x32_bf16 v[46:49], v[154:157], v[176:179], v[46:49]
	v_mfma_f32_16x16x32_bf16 v[42:45], v[162:165], v[176:179], v[42:45]
	v_mfma_f32_16x16x32_bf16 v[30:33], v[154:157], v[200:203], v[30:33]
	v_mfma_f32_16x16x32_bf16 v[26:29], v[162:165], v[200:203], v[26:29]
	v_mfma_f32_16x16x32_bf16 v[14:17], v[154:157], v[208:211], v[14:17]
	v_mfma_f32_16x16x32_bf16 v[10:13], v[162:165], v[208:211], v[10:13]
	v_mfma_f32_16x16x32_bf16 v[6:9], v[154:157], v[216:219], v[6:9]
	v_mfma_f32_16x16x32_bf16 v[2:5], v[162:165], v[216:219], v[2:5]
	v_mfma_f32_16x16x32_bf16 v[46:49], v[158:161], v[180:183], v[46:49]
	v_mfma_f32_16x16x32_bf16 v[42:45], v[172:175], v[180:183], v[42:45]
	v_mfma_f32_16x16x32_bf16 v[30:33], v[158:161], v[204:207], v[30:33]
	v_mfma_f32_16x16x32_bf16 v[26:29], v[172:175], v[204:207], v[26:29]
	v_mfma_f32_16x16x32_bf16 v[14:17], v[158:161], v[212:215], v[14:17]
	v_mfma_f32_16x16x32_bf16 v[10:13], v[172:175], v[212:215], v[10:13]
	v_mfma_f32_16x16x32_bf16 v[6:9], v[158:161], v[220:223], v[6:9]
	v_mfma_f32_16x16x32_bf16 v[2:5], v[172:175], v[220:223], v[2:5]
	s_setprio 0
	s_barrier
	s_add_i32 s44, s44, 2
	s_add_u32 s42, s42, 0x100
	s_addc_u32 s43, s43, 0
	s_add_u32 s16, s16, 0x100
	s_addc_u32 s17, s17, 0
	s_cmp_gt_u32 s44, 13
	s_cbranch_scc0 .LBB0_168
	s_and_b64 vcc, exec, s[8:9]
	s_cbranch_vccz .LBB0_171
	s_barrier

.LBB0_390:
	s_cmp_eq_u32 s36, 1
	s_cselect_b64 s[0:1], -1, 0
	s_and_b64 s[2:3], s[0:1], exec
	s_cselect_b32 s6, 0x400, s69
	s_cmp_eq_u32 s36, 0
	s_cselect_b64 s[2:3], -1, 0
	s_and_b64 s[4:5], s[2:3], exec
	s_cselect_b32 s37, 0x600, s6
	s_lshr_b32 s8, s37, 8
	s_cmp_eq_u32 s36, 2
	s_cselect_b64 s[4:5], -1, 0
	s_and_b64 s[6:7], s[4:5], exec
	s_cselect_b32 s6, 2, 6
	s_lshl_b32 s84, s8, s6
	s_mov_b32 s40, s83
	s_waitcnt lgkmcnt(0)
	v_mov_b32_e32 v2, v0
	s_cmp_ge_i32 s40, s84
	v_readfirstlane_b32 s10, v2
	s_cbranch_scc1 .LBB0_389
	v_bfe_i32 v4, v2, 27, 1
	v_lshlrev_b32_e32 v3, 4, v2
	v_lshrrev_b32_e32 v4, 22, v4
	v_add_u32_e32 v4, v3, v4
	v_and_b32_e32 v4, 0xfffffc00, v4
	v_sub_u32_e32 v4, v3, v4
	v_ashrrev_i32_e32 v1, 31, v2
	v_lshrrev_b32_e32 v5, 4, v4
	v_lshrrev_b32_e32 v1, 26, v1
	v_bitop3_b32 v5, v5, v4, 32 bitop3:0x6c
	v_ashrrev_i32_e32 v4, 31, v4
	s_and_b64 s[6:7], s[0:1], exec
	v_add_u32_e32 v1, v2, v1
	v_lshrrev_b32_e32 v4, 26, v4
	s_cselect_b32 s8, s26, s34
	s_cselect_b32 s9, s27, s35
	s_and_b64 s[6:7], s[2:3], exec
	v_ashrrev_i32_e32 v1, 6, v1
	v_add_u32_e32 v4, v5, v4
	s_cselect_b32 s41, s25, s9
	s_cselect_b32 s42, s24, s8
	s_and_b64 s[6:7], s[0:1], exec
	v_lshlrev_b32_e32 v6, 3, v1
	v_ashrrev_i32_e32 v4, 6, v4
	s_cselect_b32 s8, s30, s26
	s_cselect_b32 s9, s31, s27
	s_and_b64 s[6:7], s[2:3], exec
	v_and_b32_e32 v6, -16, v6
	v_mul_i32_i24_e32 v7, 64, v4
	s_cselect_b32 s43, s29, s9
	s_cselect_b32 s44, s28, s8
	s_and_b64 s[4:5], s[4:5], exec
	v_add_u32_e32 v6, v4, v6
	v_sub_u32_e32 v5, v5, v7
	s_cselect_b32 s45, 4, 64
	s_and_b64 s[4:5], s[2:3], exec
	v_lshlrev_b32_e32 v1, 5, v1
	v_ashrrev_i16_sdwa v5, v188, sext(v5) dst_sel:DWORD dst_unused:UNUSED_PAD src0_sel:DWORD src1_sel:BYTE_0
	v_lshlrev_b32_e32 v7, 1, v6
	v_lshrrev_b32_e32 v8, 2, v6
	v_and_b32_e32 v4, 3, v4
	s_mov_b32 s6, 0xffffe0
	s_movk_i32 s4, 0x200
	v_and_b32_e32 v1, 32, v1
	v_bfe_i32 v5, v5, 0, 16
	v_and_b32_e32 v7, 24, v7
	v_and_b32_e32 v8, 4, v8
	v_and_or_b32 v4, v6, s6, v4
	s_cselect_b32 s46, 0x300, s4
	v_or3_b32 v7, v4, v8, v7
	v_add_lshl_u32 v4, v1, v5, 1
	v_add_u32_e32 v3, 0x2000, v3
	v_mad_u64_u32 v[130:131], s[4:5], v6, s46, v[4:5]
	v_mad_u32_u24 v1, v7, s46, v4
	v_ashrrev_i32_e32 v4, 31, v3
	v_lshrrev_b32_e32 v4, 22, v4
	v_add_u32_e32 v4, v3, v4
	v_ashrrev_i32_e32 v4, 10, v4
	v_mul_i32_i24_e32 v5, 0x400, v4
	v_sub_u32_e32 v3, v3, v5
	v_lshrrev_b32_e32 v5, 4, v3
	v_bitop3_b32 v3, v5, v3, 32 bitop3:0x6c
	v_ashrrev_i32_e32 v6, 31, v3
	v_lshrrev_b32_e32 v6, 26, v6
	v_lshlrev_b32_e32 v5, 3, v4
	v_add_u32_e32 v6, v3, v6
	s_ashr_i32 s50, s40, 31
	v_and_b32_e32 v5, -16, v5
	v_ashrrev_i32_e32 v7, 6, v6
	s_lshr_b32 s4, s50, 29
	v_add_u32_e32 v5, v7, v5
	v_and_b32_e32 v7, 3, v7
	s_add_i32 s4, s40, s4
	s_ashr_i32 s11, s10, 6
	v_and_or_b32 v7, v5, s6, v7
	s_lshr_b32 s49, s84, 3
	s_ashr_i32 s6, s4, 3
	s_and_b32 s4, s4, -8
	v_and_b32_e32 v6, 0xc0, v6
	s_ashr_i32 s12, s10, 8
	s_lshl_b32 s47, s46, 7
	s_lshl_b32 s48, s11, 10
	s_sub_i32 s7, s40, s4
	s_add_i32 s51, s49, 1
	v_sub_u32_e32 v3, v3, v6
	s_cmp_lt_i32 s7, 0
	v_lshlrev_b32_e32 v4, 5, v4
	v_ashrrev_i16_sdwa v3, v188, sext(v3) dst_sel:DWORD dst_unused:UNUSED_PAD src0_sel:DWORD src1_sel:BYTE_0
	s_cselect_b32 s8, s51, s49
	s_lshr_b32 s52, s37, 5
	v_and_b32_e32 v4, 32, v4
	v_bfe_i32 v3, v3, 0, 16
	s_abs_i32 s53, s52
	v_add_lshl_u32 v4, v4, v3, 1
	v_cvt_f32_u32_e32 v3, s53
	v_mad_u64_u32 v[132:133], s[4:5], v5, s46, v[4:5]
	s_mul_i32 s4, s7, s8
	v_rcp_iflag_f32_e32 v3, v3
	s_sub_i32 s7, 0, s53
	s_add_i32 s4, s4, s6
	s_abs_i32 s6, s4
	v_mul_f32_e32 v3, 0x4f7ffffe, v3
	v_cvt_u32_f32_e32 v3, v3
	s_ashr_i32 s5, s4, 31
	s_ashr_i32 s54, s52, 31
	s_xor_b32 s5, s5, s54
	v_readfirstlane_b32 s55, v3
	s_mul_i32 s7, s7, s55
	s_mul_hi_u32 s7, s55, s7
	s_add_i32 s55, s55, s7
	s_mul_hi_u32 s7, s6, s55
	s_mul_i32 s8, s7, s53
	s_sub_i32 s6, s6, s8
	s_add_i32 s8, s7, 1
	s_sub_i32 s9, s6, s53
	s_cmp_ge_u32 s6, s53
	s_cselect_b32 s7, s8, s7
	s_cselect_b32 s6, s9, s6
	s_add_i32 s8, s7, 1
	s_cmp_ge_u32 s6, s53
	s_cselect_b32 s6, s8, s7
	s_xor_b32 s6, s6, s5
	s_sub_i32 s5, s6, s5
	s_lshl_b32 s7, s5, 3
	s_sub_i32 s6, s45, s7
	s_min_i32 s8, s6, 8
	s_sext_i32_i16 s6, s8
	v_cvt_f32_i32_e32 v3, s6
	v_lshlrev_b32_e32 v6, 1, v5
	v_lshrrev_b32_e32 v8, 2, v5
	v_and_b32_e32 v6, 24, v6
	v_and_b32_e32 v8, 4, v8
	s_mul_i32 s5, s5, s52
	v_or3_b32 v6, v7, v8, v6
	s_sub_i32 s9, s4, s5
	v_mad_u32_u24 v131, v6, s46, v4
	v_cvt_f32_i32_e32 v4, s9
	v_rcp_iflag_f32_e32 v5, v3
	s_xor_b32 s4, s9, s6
	s_ashr_i32 s4, s4, 30
	s_or_b32 s6, s4, 1
	v_mul_f32_e32 v5, v4, v5
	v_trunc_f32_e32 v5, v5
	v_fma_f32 v4, -v5, v3, v4
	v_cvt_i32_f32_e32 v5, v5
	v_cmp_ge_f32_e64 s[4:5], |v4|, |v3|
	s_and_b64 s[4:5], s[4:5], exec
	s_cselect_b32 s4, s6, 0
	v_readfirstlane_b32 s5, v5
	s_add_i32 s6, s5, s4
	s_mul_i32 s4, s6, s8
	s_sub_i32 s4, s9, s4
	s_sext_i32_i16 s4, s4
	s_add_i32 s7, s7, s4
	s_bfe_i64 s[4:5], s[6:7], 0x100000
	s_lshl_b32 s56, s46, 8
	s_lshl_b32 s65, s7, 8
	s_mul_hi_i32 s5, s56, s4
	s_mul_i32 s4, s56, s4
	s_add_u32 s16, s44, s4
	s_addc_u32 s17, s43, s5
	s_add_i32 s57, s48, 0
	v_mov_b32_e32 v3, v1
	s_add_i32 m0, s57, 0x10000
	s_mul_i32 s5, s65, s46
	global_load_lds_dwordx4 v3, s[16:17]
	s_add_i32 m0, s57, 0x12000
	s_add_u32 s8, s16, s47
	global_load_lds_dwordx4 v131, s[16:17]
	v_mov_b32_e32 v3, v1
	s_addc_u32 s9, s17, 0
	s_add_i32 m0, s57, 0x14000
	s_mul_hi_i32 s4, s65, s46
	global_load_lds_dwordx4 v3, s[8:9]
	s_add_i32 m0, s57, 0x16000
	s_add_u32 s14, s42, s5
	global_load_lds_dwordx4 v131, s[8:9]
	s_addc_u32 s15, s41, s4
	s_mov_b32 m0, s57
	s_add_i32 s58, s57, 0x2000
	global_load_lds_dwordx4 v130, s[14:15]
	s_mov_b32 m0, s58
	s_add_u32 s4, s14, s47
	global_load_lds_dwordx4 v132, s[14:15]
	s_addc_u32 s5, s15, 0
	s_add_i32 s59, s57, 0x4000
	s_mov_b32 m0, s59
	s_add_i32 s60, s57, 0x6000
	global_load_lds_dwordx4 v130, s[4:5]
	v_mov_b32_e32 v3, v132
	s_mov_b32 m0, s60
	s_cmp_eq_u32 s12, 1
	global_load_lds_dwordx4 v3, s[4:5]
	s_cselect_b64 s[4:5], -1, 0
	s_cmp_lg_u32 s12, 1
	s_cbranch_scc1 .LBB0_393
	s_barrier

.LBB0_401:
	s_add_i32 s74, s18, 2
	s_add_u32 s16, s14, 0x100
	s_addc_u32 s17, s15, 0
	s_add_i32 s75, 0, 0x10000
	s_cmp_eq_u32 s66, s18
	s_cselect_b32 s19, s1, s17
	s_cselect_b32 s18, s0, s16
	v_add_u32_e32 v137, s75, v134
	s_cselect_b32 s21, s13, s73
	s_cselect_b32 s20, s12, s72
	s_add_i32 s76, 0, 0x14000
	ds_read_b128 v[138:141], v137
	ds_read_b128 v[142:145], v137 offset:1024
	ds_read_b128 v[146:149], v137 offset:2048
	ds_read_b128 v[150:153], v137 offset:3072
	v_add_u32_e32 v137, s76, v134
	ds_read_b128 v[154:157], v137
	ds_read_b128 v[158:161], v137 offset:1024
	ds_read_b128 v[162:165], v137 offset:2048
	ds_read_b128 v[172:175], v137 offset:3072
	v_mov_b32_e32 v137, v130
	s_add_u32 s14, s14, s68
	ds_read_b128 v[176:179], v136
	ds_read_b128 v[180:183], v136 offset:1024
	ds_read_b128 v[200:203], v136 offset:2048
	ds_read_b128 v[204:207], v136 offset:3072
	ds_read_b128 v[208:211], v136 offset:4096
	ds_read_b128 v[212:215], v136 offset:5120
	ds_read_b128 v[216:219], v136 offset:6144
	ds_read_b128 v[220:223], v136 offset:7168
	s_addc_u32 s15, s15, s69
	s_add_i32 m0, s57, 0xc000
	s_nop 0
	global_load_lds_dwordx4 v137, s[14:15]
	s_add_i32 m0, s57, 0xe000
	s_nop 0
	global_load_lds_dwordx4 v132, s[14:15]
	s_waitcnt vmcnt(8)
	s_waitcnt lgkmcnt(0)
	s_barrier
	s_setprio 1
	s_waitcnt lgkmcnt(0)
	v_mfma_f32_16x16x32_bf16 v[126:129], v[138:141], v[176:179], v[126:129]
	v_mfma_f32_16x16x32_bf16 v[122:125], v[146:149], v[176:179], v[122:125]
	v_mfma_f32_16x16x32_bf16 v[118:121], v[138:141], v[200:203], v[118:121]
	v_mfma_f32_16x16x32_bf16 v[114:117], v[146:149], v[200:203], v[114:117]
	v_mfma_f32_16x16x32_bf16 v[102:105], v[138:141], v[208:211], v[102:105]
	v_mfma_f32_16x16x32_bf16 v[98:101], v[146:149], v[208:211], v[98:101]
	v_mfma_f32_16x16x32_bf16 v[86:89], v[138:141], v[216:219], v[86:89]
	v_mfma_f32_16x16x32_bf16 v[82:85], v[146:149], v[216:219], v[82:85]
	v_mfma_f32_16x16x32_bf16 v[126:129], v[142:145], v[180:183], v[126:129]
	v_mfma_f32_16x16x32_bf16 v[122:125], v[150:153], v[180:183], v[122:125]
	v_mfma_f32_16x16x32_bf16 v[118:121], v[142:145], v[204:207], v[118:121]
	v_mfma_f32_16x16x32_bf16 v[114:117], v[150:153], v[204:207], v[114:117]
	v_mfma_f32_16x16x32_bf16 v[102:105], v[142:145], v[212:215], v[102:105]
	v_mfma_f32_16x16x32_bf16 v[98:101], v[150:153], v[212:215], v[98:101]
	v_mfma_f32_16x16x32_bf16 v[86:89], v[142:145], v[220:223], v[86:89]
	v_mfma_f32_16x16x32_bf16 v[82:85], v[150:153], v[220:223], v[82:85]
	s_setprio 0
	s_setprio 1
	v_mfma_f32_16x16x32_bf16 v[110:113], v[154:157], v[176:179], v[110:113]
	v_mfma_f32_16x16x32_bf16 v[106:109], v[162:165], v[176:179], v[106:109]
	v_mfma_f32_16x16x32_bf16 v[94:97], v[154:157], v[200:203], v[94:97]
	v_mfma_f32_16x16x32_bf16 v[90:93], v[162:165], v[200:203], v[90:93]
	v_mfma_f32_16x16x32_bf16 v[78:81], v[154:157], v[208:211], v[78:81]
	v_mfma_f32_16x16x32_bf16 v[74:77], v[162:165], v[208:211], v[74:77]
	v_mfma_f32_16x16x32_bf16 v[70:73], v[154:157], v[216:219], v[70:73]
	v_mfma_f32_16x16x32_bf16 v[62:65], v[162:165], v[216:219], v[62:65]
	v_mfma_f32_16x16x32_bf16 v[110:113], v[158:161], v[180:183], v[110:113]
	v_mfma_f32_16x16x32_bf16 v[106:109], v[172:175], v[180:183], v[106:109]
	v_mfma_f32_16x16x32_bf16 v[94:97], v[158:161], v[204:207], v[94:97]
	v_mfma_f32_16x16x32_bf16 v[90:93], v[172:175], v[204:207], v[90:93]
	v_mfma_f32_16x16x32_bf16 v[78:81], v[158:161], v[212:215], v[78:81]
	v_mfma_f32_16x16x32_bf16 v[74:77], v[172:175], v[212:215], v[74:77]
	v_mfma_f32_16x16x32_bf16 v[70:73], v[158:161], v[220:223], v[70:73]
	v_mfma_f32_16x16x32_bf16 v[62:65], v[172:175], v[220:223], v[62:65]
	s_setprio 0
	s_barrier
	v_mov_b32_e32 v137, v1
	s_add_i32 s14, s75, s48
	ds_read_b128 v[176:179], v136 offset:16384
	ds_read_b128 v[180:183], v136 offset:17408
	ds_read_b128 v[200:203], v136 offset:18432
	ds_read_b128 v[204:207], v136 offset:19456
	ds_read_b128 v[208:211], v136 offset:20480
	ds_read_b128 v[212:215], v136 offset:21504
	ds_read_b128 v[216:219], v136 offset:22528
	ds_read_b128 v[220:223], v136 offset:23552
	s_mov_b32 m0, s14
	s_nop 0
	global_load_lds_dwordx4 v137, s[20:21]
	s_add_i32 m0, s14, 0x2000
	s_add_u32 s14, s20, s47
	global_load_lds_dwordx4 v131, s[20:21]
	s_addc_u32 s15, s21, 0
	s_add_i32 s75, s76, s48
	s_mov_b32 m0, s75
	s_nop 0
	global_load_lds_dwordx4 v1, s[14:15]
	s_add_i32 m0, s75, 0x2000
	s_nop 0
	global_load_lds_dwordx4 v131, s[14:15]
	s_mov_b32 m0, s57
	s_nop 0
	global_load_lds_dwordx4 v130, s[18:19]
	v_mov_b32_e32 v137, v132
	s_mov_b32 m0, s58
	s_nop 0
	global_load_lds_dwordx4 v137, s[18:19]
	s_waitcnt vmcnt(8)
	s_waitcnt lgkmcnt(0)
	s_barrier
	s_setprio 1
	s_waitcnt lgkmcnt(0)
	v_mfma_f32_16x16x32_bf16 v[66:69], v[138:141], v[176:179], v[66:69]
	v_mfma_f32_16x16x32_bf16 v[58:61], v[146:149], v[176:179], v[58:61]
	v_mfma_f32_16x16x32_bf16 v[54:57], v[138:141], v[200:203], v[54:57]
	v_mfma_f32_16x16x32_bf16 v[50:53], v[146:149], v[200:203], v[50:53]
	v_mfma_f32_16x16x32_bf16 v[38:41], v[138:141], v[208:211], v[38:41]
	v_mfma_f32_16x16x32_bf16 v[34:37], v[146:149], v[208:211], v[34:37]
	v_mfma_f32_16x16x32_bf16 v[22:25], v[138:141], v[216:219], v[22:25]
	v_mfma_f32_16x16x32_bf16 v[18:21], v[146:149], v[216:219], v[18:21]
	v_mfma_f32_16x16x32_bf16 v[66:69], v[142:145], v[180:183], v[66:69]
	v_mfma_f32_16x16x32_bf16 v[58:61], v[150:153], v[180:183], v[58:61]
	v_mfma_f32_16x16x32_bf16 v[54:57], v[142:145], v[204:207], v[54:57]
	v_mfma_f32_16x16x32_bf16 v[50:53], v[150:153], v[204:207], v[50:53]
	v_mfma_f32_16x16x32_bf16 v[38:41], v[142:145], v[212:215], v[38:41]
	v_mfma_f32_16x16x32_bf16 v[34:37], v[150:153], v[212:215], v[34:37]
	v_mfma_f32_16x16x32_bf16 v[22:25], v[142:145], v[220:223], v[22:25]
	v_mfma_f32_16x16x32_bf16 v[18:21], v[150:153], v[220:223], v[18:21]
	s_setprio 0
	s_setprio 1
	v_mfma_f32_16x16x32_bf16 v[46:49], v[154:157], v[176:179], v[46:49]
	v_mfma_f32_16x16x32_bf16 v[42:45], v[162:165], v[176:179], v[42:45]
	v_mfma_f32_16x16x32_bf16 v[30:33], v[154:157], v[200:203], v[30:33]
	v_mfma_f32_16x16x32_bf16 v[26:29], v[162:165], v[200:203], v[26:29]
	v_mfma_f32_16x16x32_bf16 v[14:17], v[154:157], v[208:211], v[14:17]
	v_mfma_f32_16x16x32_bf16 v[10:13], v[162:165], v[208:211], v[10:13]
	v_mfma_f32_16x16x32_bf16 v[6:9], v[154:157], v[216:219], v[6:9]
	v_mfma_f32_16x16x32_bf16 v[2:5], v[162:165], v[216:219], v[2:5]
	v_mfma_f32_16x16x32_bf16 v[46:49], v[158:161], v[180:183], v[46:49]
	v_mfma_f32_16x16x32_bf16 v[42:45], v[172:175], v[180:183], v[42:45]
	v_mfma_f32_16x16x32_bf16 v[30:33], v[158:161], v[204:207], v[30:33]
	v_mfma_f32_16x16x32_bf16 v[26:29], v[172:175], v[204:207], v[26:29]
	v_mfma_f32_16x16x32_bf16 v[14:17], v[158:161], v[212:215], v[14:17]
	v_mfma_f32_16x16x32_bf16 v[10:13], v[172:175], v[212:215], v[10:13]
	v_mfma_f32_16x16x32_bf16 v[6:9], v[158:161], v[220:223], v[6:9]
	v_mfma_f32_16x16x32_bf16 v[2:5], v[172:175], v[220:223], v[2:5]
	s_setprio 0
	s_barrier
	s_add_i32 s75, 0, 0x18000
	v_add_u32_e32 v137, s75, v134
	s_add_i32 s82, 0, 0x1c000
	ds_read_b128 v[138:141], v137
	ds_read_b128 v[142:145], v137 offset:1024
	ds_read_b128 v[146:149], v137 offset:2048
	ds_read_b128 v[150:153], v137 offset:3072
	v_add_u32_e32 v137, s82, v134
	ds_read_b128 v[154:157], v137
	ds_read_b128 v[158:161], v137 offset:1024
	ds_read_b128 v[162:165], v137 offset:2048
	ds_read_b128 v[172:175], v137 offset:3072
	s_add_u32 s76, s18, s47
	v_mov_b32_e32 v137, v130
	s_mov_b32 m0, s59
	ds_read_b128 v[176:179], v136 offset:32768
	ds_read_b128 v[180:183], v136 offset:33792
	ds_read_b128 v[200:203], v136 offset:34816
	ds_read_b128 v[204:207], v136 offset:35840
	ds_read_b128 v[208:211], v136 offset:36864
	ds_read_b128 v[212:215], v136 offset:37888
	ds_read_b128 v[216:219], v136 offset:38912
	ds_read_b128 v[220:223], v136 offset:39936
	s_addc_u32 s77, s19, 0
	s_nop 0
	global_load_lds_dwordx4 v137, s[76:77]
	v_mov_b32_e32 v137, v132
	s_mov_b32 m0, s60
	s_nop 0
	global_load_lds_dwordx4 v137, s[76:77]
	s_waitcnt vmcnt(8)
	s_waitcnt lgkmcnt(0)
	s_barrier
	s_setprio 1
	s_waitcnt lgkmcnt(0)
	v_mfma_f32_16x16x32_bf16 v[126:129], v[138:141], v[176:179], v[126:129]
	v_mfma_f32_16x16x32_bf16 v[122:125], v[146:149], v[176:179], v[122:125]
	v_mfma_f32_16x16x32_bf16 v[118:121], v[138:141], v[200:203], v[118:121]
	v_mfma_f32_16x16x32_bf16 v[114:117], v[146:149], v[200:203], v[114:117]
	v_mfma_f32_16x16x32_bf16 v[102:105], v[138:141], v[208:211], v[102:105]
	v_mfma_f32_16x16x32_bf16 v[98:101], v[146:149], v[208:211], v[98:101]
	v_mfma_f32_16x16x32_bf16 v[86:89], v[138:141], v[216:219], v[86:89]
	v_mfma_f32_16x16x32_bf16 v[82:85], v[146:149], v[216:219], v[82:85]
	v_mfma_f32_16x16x32_bf16 v[126:129], v[142:145], v[180:183], v[126:129]
	v_mfma_f32_16x16x32_bf16 v[122:125], v[150:153], v[180:183], v[122:125]
	v_mfma_f32_16x16x32_bf16 v[118:121], v[142:145], v[204:207], v[118:121]
	v_mfma_f32_16x16x32_bf16 v[114:117], v[150:153], v[204:207], v[114:117]
	v_mfma_f32_16x16x32_bf16 v[102:105], v[142:145], v[212:215], v[102:105]
	v_mfma_f32_16x16x32_bf16 v[98:101], v[150:153], v[212:215], v[98:101]
	v_mfma_f32_16x16x32_bf16 v[86:89], v[142:145], v[220:223], v[86:89]
	v_mfma_f32_16x16x32_bf16 v[82:85], v[150:153], v[220:223], v[82:85]
	s_setprio 0
	s_setprio 1
	v_mfma_f32_16x16x32_bf16 v[110:113], v[154:157], v[176:179], v[110:113]
	v_mfma_f32_16x16x32_bf16 v[106:109], v[162:165], v[176:179], v[106:109]
	v_mfma_f32_16x16x32_bf16 v[94:97], v[154:157], v[200:203], v[94:97]
	v_mfma_f32_16x16x32_bf16 v[90:93], v[162:165], v[200:203], v[90:93]
	v_mfma_f32_16x16x32_bf16 v[78:81], v[154:157], v[208:211], v[78:81]
	v_mfma_f32_16x16x32_bf16 v[74:77], v[162:165], v[208:211], v[74:77]
	v_mfma_f32_16x16x32_bf16 v[70:73], v[154:157], v[216:219], v[70:73]
	v_mfma_f32_16x16x32_bf16 v[62:65], v[162:165], v[216:219], v[62:65]
	v_mfma_f32_16x16x32_bf16 v[110:113], v[158:161], v[180:183], v[110:113]
	v_mfma_f32_16x16x32_bf16 v[106:109], v[172:175], v[180:183], v[106:109]
	v_mfma_f32_16x16x32_bf16 v[94:97], v[158:161], v[204:207], v[94:97]
	v_mfma_f32_16x16x32_bf16 v[90:93], v[172:175], v[204:207], v[90:93]
	v_mfma_f32_16x16x32_bf16 v[78:81], v[158:161], v[212:215], v[78:81]
	v_mfma_f32_16x16x32_bf16 v[74:77], v[172:175], v[212:215], v[74:77]
	v_mfma_f32_16x16x32_bf16 v[70:73], v[158:161], v[220:223], v[70:73]
	v_mfma_f32_16x16x32_bf16 v[62:65], v[172:175], v[220:223], v[62:65]
	s_setprio 0
	s_barrier
	v_mov_b32_e32 v166, v1
	ds_read_b128 v[176:179], v136 offset:49152
	ds_read_b128 v[180:183], v136 offset:50176
	ds_read_b128 v[200:203], v136 offset:51200
	ds_read_b128 v[204:207], v136 offset:52224
	ds_read_b128 v[208:211], v136 offset:53248
	ds_read_b128 v[212:215], v136 offset:54272
	ds_read_b128 v[216:219], v136 offset:55296
	ds_read_b128 v[220:223], v136 offset:56320
	s_add_i32 s75, s75, s48
	v_lshl_add_u64 v[184:185], s[20:21], 0, v[166:167]
	v_lshl_add_u64 v[184:185], v[184:185], 0, s[80:81]
	s_mov_b32 m0, s75
	v_mov_b32_e32 v166, v131
	global_load_lds_dwordx4 v[184:185], off
	s_add_i32 m0, s75, 0x2000
	v_lshl_add_u64 v[184:185], s[20:21], 0, v[166:167]
	v_lshl_add_u64 v[184:185], v[184:185], 0, s[80:81]
	v_mov_b32_e32 v166, v1
	global_load_lds_dwordx4 v[184:185], off
	s_add_i32 s20, s82, s48
	v_lshl_add_u64 v[184:185], s[14:15], 0, v[166:167]
	v_lshl_add_u64 v[184:185], v[184:185], 0, s[80:81]
	s_mov_b32 m0, s20
	v_mov_b32_e32 v166, v131
	global_load_lds_dwordx4 v[184:185], off
	s_add_i32 m0, s20, 0x2000
	v_lshl_add_u64 v[184:185], s[14:15], 0, v[166:167]
	v_lshl_add_u64 v[184:185], v[184:185], 0, s[80:81]
	v_mov_b32_e32 v166, v130
	global_load_lds_dwordx4 v[184:185], off
	s_mov_b32 m0, s63
	v_lshl_add_u64 v[184:185], s[18:19], 0, v[166:167]
	v_lshl_add_u64 v[184:185], v[184:185], 0, s[80:81]
	v_mov_b32_e32 v166, v132
	global_load_lds_dwordx4 v[184:185], off
	s_mov_b32 m0, s64
	v_lshl_add_u64 v[184:185], s[18:19], 0, v[166:167]
	v_lshl_add_u64 v[184:185], v[184:185], 0, s[80:81]
	global_load_lds_dwordx4 v[184:185], off
	s_waitcnt vmcnt(8)
	s_waitcnt lgkmcnt(0)
	s_barrier
	s_setprio 1
	s_waitcnt lgkmcnt(0)
	v_mfma_f32_16x16x32_bf16 v[66:69], v[138:141], v[176:179], v[66:69]
	v_mfma_f32_16x16x32_bf16 v[58:61], v[146:149], v[176:179], v[58:61]
	v_mfma_f32_16x16x32_bf16 v[54:57], v[138:141], v[200:203], v[54:57]
	v_mfma_f32_16x16x32_bf16 v[50:53], v[146:149], v[200:203], v[50:53]
	v_mfma_f32_16x16x32_bf16 v[38:41], v[138:141], v[208:211], v[38:41]
	v_mfma_f32_16x16x32_bf16 v[34:37], v[146:149], v[208:211], v[34:37]
	v_mfma_f32_16x16x32_bf16 v[22:25], v[138:141], v[216:219], v[22:25]
	v_mfma_f32_16x16x32_bf16 v[18:21], v[146:149], v[216:219], v[18:21]
	v_mfma_f32_16x16x32_bf16 v[66:69], v[142:145], v[180:183], v[66:69]
	v_mfma_f32_16x16x32_bf16 v[58:61], v[150:153], v[180:183], v[58:61]
	v_mfma_f32_16x16x32_bf16 v[54:57], v[142:145], v[204:207], v[54:57]
	v_mfma_f32_16x16x32_bf16 v[50:53], v[150:153], v[204:207], v[50:53]
	v_mfma_f32_16x16x32_bf16 v[38:41], v[142:145], v[212:215], v[38:41]
	v_mfma_f32_16x16x32_bf16 v[34:37], v[150:153], v[212:215], v[34:37]
	v_mfma_f32_16x16x32_bf16 v[22:25], v[142:145], v[220:223], v[22:25]
	v_mfma_f32_16x16x32_bf16 v[18:21], v[150:153], v[220:223], v[18:21]
	s_setprio 0
	s_setprio 1
	v_mfma_f32_16x16x32_bf16 v[46:49], v[154:157], v[176:179], v[46:49]
	v_mfma_f32_16x16x32_bf16 v[42:45], v[162:165], v[176:179], v[42:45]
	v_mfma_f32_16x16x32_bf16 v[30:33], v[154:157], v[200:203], v[30:33]
	v_mfma_f32_16x16x32_bf16 v[26:29], v[162:165], v[200:203], v[26:29]
	v_mfma_f32_16x16x32_bf16 v[14:17], v[154:157], v[208:211], v[14:17]
	v_mfma_f32_16x16x32_bf16 v[10:13], v[162:165], v[208:211], v[10:13]
	v_mfma_f32_16x16x32_bf16 v[6:9], v[154:157], v[216:219], v[6:9]
	v_mfma_f32_16x16x32_bf16 v[2:5], v[162:165], v[216:219], v[2:5]
	v_mfma_f32_16x16x32_bf16 v[46:49], v[158:161], v[180:183], v[46:49]
	v_mfma_f32_16x16x32_bf16 v[42:45], v[172:175], v[180:183], v[42:45]
	v_mfma_f32_16x16x32_bf16 v[30:33], v[158:161], v[204:207], v[30:33]
	v_mfma_f32_16x16x32_bf16 v[26:29], v[172:175], v[204:207], v[26:29]
	v_mfma_f32_16x16x32_bf16 v[14:17], v[158:161], v[212:215], v[14:17]
	v_mfma_f32_16x16x32_bf16 v[10:13], v[172:175], v[212:215], v[10:13]
	v_mfma_f32_16x16x32_bf16 v[6:9], v[158:161], v[220:223], v[6:9]
	v_mfma_f32_16x16x32_bf16 v[2:5], v[172:175], v[220:223], v[2:5]
	s_setprio 0
	s_barrier
	s_add_u32 s72, s72, 0x100
	s_addc_u32 s73, s73, 0
	s_cmp_ge_u32 s74, s62
	s_mov_b64 s[14:15], s[16:17]
	s_mov_b32 s18, s74
	s_cbranch_scc0 .LBB0_401
	s_and_b64 vcc, exec, s[8:9]
	s_cbranch_vccz .LBB0_404
	s_barrier

.LBB0_545:
	v_bfe_i32 v4, v2, 27, 1
	v_lshlrev_b32_e32 v3, 4, v2
	v_lshrrev_b32_e32 v4, 22, v4
	v_add_u32_e32 v4, v3, v4
	v_and_b32_e32 v4, 0xfffffc00, v4
	v_sub_u32_e32 v4, v3, v4
	v_ashrrev_i32_e32 v1, 31, v2
	v_lshrrev_b32_e32 v5, 4, v4
	v_lshrrev_b32_e32 v1, 26, v1
	v_bitop3_b32 v5, v5, v4, 32 bitop3:0x6c
	v_ashrrev_i32_e32 v4, 31, v4
	v_add_u32_e32 v1, v2, v1
	v_lshrrev_b32_e32 v4, 26, v4
	v_ashrrev_i32_e32 v1, 6, v1
	v_add_u32_e32 v4, v5, v4
	v_lshlrev_b32_e32 v6, 3, v1
	v_ashrrev_i32_e32 v4, 6, v4
	v_and_b32_e32 v6, -16, v6
	v_mul_i32_i24_e32 v7, 64, v4
	v_add_u32_e32 v6, v4, v6
	v_sub_u32_e32 v5, v5, v7
	s_add_u32 s26, s4, 0x13200000
	v_lshlrev_b32_e32 v1, 5, v1
	v_ashrrev_i16_sdwa v5, v188, sext(v5) dst_sel:DWORD dst_unused:UNUSED_PAD src0_sel:DWORD src1_sel:BYTE_0
	v_lshlrev_b32_e32 v7, 1, v6
	v_lshrrev_b32_e32 v8, 2, v6
	v_and_b32_e32 v4, 3, v4
	s_mov_b32 s4, 0x1fffe0
	v_and_b32_e32 v1, 32, v1
	v_bfe_i32 v5, v5, 0, 16
	v_and_b32_e32 v7, 24, v7
	v_and_b32_e32 v8, 4, v8
	v_and_or_b32 v4, v6, s4, v4
	v_or3_b32 v4, v4, v8, v7
	v_add_lshl_u32 v5, v1, v5, 1
	v_add_u32_e32 v3, 0x2000, v3
	v_lshl_add_u32 v130, v4, 11, v5
	v_ashrrev_i32_e32 v4, 31, v3
	v_lshrrev_b32_e32 v4, 22, v4
	v_add_u32_e32 v4, v3, v4
	v_ashrrev_i32_e32 v4, 10, v4
	v_lshl_add_u32 v1, v6, 11, v5
	v_mul_i32_i24_e32 v5, 0x400, v4
	v_sub_u32_e32 v3, v3, v5
	v_lshrrev_b32_e32 v5, 4, v3
	v_bitop3_b32 v3, v5, v3, 32 bitop3:0x6c
	v_ashrrev_i32_e32 v6, 31, v3
	v_lshrrev_b32_e32 v6, 26, v6
	v_lshlrev_b32_e32 v5, 3, v4
	v_add_u32_e32 v6, v3, v6
	v_and_b32_e32 v5, -16, v5
	v_ashrrev_i32_e32 v7, 6, v6
	v_add_u32_e32 v5, v7, v5
	v_and_b32_e32 v7, 3, v7
	s_addc_u32 s27, s5, 0
	v_and_or_b32 v7, v5, s4, v7
	s_add_i32 s4, s8, s6
	s_ashr_i32 s5, s4, 31
	s_lshr_b32 s5, s5, 27
	s_add_i32 s5, s4, s5
	s_and_b32 s6, s5, 0xffe0
	s_sub_i32 s4, s4, s6
	s_bfe_i32 s6, s4, 0x80000
	s_bfe_u32 s6, s6, 0x3000c
	s_add_i32 s7, s4, s6
	s_bfe_i32 s6, s7, 0x80000
	s_and_b32 s7, s7, 0xf8
	s_sub_i32 s4, s4, s7
	s_sext_i32_i16 s6, s6
	s_sext_i32_i8 s4, s4
	s_lshl_b32 s5, s5, 6
	v_and_b32_e32 v6, 0xc0, v6
	s_lshr_b32 s6, s6, 3
	s_and_b32 s5, s5, 0xfffff800
	s_lshl_b32 s4, s4, 8
	s_ashr_i32 s11, s10, 6
	v_sub_u32_e32 v3, v3, v6
	s_add_i32 s8, s4, s5
	s_bfe_i64 s[4:5], s[6:7], 0x100000
	v_lshlrev_b32_e32 v4, 5, v4
	v_ashrrev_i16_sdwa v3, v188, sext(v3) dst_sel:DWORD dst_unused:UNUSED_PAD src0_sel:DWORD src1_sel:BYTE_0
	v_lshlrev_b32_e32 v6, 1, v5
	v_lshrrev_b32_e32 v8, 2, v5
	s_ashr_i32 s12, s10, 8
	s_lshl_b32 s28, s11, 10
	s_lshl_b64 s[4:5], s[4:5], 19
	v_and_b32_e32 v4, 32, v4
	v_bfe_i32 v3, v3, 0, 16
	v_and_b32_e32 v6, 24, v6
	v_and_b32_e32 v8, 4, v8
	s_add_u32 s18, s0, s4
	v_or3_b32 v6, v7, v8, v6
	v_add_lshl_u32 v3, v4, v3, 1
	s_addc_u32 s19, s1, s5
	s_ashr_i32 s9, s8, 31
	v_lshl_add_u32 v131, v5, 11, v3
	v_lshl_add_u32 v132, v6, 11, v3
	s_lshl_b64 s[4:5], s[8:9], 11
	s_add_i32 s9, s28, 0
	s_add_i32 m0, s9, 0x10000
	s_nop 0
	global_load_lds_dwordx4 v130, s[18:19]
	s_add_i32 m0, s9, 0x12000
	s_add_u32 s14, s18, 0x40000
	global_load_lds_dwordx4 v132, s[18:19]
	s_addc_u32 s15, s19, 0
	s_add_i32 m0, s9, 0x14000
	s_nop 0
	global_load_lds_dwordx4 v130, s[14:15]
	s_add_i32 m0, s9, 0x16000
	s_add_u32 s20, s26, s4
	global_load_lds_dwordx4 v132, s[14:15]
	s_addc_u32 s21, s27, s5
	s_mov_b32 m0, s9
	s_add_i32 s29, s9, 0x2000
	global_load_lds_dwordx4 v1, s[20:21]
	s_mov_b32 m0, s29
	s_add_u32 s4, s20, 0x40000
	global_load_lds_dwordx4 v131, s[20:21]
	s_addc_u32 s5, s21, 0
	s_add_i32 s30, s9, 0x4000
	s_mov_b32 m0, s30
	s_add_i32 s31, s9, 0x6000
	global_load_lds_dwordx4 v1, s[4:5]
	v_mov_b32_e32 v3, v131
	s_mov_b32 m0, s31
	s_cmp_eq_u32 s12, 1
	global_load_lds_dwordx4 v3, s[4:5]
	s_cselect_b64 s[4:5], -1, 0
	s_cmp_lg_u32 s12, 1
	s_cbranch_scc1 .LBB0_547
	s_barrier

.LBB0_557:
	s_add_u32 s20, s18, 0xfffc0080
	s_addc_u32 s21, s19, -1
	s_add_i32 s43, 0, 0x10000
	s_cmp_eq_u32 s42, 12
	s_cselect_b32 s21, s13, s21
	s_cselect_b32 s20, s39, s20
	v_add_u32_e32 v137, s43, v134
	s_cselect_b32 s23, s15, s41
	s_cselect_b32 s22, s14, s40
	s_add_i32 s46, 0, 0x14000
	ds_read_b128 v[138:141], v137
	ds_read_b128 v[142:145], v137 offset:1024
	ds_read_b128 v[146:149], v137 offset:2048
	ds_read_b128 v[150:153], v137 offset:3072
	v_add_u32_e32 v137, s46, v134
	ds_read_b128 v[154:157], v137
	ds_read_b128 v[158:161], v137 offset:1024
	ds_read_b128 v[162:165], v137 offset:2048
	ds_read_b128 v[172:175], v137 offset:3072
	v_mov_b32_e32 v137, v1
	ds_read_b128 v[176:179], v136
	ds_read_b128 v[180:183], v136 offset:1024
	ds_read_b128 v[200:203], v136 offset:2048
	ds_read_b128 v[204:207], v136 offset:3072
	ds_read_b128 v[208:211], v136 offset:4096
	ds_read_b128 v[212:215], v136 offset:5120
	ds_read_b128 v[216:219], v136 offset:6144
	ds_read_b128 v[220:223], v136 offset:7168
	s_add_i32 m0, s9, 0xc000
	s_nop 0
	global_load_lds_dwordx4 v137, s[18:19]
	s_add_i32 m0, s9, 0xe000
	s_nop 0
	global_load_lds_dwordx4 v131, s[18:19]
	s_waitcnt vmcnt(8)
	s_waitcnt lgkmcnt(0)
	s_barrier
	s_setprio 1
	s_waitcnt lgkmcnt(0)
	v_mfma_f32_16x16x32_bf16 v[126:129], v[138:141], v[176:179], v[126:129]
	v_mfma_f32_16x16x32_bf16 v[122:125], v[146:149], v[176:179], v[122:125]
	v_mfma_f32_16x16x32_bf16 v[118:121], v[138:141], v[200:203], v[118:121]
	v_mfma_f32_16x16x32_bf16 v[114:117], v[146:149], v[200:203], v[114:117]
	v_mfma_f32_16x16x32_bf16 v[102:105], v[138:141], v[208:211], v[102:105]
	v_mfma_f32_16x16x32_bf16 v[98:101], v[146:149], v[208:211], v[98:101]
	v_mfma_f32_16x16x32_bf16 v[86:89], v[138:141], v[216:219], v[86:89]
	v_mfma_f32_16x16x32_bf16 v[82:85], v[146:149], v[216:219], v[82:85]
	v_mfma_f32_16x16x32_bf16 v[126:129], v[142:145], v[180:183], v[126:129]
	v_mfma_f32_16x16x32_bf16 v[122:125], v[150:153], v[180:183], v[122:125]
	v_mfma_f32_16x16x32_bf16 v[118:121], v[142:145], v[204:207], v[118:121]
	v_mfma_f32_16x16x32_bf16 v[114:117], v[150:153], v[204:207], v[114:117]
	v_mfma_f32_16x16x32_bf16 v[102:105], v[142:145], v[212:215], v[102:105]
	v_mfma_f32_16x16x32_bf16 v[98:101], v[150:153], v[212:215], v[98:101]
	v_mfma_f32_16x16x32_bf16 v[86:89], v[142:145], v[220:223], v[86:89]
	v_mfma_f32_16x16x32_bf16 v[82:85], v[150:153], v[220:223], v[82:85]
	s_setprio 0
	s_setprio 1
	v_mfma_f32_16x16x32_bf16 v[110:113], v[154:157], v[176:179], v[110:113]
	v_mfma_f32_16x16x32_bf16 v[106:109], v[162:165], v[176:179], v[106:109]
	v_mfma_f32_16x16x32_bf16 v[94:97], v[154:157], v[200:203], v[94:97]
	v_mfma_f32_16x16x32_bf16 v[90:93], v[162:165], v[200:203], v[90:93]
	v_mfma_f32_16x16x32_bf16 v[78:81], v[154:157], v[208:211], v[78:81]
	v_mfma_f32_16x16x32_bf16 v[74:77], v[162:165], v[208:211], v[74:77]
	v_mfma_f32_16x16x32_bf16 v[70:73], v[154:157], v[216:219], v[70:73]
	v_mfma_f32_16x16x32_bf16 v[62:65], v[162:165], v[216:219], v[62:65]
	v_mfma_f32_16x16x32_bf16 v[110:113], v[158:161], v[180:183], v[110:113]
	v_mfma_f32_16x16x32_bf16 v[106:109], v[172:175], v[180:183], v[106:109]
	v_mfma_f32_16x16x32_bf16 v[94:97], v[158:161], v[204:207], v[94:97]
	v_mfma_f32_16x16x32_bf16 v[90:93], v[172:175], v[204:207], v[90:93]
	v_mfma_f32_16x16x32_bf16 v[78:81], v[158:161], v[212:215], v[78:81]
	v_mfma_f32_16x16x32_bf16 v[74:77], v[172:175], v[212:215], v[74:77]
	v_mfma_f32_16x16x32_bf16 v[70:73], v[158:161], v[220:223], v[70:73]
	v_mfma_f32_16x16x32_bf16 v[62:65], v[172:175], v[220:223], v[62:65]
	s_setprio 0
	s_barrier
	v_mov_b32_e32 v137, v130
	s_add_i32 s43, s43, s28
	ds_read_b128 v[176:179], v136 offset:16384
	ds_read_b128 v[180:183], v136 offset:17408
	ds_read_b128 v[200:203], v136 offset:18432
	ds_read_b128 v[204:207], v136 offset:19456
	ds_read_b128 v[208:211], v136 offset:20480
	ds_read_b128 v[212:215], v136 offset:21504
	ds_read_b128 v[216:219], v136 offset:22528
	ds_read_b128 v[220:223], v136 offset:23552
	s_mov_b32 m0, s43
	s_nop 0
	global_load_lds_dwordx4 v137, s[22:23]
	s_add_i32 m0, s43, 0x2000
	s_add_u32 s44, s22, 0x40000
	global_load_lds_dwordx4 v132, s[22:23]
	s_addc_u32 s45, s23, 0
	s_add_i32 s43, s46, s28
	s_mov_b32 m0, s43
	s_nop 0
	global_load_lds_dwordx4 v130, s[44:45]
	s_add_i32 m0, s43, 0x2000
	s_nop 0
	global_load_lds_dwordx4 v132, s[44:45]
	s_mov_b32 m0, s9
	s_nop 0
	global_load_lds_dwordx4 v1, s[20:21]
	v_mov_b32_e32 v137, v131
	s_mov_b32 m0, s29
	s_nop 0
	global_load_lds_dwordx4 v137, s[20:21]
	s_waitcnt vmcnt(8)
	s_waitcnt lgkmcnt(0)
	s_barrier
	s_setprio 1
	s_waitcnt lgkmcnt(0)
	v_mfma_f32_16x16x32_bf16 v[66:69], v[138:141], v[176:179], v[66:69]
	v_mfma_f32_16x16x32_bf16 v[58:61], v[146:149], v[176:179], v[58:61]
	v_mfma_f32_16x16x32_bf16 v[54:57], v[138:141], v[200:203], v[54:57]
	v_mfma_f32_16x16x32_bf16 v[50:53], v[146:149], v[200:203], v[50:53]
	v_mfma_f32_16x16x32_bf16 v[38:41], v[138:141], v[208:211], v[38:41]
	v_mfma_f32_16x16x32_bf16 v[34:37], v[146:149], v[208:211], v[34:37]
	v_mfma_f32_16x16x32_bf16 v[22:25], v[138:141], v[216:219], v[22:25]
	v_mfma_f32_16x16x32_bf16 v[18:21], v[146:149], v[216:219], v[18:21]
	v_mfma_f32_16x16x32_bf16 v[66:69], v[142:145], v[180:183], v[66:69]
	v_mfma_f32_16x16x32_bf16 v[58:61], v[150:153], v[180:183], v[58:61]
	v_mfma_f32_16x16x32_bf16 v[54:57], v[142:145], v[204:207], v[54:57]
	v_mfma_f32_16x16x32_bf16 v[50:53], v[150:153], v[204:207], v[50:53]
	v_mfma_f32_16x16x32_bf16 v[38:41], v[142:145], v[212:215], v[38:41]
	v_mfma_f32_16x16x32_bf16 v[34:37], v[150:153], v[212:215], v[34:37]
	v_mfma_f32_16x16x32_bf16 v[22:25], v[142:145], v[220:223], v[22:25]
	v_mfma_f32_16x16x32_bf16 v[18:21], v[150:153], v[220:223], v[18:21]
	s_setprio 0
	s_setprio 1
	v_mfma_f32_16x16x32_bf16 v[46:49], v[154:157], v[176:179], v[46:49]
	v_mfma_f32_16x16x32_bf16 v[42:45], v[162:165], v[176:179], v[42:45]
	v_mfma_f32_16x16x32_bf16 v[30:33], v[154:157], v[200:203], v[30:33]
	v_mfma_f32_16x16x32_bf16 v[26:29], v[162:165], v[200:203], v[26:29]
	v_mfma_f32_16x16x32_bf16 v[14:17], v[154:157], v[208:211], v[14:17]
	v_mfma_f32_16x16x32_bf16 v[10:13], v[162:165], v[208:211], v[10:13]
	v_mfma_f32_16x16x32_bf16 v[6:9], v[154:157], v[216:219], v[6:9]
	v_mfma_f32_16x16x32_bf16 v[2:5], v[162:165], v[216:219], v[2:5]
	v_mfma_f32_16x16x32_bf16 v[46:49], v[158:161], v[180:183], v[46:49]
	v_mfma_f32_16x16x32_bf16 v[42:45], v[172:175], v[180:183], v[42:45]
	v_mfma_f32_16x16x32_bf16 v[30:33], v[158:161], v[204:207], v[30:33]
	v_mfma_f32_16x16x32_bf16 v[26:29], v[172:175], v[204:207], v[26:29]
	v_mfma_f32_16x16x32_bf16 v[14:17], v[158:161], v[212:215], v[14:17]
	v_mfma_f32_16x16x32_bf16 v[10:13], v[172:175], v[212:215], v[10:13]
	v_mfma_f32_16x16x32_bf16 v[6:9], v[158:161], v[220:223], v[6:9]
	v_mfma_f32_16x16x32_bf16 v[2:5], v[172:175], v[220:223], v[2:5]
	s_setprio 0
	s_barrier
	s_add_i32 s43, 0, 0x18000
	v_add_u32_e32 v137, s43, v134
	s_add_i32 s46, 0, 0x1c000
	ds_read_b128 v[138:141], v137
	ds_read_b128 v[142:145], v137 offset:1024
	ds_read_b128 v[146:149], v137 offset:2048
	ds_read_b128 v[150:153], v137 offset:3072
	v_add_u32_e32 v137, s46, v134
	ds_read_b128 v[154:157], v137
	ds_read_b128 v[158:161], v137 offset:1024
	ds_read_b128 v[162:165], v137 offset:2048
	ds_read_b128 v[172:175], v137 offset:3072
	s_add_u32 s44, s20, 0x40000
	v_mov_b32_e32 v137, v1
	s_mov_b32 m0, s30
	ds_read_b128 v[176:179], v136 offset:32768
	ds_read_b128 v[180:183], v136 offset:33792
	ds_read_b128 v[200:203], v136 offset:34816
	ds_read_b128 v[204:207], v136 offset:35840
	ds_read_b128 v[208:211], v136 offset:36864
	ds_read_b128 v[212:215], v136 offset:37888
	ds_read_b128 v[216:219], v136 offset:38912
	ds_read_b128 v[220:223], v136 offset:39936
	s_addc_u32 s45, s21, 0
	s_nop 0
	global_load_lds_dwordx4 v137, s[44:45]
	s_mov_b32 m0, s31
	s_nop 0
	global_load_lds_dwordx4 v131, s[44:45]
	s_waitcnt vmcnt(8)
	s_waitcnt lgkmcnt(0)
	s_barrier
	s_setprio 1
	s_waitcnt lgkmcnt(0)
	v_mfma_f32_16x16x32_bf16 v[126:129], v[138:141], v[176:179], v[126:129]
	v_mfma_f32_16x16x32_bf16 v[122:125], v[146:149], v[176:179], v[122:125]
	v_mfma_f32_16x16x32_bf16 v[118:121], v[138:141], v[200:203], v[118:121]
	v_mfma_f32_16x16x32_bf16 v[114:117], v[146:149], v[200:203], v[114:117]
	v_mfma_f32_16x16x32_bf16 v[102:105], v[138:141], v[208:211], v[102:105]
	v_mfma_f32_16x16x32_bf16 v[98:101], v[146:149], v[208:211], v[98:101]
	v_mfma_f32_16x16x32_bf16 v[86:89], v[138:141], v[216:219], v[86:89]
	v_mfma_f32_16x16x32_bf16 v[82:85], v[146:149], v[216:219], v[82:85]
	v_mfma_f32_16x16x32_bf16 v[126:129], v[142:145], v[180:183], v[126:129]
	v_mfma_f32_16x16x32_bf16 v[122:125], v[150:153], v[180:183], v[122:125]
	v_mfma_f32_16x16x32_bf16 v[118:121], v[142:145], v[204:207], v[118:121]
	v_mfma_f32_16x16x32_bf16 v[114:117], v[150:153], v[204:207], v[114:117]
	v_mfma_f32_16x16x32_bf16 v[102:105], v[142:145], v[212:215], v[102:105]
	v_mfma_f32_16x16x32_bf16 v[98:101], v[150:153], v[212:215], v[98:101]
	v_mfma_f32_16x16x32_bf16 v[86:89], v[142:145], v[220:223], v[86:89]
	v_mfma_f32_16x16x32_bf16 v[82:85], v[150:153], v[220:223], v[82:85]
	s_setprio 0
	s_setprio 1
	v_mfma_f32_16x16x32_bf16 v[110:113], v[154:157], v[176:179], v[110:113]
	v_mfma_f32_16x16x32_bf16 v[106:109], v[162:165], v[176:179], v[106:109]
	v_mfma_f32_16x16x32_bf16 v[94:97], v[154:157], v[200:203], v[94:97]
	v_mfma_f32_16x16x32_bf16 v[90:93], v[162:165], v[200:203], v[90:93]
	v_mfma_f32_16x16x32_bf16 v[78:81], v[154:157], v[208:211], v[78:81]
	v_mfma_f32_16x16x32_bf16 v[74:77], v[162:165], v[208:211], v[74:77]
	v_mfma_f32_16x16x32_bf16 v[70:73], v[154:157], v[216:219], v[70:73]
	v_mfma_f32_16x16x32_bf16 v[62:65], v[162:165], v[216:219], v[62:65]
	v_mfma_f32_16x16x32_bf16 v[110:113], v[158:161], v[180:183], v[110:113]
	v_mfma_f32_16x16x32_bf16 v[106:109], v[172:175], v[180:183], v[106:109]
	v_mfma_f32_16x16x32_bf16 v[94:97], v[158:161], v[204:207], v[94:97]
	v_mfma_f32_16x16x32_bf16 v[90:93], v[172:175], v[204:207], v[90:93]
	v_mfma_f32_16x16x32_bf16 v[78:81], v[158:161], v[212:215], v[78:81]
	v_mfma_f32_16x16x32_bf16 v[74:77], v[172:175], v[212:215], v[74:77]
	v_mfma_f32_16x16x32_bf16 v[70:73], v[158:161], v[220:223], v[70:73]
	v_mfma_f32_16x16x32_bf16 v[62:65], v[172:175], v[220:223], v[62:65]
	s_setprio 0
	s_barrier
	v_mov_b32_e32 v166, v130
	ds_read_b128 v[176:179], v136 offset:49152
	ds_read_b128 v[180:183], v136 offset:50176
	ds_read_b128 v[200:203], v136 offset:51200
	ds_read_b128 v[204:207], v136 offset:52224
	ds_read_b128 v[208:211], v136 offset:53248
	ds_read_b128 v[212:215], v136 offset:54272
	ds_read_b128 v[216:219], v136 offset:55296
	ds_read_b128 v[220:223], v136 offset:56320
	s_add_i32 s43, s43, s28
	v_lshl_add_u64 v[184:185], s[22:23], 0, v[166:167]
	v_lshl_add_u64 v[184:185], v[184:185], 0, s[80:81]
	s_mov_b32 m0, s43
	v_mov_b32_e32 v166, v132
	global_load_lds_dwordx4 v[184:185], off
	s_add_i32 m0, s43, 0x2000
	v_mov_b32_e32 v137, v130
	v_lshl_add_u64 v[184:185], s[22:23], 0, v[166:167]
	s_add_u32 s22, s22, 0x40080
	v_lshl_add_u64 v[184:185], v[184:185], 0, s[80:81]
	s_addc_u32 s23, s23, 0
	s_add_i32 s43, s46, s28
	global_load_lds_dwordx4 v[184:185], off
	s_mov_b32 m0, s43
	v_mov_b32_e32 v166, v1
	global_load_lds_dwordx4 v137, s[22:23]
	v_mov_b32_e32 v137, v132
	s_add_i32 m0, s43, 0x2000
	s_nop 0
	global_load_lds_dwordx4 v137, s[22:23]
	s_mov_b32 m0, s34
	v_lshl_add_u64 v[184:185], s[20:21], 0, v[166:167]
	v_lshl_add_u64 v[184:185], v[184:185], 0, s[80:81]
	v_mov_b32_e32 v166, v131
	global_load_lds_dwordx4 v[184:185], off
	s_mov_b32 m0, s35
	v_lshl_add_u64 v[184:185], s[20:21], 0, v[166:167]
	v_lshl_add_u64 v[184:185], v[184:185], 0, s[80:81]
	global_load_lds_dwordx4 v[184:185], off
	s_waitcnt vmcnt(8)
	s_waitcnt lgkmcnt(0)
	s_barrier
	s_setprio 1
	s_waitcnt lgkmcnt(0)
	v_mfma_f32_16x16x32_bf16 v[66:69], v[138:141], v[176:179], v[66:69]
	v_mfma_f32_16x16x32_bf16 v[58:61], v[146:149], v[176:179], v[58:61]
	v_mfma_f32_16x16x32_bf16 v[54:57], v[138:141], v[200:203], v[54:57]
	v_mfma_f32_16x16x32_bf16 v[50:53], v[146:149], v[200:203], v[50:53]
	v_mfma_f32_16x16x32_bf16 v[38:41], v[138:141], v[208:211], v[38:41]
	v_mfma_f32_16x16x32_bf16 v[34:37], v[146:149], v[208:211], v[34:37]
	v_mfma_f32_16x16x32_bf16 v[22:25], v[138:141], v[216:219], v[22:25]
	v_mfma_f32_16x16x32_bf16 v[18:21], v[146:149], v[216:219], v[18:21]
	v_mfma_f32_16x16x32_bf16 v[66:69], v[142:145], v[180:183], v[66:69]
	v_mfma_f32_16x16x32_bf16 v[58:61], v[150:153], v[180:183], v[58:61]
	v_mfma_f32_16x16x32_bf16 v[54:57], v[142:145], v[204:207], v[54:57]
	v_mfma_f32_16x16x32_bf16 v[50:53], v[150:153], v[204:207], v[50:53]
	v_mfma_f32_16x16x32_bf16 v[38:41], v[142:145], v[212:215], v[38:41]
	v_mfma_f32_16x16x32_bf16 v[34:37], v[150:153], v[212:215], v[34:37]
	v_mfma_f32_16x16x32_bf16 v[22:25], v[142:145], v[220:223], v[22:25]
	v_mfma_f32_16x16x32_bf16 v[18:21], v[150:153], v[220:223], v[18:21]
	s_setprio 0
	s_setprio 1
	v_mfma_f32_16x16x32_bf16 v[46:49], v[154:157], v[176:179], v[46:49]
	v_mfma_f32_16x16x32_bf16 v[42:45], v[162:165], v[176:179], v[42:45]
	v_mfma_f32_16x16x32_bf16 v[30:33], v[154:157], v[200:203], v[30:33]
	v_mfma_f32_16x16x32_bf16 v[26:29], v[162:165], v[200:203], v[26:29]
	v_mfma_f32_16x16x32_bf16 v[14:17], v[154:157], v[208:211], v[14:17]
	v_mfma_f32_16x16x32_bf16 v[10:13], v[162:165], v[208:211], v[10:13]
	v_mfma_f32_16x16x32_bf16 v[6:9], v[154:157], v[216:219], v[6:9]
	v_mfma_f32_16x16x32_bf16 v[2:5], v[162:165], v[216:219], v[2:5]
	v_mfma_f32_16x16x32_bf16 v[46:49], v[158:161], v[180:183], v[46:49]
	v_mfma_f32_16x16x32_bf16 v[42:45], v[172:175], v[180:183], v[42:45]
	v_mfma_f32_16x16x32_bf16 v[30:33], v[158:161], v[204:207], v[30:33]
	v_mfma_f32_16x16x32_bf16 v[26:29], v[172:175], v[204:207], v[26:29]
	v_mfma_f32_16x16x32_bf16 v[14:17], v[158:161], v[212:215], v[14:17]
	v_mfma_f32_16x16x32_bf16 v[10:13], v[172:175], v[212:215], v[10:13]
	v_mfma_f32_16x16x32_bf16 v[6:9], v[158:161], v[220:223], v[6:9]
	v_mfma_f32_16x16x32_bf16 v[2:5], v[172:175], v[220:223], v[2:5]
	s_setprio 0
	s_barrier
	s_add_i32 s42, s42, 2
	s_add_u32 s40, s40, 0x100
	s_addc_u32 s41, s41, 0
	s_add_u32 s18, s18, 0x100
	s_addc_u32 s19, s19, 0
	s_cmp_gt_u32 s42, 13
	s_cbranch_scc0 .LBB0_557
	s_and_b64 vcc, exec, s[10:11]
	s_cbranch_vccz .LBB0_560
	s_barrier

.LBB0_767:
	s_mov_b64 s[0:1], s[78:79]
	s_mov_b64 s[6:7], s[78:79]
	v_readlane_b32 s2, v238, 7
	s_mov_b64 s[8:9], s[78:79]
	v_mov_b32_e32 v162, 0x7f
	s_waitcnt vmcnt(0)
	v_mov_b32_e32 v1, s2
	s_waitcnt vmcnt(0) lgkmcnt(0)
	ds_read_b64 v[2:3], v1
	v_readlane_b32 s2, v238, 8
	s_mov_b32 s4, s92
	s_waitcnt lgkmcnt(0)
	v_readfirstlane_b32 s14, v3
	v_mov_b32_e32 v1, s2
	v_readfirstlane_b32 s15, v2
	ds_read_b64 v[4:5], v1
	v_mov_b32_e32 v2, v0
	v_mov_b32_e32 v1, 0x79
	v_mov_b32_e32 v3, s68
	ds_read_b32 v3, v3
	s_ashr_i32 s2, s4, 31
	s_lshr_b32 s2, s2, 29
	s_add_i32 s2, s4, s2
	s_ashr_i32 s2, s2, 3
	s_waitcnt lgkmcnt(0)
	v_readfirstlane_b32 s3, v3
	s_lshl_b32 s3, s3, 3
	s_addk_i32 s2, 0xb0
	s_cmpk_lt_i32 s4, 0xa00
	s_cselect_b32 s2, s2, 0xb0
	s_lshl_b32 s2, s2, 2
	s_add_i32 s2, s2, 0
	s_add_i32 s2, s2, 0x23040
	v_mov_b32_e32 v3, s2
	ds_read_b32 v3, v3
	v_readfirstlane_b32 s16, v5
	v_readfirstlane_b32 s17, v4
	v_readfirstlane_b32 s12, v2
	s_cmp_ge_i32 s4, s3
	s_waitcnt lgkmcnt(0)
	v_readfirstlane_b32 s2, v3
	s_cbranch_scc1 .LBB0_787
	v_bfe_i32 v5, v2, 27, 1
	v_lshlrev_b32_e32 v3, 4, v2
	v_lshrrev_b32_e32 v5, 22, v5
	v_add_u32_e32 v5, v3, v5
	v_and_b32_e32 v5, 0xfffffc00, v5
	v_sub_u32_e32 v5, v3, v5
	v_lshrrev_b32_e32 v6, 4, v5
	v_ashrrev_i32_e32 v4, 31, v2
	v_bitop3_b32 v6, v6, v5, 32 bitop3:0x6c
	v_ashrrev_i32_e32 v5, 31, v5
	v_lshrrev_b32_e32 v4, 26, v4
	v_lshrrev_b32_e32 v5, 26, v5
	v_add_u32_e32 v4, v2, v4
	v_add_u32_e32 v5, v6, v5
	v_ashrrev_i32_e32 v4, 6, v4
	v_ashrrev_i32_e32 v5, 6, v5
	v_lshlrev_b32_e32 v7, 3, v4
	v_mul_i32_i24_e32 v8, 64, v5
	v_and_b32_e32 v7, -16, v7
	v_lshlrev_b32_e32 v4, 5, v4
	v_sub_u32_e32 v6, v6, v8
	v_add_u32_e32 v7, v5, v7
	v_and_b32_e32 v4, 32, v4
	v_ashrrev_i16_sdwa v6, v188, sext(v6) dst_sel:DWORD dst_unused:UNUSED_PAD src0_sel:DWORD src1_sel:BYTE_0
	v_add_u32_sdwa v6, v4, sext(v6) dst_sel:DWORD dst_unused:UNUSED_PAD src0_sel:DWORD src1_sel:WORD_0
	v_lshlrev_b32_e32 v4, 1, v7
	v_lshrrev_b32_e32 v8, 2, v7
	v_and_b32_e32 v5, 3, v5
	s_mov_b32 s3, 0x3fffe0
	v_and_b32_e32 v4, 24, v4
	v_and_b32_e32 v8, 4, v8
	v_and_or_b32 v5, v7, s3, v5
	v_or3_b32 v4, v5, v8, v4
	v_lshlrev_b32_e32 v8, 1, v6
	v_add_u32_e32 v3, 0x2000, v3
	v_lshl_add_u32 v163, v4, 10, v8
	v_ashrrev_i32_e32 v4, 31, v3
	v_lshrrev_b32_e32 v4, 22, v4
	v_add_u32_e32 v4, v3, v4
	v_ashrrev_i32_e32 v4, 10, v4
	v_mul_i32_i24_e32 v5, 0x400, v4
	v_sub_u32_e32 v3, v3, v5
	v_lshrrev_b32_e32 v5, 4, v3
	v_bitop3_b32 v3, v5, v3, 32 bitop3:0x6c
	v_ashrrev_i32_e32 v9, 31, v3
	v_lshrrev_b32_e32 v9, 26, v9
	v_lshlrev_b32_e32 v5, 3, v4
	v_add_u32_e32 v9, v3, v9
	v_and_b32_e32 v5, -16, v5
	v_ashrrev_i32_e32 v10, 6, v9
	s_add_u32 s26, s0, 0x1f200000
	v_add_u32_e32 v11, v10, v5
	v_and_b32_e32 v5, 0xc0, v9
	s_addc_u32 s27, s1, 0
	v_lshlrev_b32_e32 v4, 5, v4
	v_sub_u32_e32 v3, v3, v5
	s_add_u32 s0, s8, 0x37600000
	v_and_b32_e32 v4, 32, v4
	v_ashrrev_i16_sdwa v3, v188, sext(v3) dst_sel:DWORD dst_unused:UNUSED_PAD src0_sel:DWORD src1_sel:BYTE_0
	s_addc_u32 s1, s9, 0
	v_add_u32_sdwa v3, v4, sext(v3) dst_sel:DWORD dst_unused:UNUSED_PAD src0_sel:DWORD src1_sel:WORD_0
	v_lshlrev_b32_e32 v4, 1, v11
	v_lshrrev_b32_e32 v5, 2, v11
	v_and_b32_e32 v9, 3, v10
	s_lshl_b32 s5, s2, 2
	v_and_b32_e32 v4, 24, v4
	v_and_b32_e32 v5, 4, v5
	v_and_or_b32 v9, v11, s3, v9
	s_add_i32 s5, s5, 0
	v_or3_b32 v4, v9, v5, v4
	v_lshlrev_b32_e32 v9, 1, v3
	s_add_i32 s10, s5, 0x23040
	v_lshl_add_u32 v164, v4, 10, v9
	v_mov_b32_e32 v4, s10
	ds_read2_b32 v[4:5], v4 offset1:1
	s_ashr_i32 s18, s12, 6
	s_ashr_i32 s13, s12, 8
	s_lshl_b32 s28, s18, 10
	s_ashr_i32 s3, s2, 31
	s_waitcnt lgkmcnt(0)
	v_readfirstlane_b32 s19, v4
	v_readfirstlane_b32 s10, v5
	s_sub_i32 s11, s10, s19
	s_abs_i32 s21, s11
	v_cvt_f32_u32_e32 v4, s21
	s_sub_i32 s22, 0, s21
	s_lshl_b32 s10, s19, 3
	s_sub_i32 s4, s4, s10
	v_rcp_iflag_f32_e32 v4, v4
	s_abs_i32 s20, s4
	s_xor_b32 s10, s4, s11
	s_ashr_i32 s10, s10, 31
	v_mul_f32_e32 v4, 0x4f7ffffe, v4
	v_cvt_u32_f32_e32 v4, v4
	v_lshrrev_b32_e32 v3, 9, v3
	v_add_u32_e32 v3, v3, v11
	v_and_b32_e32 v172, 0x3fffff, v3
	v_readfirstlane_b32 s23, v4
	s_mul_i32 s22, s22, s23
	s_mul_hi_u32 s22, s23, s22
	s_add_i32 s23, s23, s22
	s_mul_hi_u32 s22, s20, s23
	s_mul_i32 s23, s22, s21
	s_sub_i32 s20, s20, s23
	s_add_i32 s23, s22, 1
	s_sub_i32 s24, s20, s21
	s_cmp_ge_u32 s20, s21
	s_cselect_b32 s22, s23, s22
	s_cselect_b32 s20, s24, s20
	s_add_i32 s23, s22, 1
	s_cmp_ge_u32 s20, s21
	s_cselect_b32 s20, s23, s22
	s_xor_b32 s20, s20, s10
	s_sub_i32 s10, s20, s10
	s_mul_i32 s11, s10, s11
	s_sub_i32 s22, s4, s11
	s_add_i32 s4, s5, 0x23100
	v_mov_b32_e32 v4, s4
	ds_read_b32 v4, v4
	s_lshl_b32 s29, s22, 8
	s_lshl_b64 s[4:5], s[2:3], 21
	v_readlane_b32 s11, v238, 43
	s_add_u32 s20, s11, s4
	v_readlane_b32 s4, v238, 44
	s_addc_u32 s21, s4, s5
	s_ashr_i32 s11, s10, 31
	s_lshl_b64 s[4:5], s[10:11], 18
	s_waitcnt lgkmcnt(0)
	v_readfirstlane_b32 s30, v4
	s_add_u32 s20, s20, s4
	v_lshrrev_b32_e32 v4, 9, v6
	s_addc_u32 s21, s21, s5
	s_lshl_b64 s[4:5], s[2:3], 17
	v_add_u32_e32 v4, v4, v7
	s_add_u32 s4, s26, s4
	v_and_b32_e32 v165, 0x3fffff, v4
	s_addc_u32 s5, s27, s5
	s_add_i32 s3, s30, -1
	v_add_u32_e32 v4, s29, v165
	v_min_i32_e32 v4, s3, v4
	v_ashrrev_i32_e32 v5, 31, v4
	v_lshl_add_u64 v[4:5], v[4:5], 3, s[4:5]
	v_add_u32_e32 v3, s29, v172
	global_load_dword v6, v[4:5], off
	v_min_i32_e32 v4, s3, v3
	v_ashrrev_i32_e32 v5, 31, v4
	v_lshl_add_u64 v[4:5], v[4:5], 3, s[4:5]
	s_or_b32 s11, s29, 0x80
	global_load_dword v3, v[4:5], off
	v_add_u32_e32 v4, s11, v165
	v_min_i32_e32 v4, s3, v4
	v_ashrrev_i32_e32 v5, 31, v4
	v_lshl_add_u64 v[4:5], v[4:5], 3, s[4:5]
	global_load_dword v7, v[4:5], off
	v_add_u32_e32 v4, s11, v172
	v_min_i32_e32 v4, s3, v4
	v_ashrrev_i32_e32 v5, 31, v4
	v_lshl_add_u64 v[4:5], v[4:5], 3, s[4:5]
	global_load_dword v4, v[4:5], off
	v_and_b32_e32 v174, 0x3fe, v9
	v_and_b32_e32 v173, 0x3fe, v8
	s_add_i32 s31, s28, 0
	s_add_i32 m0, s31, 0x10000
	s_waitcnt vmcnt(3)
	v_lshlrev_b32_e32 v5, 8, v6
	v_and_or_b32 v199, v5, s89, v173
	s_waitcnt vmcnt(2)
	v_lshlrev_b32_e32 v3, 8, v3
	v_and_or_b32 v200, v3, s89, v174
	s_waitcnt vmcnt(1)
	v_lshlrev_b32_e32 v3, 8, v7
	v_and_or_b32 v201, v3, s89, v173
	s_waitcnt vmcnt(0)
	v_lshlrev_b32_e32 v3, 8, v4
	v_and_or_b32 v202, v3, s89, v174
	s_nop 0
	global_load_lds_dwordx4 v163, s[20:21]
	s_add_i32 m0, s31, 0x12000
	s_add_u32 s4, s20, 0x20000
	global_load_lds_dwordx4 v164, s[20:21]
	s_addc_u32 s5, s21, 0
	s_add_i32 m0, s31, 0x14000
	s_add_i32 s34, s31, 0x2000
	global_load_lds_dwordx4 v163, s[4:5]
	s_add_i32 m0, s31, 0x16000
	s_add_i32 s35, s31, 0x4000
	global_load_lds_dwordx4 v164, s[4:5]
	s_mov_b32 m0, s31
	s_add_i32 s36, s31, 0x6000
	global_load_lds_dwordx4 v199, s[0:1]
	s_mov_b32 m0, s34
	v_mov_b32_e32 v3, v200
	s_cmp_eq_u32 s13, 1
	global_load_lds_dwordx4 v3, s[0:1]
	s_mov_b32 m0, s35
	v_mov_b32_e32 v3, v201
	s_cselect_b64 s[4:5], -1, 0
	global_load_lds_dwordx4 v3, s[0:1]
	s_mov_b32 m0, s36
	v_mov_b32_e32 v3, v202
	s_cmp_lg_u32 s13, 1
	global_load_lds_dwordx4 v3, s[0:1]
	s_cbranch_scc1 .LBB0_770
	s_barrier
.LBB0_770:
	s_add_i32 s22, s22, s19
	s_lshl_b32 s47, s22, 8
	s_lshl_b32 s24, s10, 8
	s_add_u32 s6, s6, 0x8200000
	v_readlane_b32 s3, v238, 41
	v_and_b32_e32 v3, 15, v2
	v_and_b32_e32 v4, 63, v2
	v_bfe_u32 v5, v2, 4, 2
	v_and_b32_e32 v7, 48, v2
	v_lshlrev_b32_e32 v2, 2, v2
	s_addc_u32 s7, s7, 0
	s_lshl_b32 s84, s3, 15
	s_and_b32 s3, s18, 3
	v_lshl_or_b32 v175, s13, 6, v3
	s_lshl_b32 s10, s13, 13
	v_lshl_or_b32 v3, v3, 6, v7
	v_and_b32_e32 v2, 32, v2
	v_bitop3_b32 v7, v3, s10, v2 bitop3:0xde
	s_lshl_b32 s10, s3, 12
	v_mov_b32_e32 v166, v163
	v_bitop3_b32 v176, v3, s10, v2 bitop3:0xde
	s_waitcnt vmcnt(2)
	s_barrier
	s_add_i32 m0, s31, 0x18000
	v_lshl_add_u64 v[2:3], s[20:21], 0, v[166:167]
	v_lshl_add_u64 v[2:3], v[2:3], 0, s[80:81]
	v_mov_b32_e32 v166, v164
	global_load_lds_dwordx4 v[2:3], off
	s_add_i32 m0, s31, 0x1a000
	v_lshl_add_u64 v[2:3], s[20:21], 0, v[166:167]
	v_lshl_add_u64 v[2:3], v[2:3], 0, s[80:81]
	global_load_lds_dwordx4 v[2:3], off
	s_add_u32 s8, s8, 0x37600080
	s_addc_u32 s9, s9, 0
	s_add_i32 s37, s31, 0x8000
	s_mov_b32 m0, s37
	s_add_i32 s38, s31, 0xa000
	global_load_lds_dwordx4 v199, s[8:9]
	s_mov_b32 m0, s38
	s_add_u32 s10, s20, 0x20080
	global_load_lds_dwordx4 v200, s[8:9]
	v_mov_b32_e32 v2, v163
	s_addc_u32 s11, s21, 0
	s_add_i32 m0, s31, 0x1c000
	v_lshlrev_b32_e32 v6, 3, v5
	global_load_lds_dwordx4 v2, s[10:11]
	v_mov_b32_e32 v2, v164
	s_add_i32 m0, s31, 0x1e000
	s_cmp_lt_i32 s18, 4
	global_load_lds_dwordx4 v2, s[10:11]
	s_cselect_b64 s[10:11], -1, 0
	s_and_b32 s39, s12, 64
	s_lshl_b32 s19, s18, 8
	s_cmpk_lt_u32 s12, 0x100
	s_cselect_b64 s[12:13], -1, 0
	s_cmp_gt_i32 s18, 1
	v_lshlrev_b32_e32 v2, 5, v5
	v_lshl_or_b32 v178, s3, 7, v2
	v_lshl_or_b32 v180, s3, 5, v6
	s_cselect_b32 s3, s16, s14
	s_cselect_b32 s16, s17, s15
	s_lshl_b64 s[14:15], s[84:85], 2
	s_waitcnt vmcnt(6)
	s_add_u32 s40, s16, s14
	s_addc_u32 s41, s3, s15
	s_add_i32 s43, s19, 0
	v_lshlrev_b32_e32 v177, 2, v4
	v_or_b32_e32 v179, 16, v178
	s_mov_b32 s42, 0
	s_add_i32 s43, s43, 0x20000
	v_add_u32_e32 v181, 0, v7
	s_barrier
	s_branch .LBB0_773

.LBB0_778:
	s_add_u32 s24, s20, 0x80
	s_addc_u32 s25, s21, 0
	s_and_b64 s[22:23], s[2:3], exec
	s_cselect_b32 s23, s1, s25
	s_cselect_b32 s22, s0, s24
	s_add_i32 s53, 0, 0x10000
	s_and_b64 s[24:25], s[2:3], exec
	s_cselect_b32 s25, s17, s50
	s_cselect_b32 s24, s16, s49
	s_add_i32 s52, 0, 0x14000
	v_add_u32_e32 v2, s53, v176
	v_add_u32_e32 v6, s52, v176
	ds_read_b128 v[26:29], v2
	ds_read_b128 v[30:33], v2 offset:1024
	ds_read_b128 v[18:21], v2 offset:2048
	ds_read_b128 v[22:25], v2 offset:3072
	ds_read_b128 v[10:13], v6
	ds_read_b128 v[14:17], v6 offset:1024
	ds_read_b128 v[2:5], v6 offset:2048
	ds_read_b128 v[6:9], v6 offset:3072
	v_mov_b32_e32 v166, v184
	ds_read_b128 v[204:207], v181
	ds_read_b128 v[208:211], v181 offset:1024
	ds_read_b128 v[212:215], v181 offset:2048
	ds_read_b128 v[216:219], v181 offset:3072
	ds_read_b128 v[220:223], v181 offset:4096
	ds_read_b128 v[224:227], v181 offset:5120
	ds_read_b128 v[228:231], v181 offset:6144
	ds_read_b128 v[232:235], v181 offset:7168
	s_add_i32 m0, s31, 0xc000
	s_nop 0
	global_load_lds_dwordx4 v201, s[20:21]
	v_mov_b32_e32 v166, v185
	s_add_i32 m0, s31, 0xe000
	v_mov_b32_e32 v166, v202
	s_nop 0
	global_load_lds_dwordx4 v166, s[20:21]
	s_waitcnt vmcnt(8)
	s_waitcnt lgkmcnt(0)
	s_barrier
	s_setprio 1
	s_waitcnt lgkmcnt(0)
	s_cmp_eq_u32 s51, -2
	s_cbranch_scc1 .Lmy_zfirst_p6_0
	s_nop 1
	v_mfma_scale_f32_16x16x128_f8f6f4 v[158:161], v[26:33], v[204:211], v[158:161], v1, v162 op_sel_hi:[0,0,0]
	s_nop 1
	v_mfma_scale_f32_16x16x128_f8f6f4 v[150:153], v[18:25], v[204:211], v[150:153], v1, v162 op_sel_hi:[0,0,0]
	s_nop 1
	v_mfma_scale_f32_16x16x128_f8f6f4 v[142:145], v[26:33], v[212:219], v[142:145], v1, v162 op_sel_hi:[0,0,0]
	s_nop 1
	v_mfma_scale_f32_16x16x128_f8f6f4 v[134:137], v[18:25], v[212:219], v[134:137], v1, v162 op_sel_hi:[0,0,0]
	s_nop 1
	v_mfma_scale_f32_16x16x128_f8f6f4 v[126:129], v[26:33], v[220:227], v[126:129], v1, v162 op_sel_hi:[0,0,0]
	s_nop 1
	v_mfma_scale_f32_16x16x128_f8f6f4 v[118:121], v[18:25], v[220:227], v[118:121], v1, v162 op_sel_hi:[0,0,0]
	s_nop 1
	v_mfma_scale_f32_16x16x128_f8f6f4 v[110:113], v[26:33], v[228:235], v[110:113], v1, v162 op_sel_hi:[0,0,0]
	s_nop 1
	v_mfma_scale_f32_16x16x128_f8f6f4 v[102:105], v[18:25], v[228:235], v[102:105], v1, v162 op_sel_hi:[0,0,0]
	s_setprio 0
	s_setprio 1
	s_nop 1
	v_mfma_scale_f32_16x16x128_f8f6f4 v[154:157], v[10:17], v[204:211], v[154:157], v1, v162 op_sel_hi:[0,0,0]
	s_nop 1
	v_mfma_scale_f32_16x16x128_f8f6f4 v[146:149], v[2:9], v[204:211], v[146:149], v1, v162 op_sel_hi:[0,0,0]
	s_nop 1
	v_mfma_scale_f32_16x16x128_f8f6f4 v[138:141], v[10:17], v[212:219], v[138:141], v1, v162 op_sel_hi:[0,0,0]
	s_nop 1
	v_mfma_scale_f32_16x16x128_f8f6f4 v[130:133], v[2:9], v[212:219], v[130:133], v1, v162 op_sel_hi:[0,0,0]
	s_nop 1
	v_mfma_scale_f32_16x16x128_f8f6f4 v[122:125], v[10:17], v[220:227], v[122:125], v1, v162 op_sel_hi:[0,0,0]
	s_nop 1
	v_mfma_scale_f32_16x16x128_f8f6f4 v[114:117], v[2:9], v[220:227], v[114:117], v1, v162 op_sel_hi:[0,0,0]
	s_nop 1
	v_mfma_scale_f32_16x16x128_f8f6f4 v[106:109], v[10:17], v[228:235], v[106:109], v1, v162 op_sel_hi:[0,0,0]
	s_nop 1
	v_mfma_scale_f32_16x16x128_f8f6f4 v[98:101], v[2:9], v[228:235], v[98:101], v1, v162 op_sel_hi:[0,0,0]
.Lmy_zjoin_p6_0:
	s_setprio 0
	s_barrier
	v_mov_b32_e32 v166, v163
	s_add_i32 s53, s53, s28
	ds_read_b128 v[204:207], v181 offset:16384
	ds_read_b128 v[208:211], v181 offset:17408
	ds_read_b128 v[212:215], v181 offset:18432
	ds_read_b128 v[216:219], v181 offset:19456
	ds_read_b128 v[220:223], v181 offset:20480
	ds_read_b128 v[224:227], v181 offset:21504
	ds_read_b128 v[228:231], v181 offset:22528
	ds_read_b128 v[232:235], v181 offset:23552
	s_mov_b32 m0, s53
	s_nop 0
	global_load_lds_dwordx4 v166, s[24:25]
	s_add_i32 m0, s53, 0x2000
	s_add_u32 s54, s24, 0x20000
	global_load_lds_dwordx4 v164, s[24:25]
	s_addc_u32 s55, s25, 0
	s_add_i32 s52, s52, s28
	s_mov_b32 m0, s52
	s_nop 0
	global_load_lds_dwordx4 v163, s[54:55]
	s_add_i32 m0, s52, 0x2000
	s_nop 0
	global_load_lds_dwordx4 v164, s[54:55]
	v_mov_b32_e32 v166, v182
	s_mov_b32 m0, s31
	v_lshlrev_b32_e32 v166, 8, v166
	v_and_or_b32 v166, v166, s89, v173
	v_cndmask_b32_e64 v166, v199, v166, s[2:3]
	s_nop 0
	global_load_lds_dwordx4 v166, s[22:23]
	v_mov_b32_e32 v166, v183
	s_mov_b32 m0, s34
	v_lshlrev_b32_e32 v166, 8, v166
	v_and_or_b32 v166, v166, s89, v174
	v_cndmask_b32_e64 v166, v200, v166, s[2:3]
	s_nop 0
	global_load_lds_dwordx4 v166, s[22:23]
	s_waitcnt vmcnt(8)
	s_waitcnt lgkmcnt(0)
	s_barrier
	s_setprio 1
	s_waitcnt lgkmcnt(0)
	s_cmp_eq_u32 s51, -2
	s_cbranch_scc1 .Lmy_zfirst_p6_1
	s_nop 1
	v_mfma_scale_f32_16x16x128_f8f6f4 v[94:97], v[26:33], v[204:211], v[94:97], v1, v162 op_sel_hi:[0,0,0]
	s_nop 1
	v_mfma_scale_f32_16x16x128_f8f6f4 v[86:89], v[18:25], v[204:211], v[86:89], v1, v162 op_sel_hi:[0,0,0]
	s_nop 1
	v_mfma_scale_f32_16x16x128_f8f6f4 v[78:81], v[26:33], v[212:219], v[78:81], v1, v162 op_sel_hi:[0,0,0]
	s_nop 1
	v_mfma_scale_f32_16x16x128_f8f6f4 v[70:73], v[18:25], v[212:219], v[70:73], v1, v162 op_sel_hi:[0,0,0]
	s_nop 1
	v_mfma_scale_f32_16x16x128_f8f6f4 v[62:65], v[26:33], v[220:227], v[62:65], v1, v162 op_sel_hi:[0,0,0]
	s_nop 1
	v_mfma_scale_f32_16x16x128_f8f6f4 v[54:57], v[18:25], v[220:227], v[54:57], v1, v162 op_sel_hi:[0,0,0]
	s_nop 1
	v_mfma_scale_f32_16x16x128_f8f6f4 v[46:49], v[26:33], v[228:235], v[46:49], v1, v162 op_sel_hi:[0,0,0]
	s_nop 1
	v_mfma_scale_f32_16x16x128_f8f6f4 v[38:41], v[18:25], v[228:235], v[38:41], v1, v162 op_sel_hi:[0,0,0]
	s_setprio 0
	s_setprio 1
	s_nop 1
	v_mfma_scale_f32_16x16x128_f8f6f4 v[90:93], v[10:17], v[204:211], v[90:93], v1, v162 op_sel_hi:[0,0,0]
	s_nop 1
	v_mfma_scale_f32_16x16x128_f8f6f4 v[82:85], v[2:9], v[204:211], v[82:85], v1, v162 op_sel_hi:[0,0,0]
	s_nop 1
	v_mfma_scale_f32_16x16x128_f8f6f4 v[74:77], v[10:17], v[212:219], v[74:77], v1, v162 op_sel_hi:[0,0,0]
	s_nop 1
	v_mfma_scale_f32_16x16x128_f8f6f4 v[66:69], v[2:9], v[212:219], v[66:69], v1, v162 op_sel_hi:[0,0,0]
	s_nop 1
	v_mfma_scale_f32_16x16x128_f8f6f4 v[58:61], v[10:17], v[220:227], v[58:61], v1, v162 op_sel_hi:[0,0,0]
	s_nop 1
	v_mfma_scale_f32_16x16x128_f8f6f4 v[50:53], v[2:9], v[220:227], v[50:53], v1, v162 op_sel_hi:[0,0,0]
	s_nop 1
	v_mfma_scale_f32_16x16x128_f8f6f4 v[42:45], v[10:17], v[228:235], v[42:45], v1, v162 op_sel_hi:[0,0,0]
	s_nop 1
	v_mfma_scale_f32_16x16x128_f8f6f4 v[34:37], v[2:9], v[228:235], v[34:37], v1, v162 op_sel_hi:[0,0,0]
.Lmy_zjoin_p6_1:
	s_setprio 0
	s_barrier
	s_add_i32 s53, 0, 0x18000
	s_add_i32 s52, 0, 0x1c000
	v_add_u32_e32 v2, s53, v176
	v_add_u32_e32 v6, s52, v176
	ds_read_b128 v[26:29], v2
	ds_read_b128 v[30:33], v2 offset:1024
	ds_read_b128 v[18:21], v2 offset:2048
	ds_read_b128 v[22:25], v2 offset:3072
	ds_read_b128 v[10:13], v6
	ds_read_b128 v[14:17], v6 offset:1024
	ds_read_b128 v[2:5], v6 offset:2048
	ds_read_b128 v[6:9], v6 offset:3072
	v_mov_b32_e32 v166, v184
	ds_read_b128 v[204:207], v181 offset:32768
	ds_read_b128 v[208:211], v181 offset:33792
	ds_read_b128 v[212:215], v181 offset:34816
	ds_read_b128 v[216:219], v181 offset:35840
	ds_read_b128 v[220:223], v181 offset:36864
	ds_read_b128 v[224:227], v181 offset:37888
	ds_read_b128 v[228:231], v181 offset:38912
	ds_read_b128 v[232:235], v181 offset:39936
	s_mov_b32 m0, s35
	v_lshlrev_b32_e32 v166, 8, v166
	v_and_or_b32 v166, v166, s89, v173
	v_cndmask_b32_e64 v166, v201, v166, s[2:3]
	s_nop 0
	global_load_lds_dwordx4 v166, s[22:23]
	v_mov_b32_e32 v166, v185
	s_mov_b32 m0, s36
	v_lshlrev_b32_e32 v166, 8, v166
	v_and_or_b32 v166, v166, s89, v174
	v_cndmask_b32_e64 v166, v202, v166, s[2:3]
	s_nop 0
	global_load_lds_dwordx4 v166, s[22:23]
	s_waitcnt vmcnt(8)
	s_waitcnt lgkmcnt(0)
	s_barrier
	s_setprio 1
	s_waitcnt lgkmcnt(0)
	s_nop 1
	v_mfma_scale_f32_16x16x128_f8f6f4 v[158:161], v[26:33], v[204:211], v[158:161], v1, v162 op_sel_hi:[0,0,0]
	s_nop 1
	v_mfma_scale_f32_16x16x128_f8f6f4 v[150:153], v[18:25], v[204:211], v[150:153], v1, v162 op_sel_hi:[0,0,0]
	s_nop 1
	v_mfma_scale_f32_16x16x128_f8f6f4 v[142:145], v[26:33], v[212:219], v[142:145], v1, v162 op_sel_hi:[0,0,0]
	s_nop 1
	v_mfma_scale_f32_16x16x128_f8f6f4 v[134:137], v[18:25], v[212:219], v[134:137], v1, v162 op_sel_hi:[0,0,0]
	s_nop 1
	v_mfma_scale_f32_16x16x128_f8f6f4 v[126:129], v[26:33], v[220:227], v[126:129], v1, v162 op_sel_hi:[0,0,0]
	s_nop 1
	v_mfma_scale_f32_16x16x128_f8f6f4 v[118:121], v[18:25], v[220:227], v[118:121], v1, v162 op_sel_hi:[0,0,0]
	s_nop 1
	v_mfma_scale_f32_16x16x128_f8f6f4 v[110:113], v[26:33], v[228:235], v[110:113], v1, v162 op_sel_hi:[0,0,0]
	s_nop 1
	v_mfma_scale_f32_16x16x128_f8f6f4 v[102:105], v[18:25], v[228:235], v[102:105], v1, v162 op_sel_hi:[0,0,0]
	s_setprio 0
	s_setprio 1
	s_nop 1
	v_mfma_scale_f32_16x16x128_f8f6f4 v[154:157], v[10:17], v[204:211], v[154:157], v1, v162 op_sel_hi:[0,0,0]
	s_nop 1
	v_mfma_scale_f32_16x16x128_f8f6f4 v[146:149], v[2:9], v[204:211], v[146:149], v1, v162 op_sel_hi:[0,0,0]
	s_nop 1
	v_mfma_scale_f32_16x16x128_f8f6f4 v[138:141], v[10:17], v[212:219], v[138:141], v1, v162 op_sel_hi:[0,0,0]
	s_nop 1
	v_mfma_scale_f32_16x16x128_f8f6f4 v[130:133], v[2:9], v[212:219], v[130:133], v1, v162 op_sel_hi:[0,0,0]
	s_nop 1
	v_mfma_scale_f32_16x16x128_f8f6f4 v[122:125], v[10:17], v[220:227], v[122:125], v1, v162 op_sel_hi:[0,0,0]
	s_nop 1
	v_mfma_scale_f32_16x16x128_f8f6f4 v[114:117], v[2:9], v[220:227], v[114:117], v1, v162 op_sel_hi:[0,0,0]
	s_nop 1
	v_mfma_scale_f32_16x16x128_f8f6f4 v[106:109], v[10:17], v[228:235], v[106:109], v1, v162 op_sel_hi:[0,0,0]
	s_nop 1
	v_mfma_scale_f32_16x16x128_f8f6f4 v[98:101], v[2:9], v[228:235], v[98:101], v1, v162 op_sel_hi:[0,0,0]
	s_setprio 0
	s_barrier
	v_mov_b32_e32 v166, v163
	ds_read_b128 v[204:207], v181 offset:49152
	ds_read_b128 v[208:211], v181 offset:50176
	ds_read_b128 v[212:215], v181 offset:51200
	ds_read_b128 v[216:219], v181 offset:52224
	ds_read_b128 v[220:223], v181 offset:53248
	ds_read_b128 v[224:227], v181 offset:54272
	ds_read_b128 v[228:231], v181 offset:55296
	ds_read_b128 v[232:235], v181 offset:56320
	s_add_i32 s53, s53, s28
	v_lshl_add_u64 v[236:237], s[24:25], 0, v[166:167]
	v_lshl_add_u64 v[236:237], v[236:237], 0, s[80:81]
	s_mov_b32 m0, s53
	v_mov_b32_e32 v166, v164
	global_load_lds_dwordx4 v[236:237], off
	s_add_i32 m0, s53, 0x2000
	s_nop 0
	v_lshl_add_u64 v[236:237], s[24:25], 0, v[166:167]
	s_add_u32 s24, s24, 0x20080
	v_lshl_add_u64 v[236:237], v[236:237], 0, s[80:81]
	s_addc_u32 s25, s25, 0
	v_mov_b32_e32 v166, v163
	s_add_i32 s52, s52, s28
	global_load_lds_dwordx4 v[236:237], off
	s_mov_b32 m0, s52
	s_nop 0
	global_load_lds_dwordx4 v166, s[24:25]
	s_add_i32 m0, s52, 0x2000
	s_nop 0
	global_load_lds_dwordx4 v164, s[24:25]
	v_mov_b32_e32 v166, v182
	s_mov_b32 m0, s37
	v_lshlrev_b32_e32 v166, 8, v166
	v_and_or_b32 v166, v166, s89, v173
	v_cndmask_b32_e64 v166, v199, v166, s[2:3]
	s_nop 0
	v_lshl_add_u64 v[236:237], s[22:23], 0, v[166:167]
	v_lshl_add_u64 v[236:237], v[236:237], 0, s[80:81]
	v_mov_b32_e32 v166, v183
	global_load_lds_dwordx4 v[236:237], off
	s_mov_b32 m0, s38
	v_lshlrev_b32_e32 v166, 8, v166
	v_and_or_b32 v166, v166, s89, v174
	v_cndmask_b32_e64 v166, v200, v166, s[2:3]
	s_nop 0
	v_lshl_add_u64 v[236:237], s[22:23], 0, v[166:167]
	v_lshl_add_u64 v[236:237], v[236:237], 0, s[80:81]
	global_load_lds_dwordx4 v[236:237], off
	s_waitcnt vmcnt(8)
	s_waitcnt lgkmcnt(0)
	s_barrier
	s_setprio 1
	s_waitcnt lgkmcnt(0)
	s_nop 1
	v_mfma_scale_f32_16x16x128_f8f6f4 v[94:97], v[26:33], v[204:211], v[94:97], v1, v162 op_sel_hi:[0,0,0]
	s_nop 1
	v_mfma_scale_f32_16x16x128_f8f6f4 v[86:89], v[18:25], v[204:211], v[86:89], v1, v162 op_sel_hi:[0,0,0]
	s_nop 1
	v_mfma_scale_f32_16x16x128_f8f6f4 v[78:81], v[26:33], v[212:219], v[78:81], v1, v162 op_sel_hi:[0,0,0]
	s_nop 1
	v_mfma_scale_f32_16x16x128_f8f6f4 v[70:73], v[18:25], v[212:219], v[70:73], v1, v162 op_sel_hi:[0,0,0]
	s_nop 1
	v_mfma_scale_f32_16x16x128_f8f6f4 v[62:65], v[26:33], v[220:227], v[62:65], v1, v162 op_sel_hi:[0,0,0]
	s_nop 1
	v_mfma_scale_f32_16x16x128_f8f6f4 v[54:57], v[18:25], v[220:227], v[54:57], v1, v162 op_sel_hi:[0,0,0]
	s_nop 1
	v_mfma_scale_f32_16x16x128_f8f6f4 v[46:49], v[26:33], v[228:235], v[46:49], v1, v162 op_sel_hi:[0,0,0]
	s_nop 1
	v_mfma_scale_f32_16x16x128_f8f6f4 v[38:41], v[18:25], v[228:235], v[38:41], v1, v162 op_sel_hi:[0,0,0]
	s_setprio 0
	s_setprio 1
	s_nop 1
	v_mfma_scale_f32_16x16x128_f8f6f4 v[90:93], v[10:17], v[204:211], v[90:93], v1, v162 op_sel_hi:[0,0,0]
	s_nop 1
	v_mfma_scale_f32_16x16x128_f8f6f4 v[82:85], v[2:9], v[204:211], v[82:85], v1, v162 op_sel_hi:[0,0,0]
	s_nop 1
	v_mfma_scale_f32_16x16x128_f8f6f4 v[74:77], v[10:17], v[212:219], v[74:77], v1, v162 op_sel_hi:[0,0,0]
	s_nop 1
	v_mfma_scale_f32_16x16x128_f8f6f4 v[66:69], v[2:9], v[212:219], v[66:69], v1, v162 op_sel_hi:[0,0,0]
	s_nop 1
	v_mfma_scale_f32_16x16x128_f8f6f4 v[58:61], v[10:17], v[220:227], v[58:61], v1, v162 op_sel_hi:[0,0,0]
	s_nop 1
	v_mfma_scale_f32_16x16x128_f8f6f4 v[50:53], v[2:9], v[220:227], v[50:53], v1, v162 op_sel_hi:[0,0,0]
	s_nop 1
	v_mfma_scale_f32_16x16x128_f8f6f4 v[42:45], v[10:17], v[228:235], v[42:45], v1, v162 op_sel_hi:[0,0,0]
	s_nop 1
	v_mfma_scale_f32_16x16x128_f8f6f4 v[34:37], v[2:9], v[228:235], v[34:37], v1, v162 op_sel_hi:[0,0,0]
	s_setprio 0
	s_barrier
	s_add_i32 s51, s51, 2
	s_add_u32 s49, s49, 0x100
	s_addc_u32 s50, s50, 0
	s_add_u32 s20, s20, 0x100
	s_addc_u32 s21, s21, 0
	s_cmp_gt_u32 s51, 5
	s_cbranch_scc1 .LBB0_781

.LBB0_783:
	s_add_i32 s2, 0, 0x20000
	s_nop 11
	v_add_u32_e32 v2, s2, v178
	ds_read_b128 v[10:13], v2
	v_readlane_b32 s3, v238, 9
	v_add_u32_e32 v18, s47, v175
	v_ashrrev_i32_e32 v19, 31, v18
	v_add_u32_e32 v6, s3, v179
	ds_read_b128 v[6:9], v6
	s_waitcnt lgkmcnt(0)
	v_pk_add_f32 v[24:25], v[158:159], v[10:11]
	v_pk_add_f32 v[22:23], v[160:161], v[12:13]
	v_min_f32_e32 v25, 0x40e00000, v25
	v_min_f32_e32 v24, 0x40e00000, v24
	v_mul_f32_e32 v30, 0xc01d265f, v24
	v_mul_f32_e32 v31, 0xc01d265f, v25
	v_min_f32_e32 v23, 0x40e00000, v23
	v_min_f32_e32 v22, 0x40e00000, v22
	v_exp_f32_e32 v30, v30
	v_exp_f32_e32 v31, v31
	v_add_u32_e32 v2, s3, v178
	v_mul_f32_e32 v32, 0xc01d265f, v22
	v_mul_f32_e32 v33, 0xc01d265f, v23
	ds_read_b128 v[14:17], v2
	v_exp_f32_e32 v32, v32
	v_exp_f32_e32 v33, v33
	v_pk_add_f32 v[30:31], v[30:31], 1.0 op_sel_hi:[1,0]
	v_add_u32_e32 v2, s2, v179
	v_rcp_f32_e32 v30, v30
	v_rcp_f32_e32 v31, v31
	v_pk_add_f32 v[32:33], v[32:33], 1.0 op_sel_hi:[1,0]
	s_waitcnt lgkmcnt(0)
	v_pk_add_f32 v[28:29], v[154:155], v[14:15]
	v_rcp_f32_e32 v32, v32
	v_rcp_f32_e32 v33, v33
	ds_read_b128 v[2:5], v2
	v_med3_f32 v28, v28, s91, v198
	v_pk_add_f32 v[26:27], v[156:157], v[16:17]
	v_med3_f32 v29, v29, s91, v198
	v_pk_mul_f32 v[24:25], v[24:25], v[30:31]
	v_add_f32_e32 v28, 1.0, v28
	v_med3_f32 v26, v26, s91, v198
	v_mul_f32_e32 v154, v28, v24
	v_add_f32_e32 v24, 1.0, v29
	v_med3_f32 v27, v27, s91, v198
	v_pk_mul_f32 v[22:23], v[22:23], v[32:33]
	v_mul_f32_e32 v155, v24, v25
	v_add_f32_e32 v24, 1.0, v26
	v_mul_f32_e32 v156, v24, v22
	v_add_f32_e32 v22, 1.0, v27
	v_mul_f32_e32 v157, v22, v23
	s_waitcnt lgkmcnt(0)
	v_pk_add_f32 v[22:23], v[152:153], v[4:5]
	v_pk_add_f32 v[24:25], v[150:151], v[2:3]
	v_min_f32_e32 v23, 0x40e00000, v23
	v_min_f32_e32 v22, 0x40e00000, v22
	v_min_f32_e32 v25, 0x40e00000, v25
	v_min_f32_e32 v24, 0x40e00000, v24
	v_mul_f32_e32 v30, 0xc01d265f, v24
	v_mul_f32_e32 v31, 0xc01d265f, v25
	v_mul_f32_e32 v32, 0xc01d265f, v22
	v_mul_f32_e32 v33, 0xc01d265f, v23
	v_exp_f32_e32 v30, v30
	v_exp_f32_e32 v31, v31
	v_exp_f32_e32 v32, v32
	v_exp_f32_e32 v33, v33
	v_pk_add_f32 v[26:27], v[148:149], v[8:9]
	v_pk_add_f32 v[30:31], v[30:31], 1.0 op_sel_hi:[1,0]
	v_pk_add_f32 v[28:29], v[146:147], v[6:7]
	v_pk_add_f32 v[32:33], v[32:33], 1.0 op_sel_hi:[1,0]
	v_rcp_f32_e32 v30, v30
	v_rcp_f32_e32 v31, v31
	v_rcp_f32_e32 v32, v32
	v_rcp_f32_e32 v33, v33
	v_med3_f32 v26, v26, s91, v198
	v_med3_f32 v28, v28, s91, v198
	v_med3_f32 v27, v27, s91, v198
	v_med3_f32 v29, v29, s91, v198
	v_pk_mul_f32 v[22:23], v[22:23], v[32:33]
	v_pk_mul_f32 v[24:25], v[24:25], v[30:31]
	v_add_f32_e32 v28, 1.0, v28
	v_add_f32_e32 v26, 1.0, v26
	v_mul_f32_e32 v24, v28, v24
	v_add_f32_e32 v28, 1.0, v29
	v_mul_f32_e32 v26, v26, v22
	v_add_f32_e32 v22, 1.0, v27
	v_mul_f32_e32 v25, v28, v25
	v_mul_f32_e32 v27, v22, v23
	v_mov_b32_e32 v22, v167
	v_mov_b32_e32 v23, v167
	v_cvt_pk_fp8_f32 v22, v154, v155
	v_cvt_pk_fp8_f32 v23, v24, v25
	v_add_u32_e32 v20, s48, v180
	v_lshlrev_b64 v[18:19], 10, v[18:19]
	v_cvt_pk_fp8_f32 v22, v156, v157 op_sel:[0,0,1]
	v_cvt_pk_fp8_f32 v23, v26, v27 op_sel:[0,0,1]
	v_ashrrev_i32_e32 v21, 31, v20
	v_lshl_add_u64 v[18:19], s[6:7], 0, v[18:19]
	v_lshl_add_u64 v[18:19], v[18:19], 0, v[20:21]
	flat_store_dwordx2 v[18:19], v[22:23]
	v_pk_add_f32 v[22:23], v[142:143], v[10:11]
	v_pk_add_f32 v[20:21], v[144:145], v[12:13]
	v_min_f32_e32 v23, 0x40e00000, v23
	v_min_f32_e32 v22, 0x40e00000, v22
	v_mul_f32_e32 v28, 0xc01d265f, v22
	v_mul_f32_e32 v29, 0xc01d265f, v23
	v_min_f32_e32 v21, 0x40e00000, v21
	v_min_f32_e32 v20, 0x40e00000, v20
	v_exp_f32_e32 v28, v28
	v_exp_f32_e32 v29, v29
	v_mul_f32_e32 v30, 0xc01d265f, v20
	v_mul_f32_e32 v31, 0xc01d265f, v21
	v_exp_f32_e32 v30, v30
	v_exp_f32_e32 v31, v31
	v_pk_add_f32 v[28:29], v[28:29], 1.0 op_sel_hi:[1,0]
	v_pk_add_f32 v[26:27], v[138:139], v[14:15]
	v_rcp_f32_e32 v28, v28
	v_rcp_f32_e32 v29, v29
	v_pk_add_f32 v[30:31], v[30:31], 1.0 op_sel_hi:[1,0]
	v_med3_f32 v26, v26, s91, v198
	v_rcp_f32_e32 v30, v30
	v_rcp_f32_e32 v31, v31
	v_pk_add_f32 v[24:25], v[140:141], v[16:17]
	v_med3_f32 v27, v27, s91, v198
	v_pk_mul_f32 v[22:23], v[22:23], v[28:29]
	v_add_f32_e32 v26, 1.0, v26
	v_med3_f32 v24, v24, s91, v198
	v_mul_f32_e32 v32, v26, v22
	v_add_f32_e32 v22, 1.0, v27
	v_med3_f32 v25, v25, s91, v198
	v_pk_mul_f32 v[20:21], v[20:21], v[30:31]
	v_mul_f32_e32 v33, v22, v23
	v_add_f32_e32 v22, 1.0, v24
	v_mul_f32_e32 v138, v22, v20
	v_add_f32_e32 v20, 1.0, v25
	v_mul_f32_e32 v139, v20, v21
	v_pk_add_f32 v[20:21], v[136:137], v[4:5]
	v_pk_add_f32 v[22:23], v[134:135], v[2:3]
	v_min_f32_e32 v21, 0x40e00000, v21
	v_min_f32_e32 v20, 0x40e00000, v20
	v_min_f32_e32 v23, 0x40e00000, v23
	v_min_f32_e32 v22, 0x40e00000, v22
	v_mul_f32_e32 v28, 0xc01d265f, v22
	v_mul_f32_e32 v29, 0xc01d265f, v23
	v_mul_f32_e32 v30, 0xc01d265f, v20
	v_mul_f32_e32 v31, 0xc01d265f, v21
	v_exp_f32_e32 v28, v28
	v_exp_f32_e32 v29, v29
	v_exp_f32_e32 v30, v30
	v_exp_f32_e32 v31, v31
	v_pk_add_f32 v[24:25], v[132:133], v[8:9]
	v_pk_add_f32 v[28:29], v[28:29], 1.0 op_sel_hi:[1,0]
	v_pk_add_f32 v[26:27], v[130:131], v[6:7]
	v_pk_add_f32 v[30:31], v[30:31], 1.0 op_sel_hi:[1,0]
	v_rcp_f32_e32 v28, v28
	v_rcp_f32_e32 v29, v29
	v_rcp_f32_e32 v30, v30
	v_rcp_f32_e32 v31, v31
	v_med3_f32 v24, v24, s91, v198
	v_med3_f32 v26, v26, s91, v198
	v_med3_f32 v25, v25, s91, v198
	v_med3_f32 v27, v27, s91, v198
	v_pk_mul_f32 v[20:21], v[20:21], v[30:31]
	v_pk_mul_f32 v[22:23], v[22:23], v[28:29]
	v_add_f32_e32 v26, 1.0, v26
	v_add_f32_e32 v24, 1.0, v24
	v_mul_f32_e32 v22, v26, v22
	v_add_f32_e32 v26, 1.0, v27
	v_mul_f32_e32 v24, v24, v20
	v_add_f32_e32 v20, 1.0, v25
	v_mul_f32_e32 v23, v26, v23
	v_mul_f32_e32 v25, v20, v21
	v_mov_b32_e32 v20, v167
	v_mov_b32_e32 v21, v167
	v_cvt_pk_fp8_f32 v20, v32, v33
	v_cvt_pk_fp8_f32 v21, v22, v23
	v_add_co_u32_e32 v22, vcc, s69, v18
	v_cvt_pk_fp8_f32 v20, v138, v139 op_sel:[0,0,1]
	v_cvt_pk_fp8_f32 v21, v24, v25 op_sel:[0,0,1]
	v_addc_co_u32_e32 v23, vcc, 0, v19, vcc
	v_pk_add_f32 v[26:27], v[122:123], v[14:15]
	flat_store_dwordx2 v[22:23], v[20:21]
	v_pk_add_f32 v[22:23], v[126:127], v[10:11]
	v_pk_add_f32 v[20:21], v[128:129], v[12:13]
	v_min_f32_e32 v23, 0x40e00000, v23
	v_min_f32_e32 v22, 0x40e00000, v22
	v_mul_f32_e32 v28, 0xc01d265f, v22
	v_mul_f32_e32 v29, 0xc01d265f, v23
	v_min_f32_e32 v21, 0x40e00000, v21
	v_min_f32_e32 v20, 0x40e00000, v20
	v_exp_f32_e32 v28, v28
	v_exp_f32_e32 v29, v29
	v_mul_f32_e32 v30, 0xc01d265f, v20
	v_mul_f32_e32 v31, 0xc01d265f, v21
	v_exp_f32_e32 v30, v30
	v_exp_f32_e32 v31, v31
	v_pk_add_f32 v[28:29], v[28:29], 1.0 op_sel_hi:[1,0]
	v_med3_f32 v26, v26, s91, v198
	v_rcp_f32_e32 v28, v28
	v_rcp_f32_e32 v29, v29
	v_pk_add_f32 v[30:31], v[30:31], 1.0 op_sel_hi:[1,0]
	v_pk_add_f32 v[24:25], v[124:125], v[16:17]
	v_rcp_f32_e32 v30, v30
	v_rcp_f32_e32 v31, v31
	v_med3_f32 v27, v27, s91, v198
	v_pk_mul_f32 v[22:23], v[22:23], v[28:29]
	v_add_f32_e32 v26, 1.0, v26
	v_med3_f32 v24, v24, s91, v198
	v_mul_f32_e32 v32, v26, v22
	v_add_f32_e32 v22, 1.0, v27
	v_med3_f32 v25, v25, s91, v198
	v_pk_mul_f32 v[20:21], v[20:21], v[30:31]
	v_mul_f32_e32 v33, v22, v23
	v_add_f32_e32 v22, 1.0, v24
	v_mul_f32_e32 v122, v22, v20
	v_add_f32_e32 v20, 1.0, v25
	v_mul_f32_e32 v123, v20, v21
	v_pk_add_f32 v[20:21], v[120:121], v[4:5]
	v_pk_add_f32 v[22:23], v[118:119], v[2:3]
	v_min_f32_e32 v21, 0x40e00000, v21
	v_min_f32_e32 v20, 0x40e00000, v20
	v_min_f32_e32 v23, 0x40e00000, v23
	v_min_f32_e32 v22, 0x40e00000, v22
	v_mul_f32_e32 v28, 0xc01d265f, v22
	v_mul_f32_e32 v29, 0xc01d265f, v23
	v_mul_f32_e32 v30, 0xc01d265f, v20
	v_mul_f32_e32 v31, 0xc01d265f, v21
	v_exp_f32_e32 v28, v28
	v_exp_f32_e32 v29, v29
	v_exp_f32_e32 v30, v30
	v_exp_f32_e32 v31, v31
	v_pk_add_f32 v[24:25], v[116:117], v[8:9]
	v_pk_add_f32 v[28:29], v[28:29], 1.0 op_sel_hi:[1,0]
	v_pk_add_f32 v[26:27], v[114:115], v[6:7]
	v_pk_add_f32 v[30:31], v[30:31], 1.0 op_sel_hi:[1,0]
	v_rcp_f32_e32 v28, v28
	v_rcp_f32_e32 v29, v29
	v_rcp_f32_e32 v30, v30
	v_rcp_f32_e32 v31, v31
	v_med3_f32 v24, v24, s91, v198
	v_med3_f32 v26, v26, s91, v198
	v_med3_f32 v25, v25, s91, v198
	v_med3_f32 v27, v27, s91, v198
	v_pk_mul_f32 v[20:21], v[20:21], v[30:31]
	v_pk_mul_f32 v[22:23], v[22:23], v[28:29]
	v_add_f32_e32 v26, 1.0, v26
	v_add_f32_e32 v24, 1.0, v24
	v_mul_f32_e32 v22, v26, v22
	v_add_f32_e32 v26, 1.0, v27
	v_mul_f32_e32 v24, v24, v20
	v_add_f32_e32 v20, 1.0, v25
	v_mul_f32_e32 v23, v26, v23
	v_mul_f32_e32 v25, v20, v21
	v_mov_b32_e32 v20, v167
	v_mov_b32_e32 v21, v167
	v_cvt_pk_fp8_f32 v20, v32, v33
	v_cvt_pk_fp8_f32 v21, v22, v23
	v_add_co_u32_e32 v22, vcc, s67, v18
	v_cvt_pk_fp8_f32 v20, v122, v123 op_sel:[0,0,1]
	v_cvt_pk_fp8_f32 v21, v24, v25 op_sel:[0,0,1]
	v_addc_co_u32_e32 v23, vcc, 0, v19, vcc
	v_pk_add_f32 v[26:27], v[106:107], v[14:15]
	flat_store_dwordx2 v[22:23], v[20:21]
	v_pk_add_f32 v[22:23], v[110:111], v[10:11]
	v_pk_add_f32 v[20:21], v[112:113], v[12:13]
	v_min_f32_e32 v23, 0x40e00000, v23
	v_min_f32_e32 v22, 0x40e00000, v22
	v_mul_f32_e32 v28, 0xc01d265f, v22
	v_mul_f32_e32 v29, 0xc01d265f, v23
	v_min_f32_e32 v21, 0x40e00000, v21
	v_min_f32_e32 v20, 0x40e00000, v20
	v_exp_f32_e32 v28, v28
	v_exp_f32_e32 v29, v29
	v_mul_f32_e32 v30, 0xc01d265f, v20
	v_mul_f32_e32 v31, 0xc01d265f, v21
	v_exp_f32_e32 v30, v30
	v_exp_f32_e32 v31, v31
	v_pk_add_f32 v[28:29], v[28:29], 1.0 op_sel_hi:[1,0]
	v_med3_f32 v26, v26, s91, v198
	v_rcp_f32_e32 v28, v28
	v_rcp_f32_e32 v29, v29
	v_pk_add_f32 v[30:31], v[30:31], 1.0 op_sel_hi:[1,0]
	v_pk_add_f32 v[24:25], v[108:109], v[16:17]
	v_rcp_f32_e32 v30, v30
	v_rcp_f32_e32 v31, v31
	v_med3_f32 v27, v27, s91, v198
	v_pk_mul_f32 v[22:23], v[22:23], v[28:29]
	v_add_f32_e32 v26, 1.0, v26
	v_med3_f32 v24, v24, s91, v198
	v_mul_f32_e32 v32, v26, v22
	v_add_f32_e32 v22, 1.0, v27
	v_med3_f32 v25, v25, s91, v198
	v_pk_mul_f32 v[20:21], v[20:21], v[30:31]
	v_mul_f32_e32 v33, v22, v23
	v_add_f32_e32 v22, 1.0, v24
	v_mul_f32_e32 v106, v22, v20
	v_add_f32_e32 v20, 1.0, v25
	v_mul_f32_e32 v107, v20, v21
	v_pk_add_f32 v[20:21], v[104:105], v[4:5]
	v_pk_add_f32 v[22:23], v[102:103], v[2:3]
	v_min_f32_e32 v21, 0x40e00000, v21
	v_min_f32_e32 v20, 0x40e00000, v20
	v_min_f32_e32 v23, 0x40e00000, v23
	v_min_f32_e32 v22, 0x40e00000, v22
	v_mul_f32_e32 v28, 0xc01d265f, v22
	v_mul_f32_e32 v29, 0xc01d265f, v23
	v_mul_f32_e32 v30, 0xc01d265f, v20
	v_mul_f32_e32 v31, 0xc01d265f, v21
	v_exp_f32_e32 v28, v28
	v_exp_f32_e32 v29, v29
	v_exp_f32_e32 v30, v30
	v_exp_f32_e32 v31, v31
	v_pk_add_f32 v[24:25], v[100:101], v[8:9]
	v_pk_add_f32 v[28:29], v[28:29], 1.0 op_sel_hi:[1,0]
	v_pk_add_f32 v[26:27], v[98:99], v[6:7]
	v_pk_add_f32 v[30:31], v[30:31], 1.0 op_sel_hi:[1,0]
	v_rcp_f32_e32 v28, v28
	v_rcp_f32_e32 v29, v29
	v_rcp_f32_e32 v30, v30
	v_rcp_f32_e32 v31, v31
	v_med3_f32 v24, v24, s91, v198
	v_med3_f32 v26, v26, s91, v198
	v_med3_f32 v25, v25, s91, v198
	v_med3_f32 v27, v27, s91, v198
	v_pk_mul_f32 v[20:21], v[20:21], v[30:31]
	v_pk_mul_f32 v[22:23], v[22:23], v[28:29]
	v_add_f32_e32 v26, 1.0, v26
	v_add_f32_e32 v24, 1.0, v24
	v_mul_f32_e32 v22, v26, v22
	v_add_f32_e32 v26, 1.0, v27
	v_mul_f32_e32 v24, v24, v20
	v_add_f32_e32 v20, 1.0, v25
	v_mul_f32_e32 v23, v26, v23
	v_mul_f32_e32 v25, v20, v21
	v_mov_b32_e32 v20, v167
	v_mov_b32_e32 v21, v167
	v_cvt_pk_fp8_f32 v20, v32, v33
	v_cvt_pk_fp8_f32 v21, v22, v23
	s_mov_b32 s2, 0xc000
	v_add_co_u32_e32 v22, vcc, s2, v18
	v_cvt_pk_fp8_f32 v20, v106, v107 op_sel:[0,0,1]
	v_cvt_pk_fp8_f32 v21, v24, v25 op_sel:[0,0,1]
	v_addc_co_u32_e32 v23, vcc, 0, v19, vcc
	v_pk_add_f32 v[26:27], v[90:91], v[14:15]
	flat_store_dwordx2 v[22:23], v[20:21]
	v_pk_add_f32 v[22:23], v[94:95], v[10:11]
	v_pk_add_f32 v[20:21], v[96:97], v[12:13]
	v_min_f32_e32 v23, 0x40e00000, v23
	v_min_f32_e32 v22, 0x40e00000, v22
	v_mul_f32_e32 v28, 0xc01d265f, v22
	v_mul_f32_e32 v29, 0xc01d265f, v23
	v_min_f32_e32 v21, 0x40e00000, v21
	v_min_f32_e32 v20, 0x40e00000, v20
	v_exp_f32_e32 v28, v28
	v_exp_f32_e32 v29, v29
	v_mul_f32_e32 v30, 0xc01d265f, v20
	v_mul_f32_e32 v31, 0xc01d265f, v21
	v_exp_f32_e32 v30, v30
	v_exp_f32_e32 v31, v31
	v_pk_add_f32 v[28:29], v[28:29], 1.0 op_sel_hi:[1,0]
	v_med3_f32 v26, v26, s91, v198
	v_rcp_f32_e32 v28, v28
	v_rcp_f32_e32 v29, v29
	v_pk_add_f32 v[30:31], v[30:31], 1.0 op_sel_hi:[1,0]
	v_pk_add_f32 v[24:25], v[92:93], v[16:17]
	v_rcp_f32_e32 v30, v30
	v_rcp_f32_e32 v31, v31
	v_med3_f32 v27, v27, s91, v198
	v_pk_mul_f32 v[22:23], v[22:23], v[28:29]
	v_add_f32_e32 v26, 1.0, v26
	v_med3_f32 v24, v24, s91, v198
	v_mul_f32_e32 v32, v26, v22
	v_add_f32_e32 v22, 1.0, v27
	v_med3_f32 v25, v25, s91, v198
	v_pk_mul_f32 v[20:21], v[20:21], v[30:31]
	v_mul_f32_e32 v33, v22, v23
	v_add_f32_e32 v22, 1.0, v24
	v_mul_f32_e32 v90, v22, v20
	v_add_f32_e32 v20, 1.0, v25
	v_mul_f32_e32 v91, v20, v21
	v_pk_add_f32 v[20:21], v[88:89], v[4:5]
	v_pk_add_f32 v[22:23], v[86:87], v[2:3]
	v_min_f32_e32 v21, 0x40e00000, v21
	v_min_f32_e32 v20, 0x40e00000, v20
	v_min_f32_e32 v23, 0x40e00000, v23
	v_min_f32_e32 v22, 0x40e00000, v22
	v_mul_f32_e32 v28, 0xc01d265f, v22
	v_mul_f32_e32 v29, 0xc01d265f, v23
	v_mul_f32_e32 v30, 0xc01d265f, v20
	v_mul_f32_e32 v31, 0xc01d265f, v21
	v_exp_f32_e32 v28, v28
	v_exp_f32_e32 v29, v29
	v_exp_f32_e32 v30, v30
	v_exp_f32_e32 v31, v31
	v_pk_add_f32 v[24:25], v[84:85], v[8:9]
	v_pk_add_f32 v[28:29], v[28:29], 1.0 op_sel_hi:[1,0]
	v_pk_add_f32 v[26:27], v[82:83], v[6:7]
	v_pk_add_f32 v[30:31], v[30:31], 1.0 op_sel_hi:[1,0]
	v_rcp_f32_e32 v28, v28
	v_rcp_f32_e32 v29, v29
	v_rcp_f32_e32 v30, v30
	v_rcp_f32_e32 v31, v31
	v_med3_f32 v24, v24, s91, v198
	v_med3_f32 v26, v26, s91, v198
	v_med3_f32 v25, v25, s91, v198
	v_med3_f32 v27, v27, s91, v198
	v_pk_mul_f32 v[20:21], v[20:21], v[30:31]
	v_pk_mul_f32 v[22:23], v[22:23], v[28:29]
	v_add_f32_e32 v26, 1.0, v26
	v_add_f32_e32 v24, 1.0, v24
	v_mul_f32_e32 v22, v26, v22
	v_add_f32_e32 v26, 1.0, v27
	v_mul_f32_e32 v24, v24, v20
	v_add_f32_e32 v20, 1.0, v25
	v_mul_f32_e32 v23, v26, v23
	v_mul_f32_e32 v25, v20, v21
	v_mov_b32_e32 v20, v167
	v_mov_b32_e32 v21, v167
	v_cvt_pk_fp8_f32 v20, v32, v33
	v_cvt_pk_fp8_f32 v21, v22, v23
	s_mov_b32 s2, 0x20000
	v_add_co_u32_e32 v22, vcc, s2, v18
	v_cvt_pk_fp8_f32 v20, v90, v91 op_sel:[0,0,1]
	v_cvt_pk_fp8_f32 v21, v24, v25 op_sel:[0,0,1]
	v_addc_co_u32_e32 v23, vcc, 0, v19, vcc
	v_pk_add_f32 v[26:27], v[74:75], v[14:15]
	flat_store_dwordx2 v[22:23], v[20:21]
	v_pk_add_f32 v[22:23], v[78:79], v[10:11]
	v_pk_add_f32 v[20:21], v[80:81], v[12:13]
	v_min_f32_e32 v23, 0x40e00000, v23
	v_min_f32_e32 v22, 0x40e00000, v22
	v_mul_f32_e32 v28, 0xc01d265f, v22
	v_mul_f32_e32 v29, 0xc01d265f, v23
	v_min_f32_e32 v21, 0x40e00000, v21
	v_min_f32_e32 v20, 0x40e00000, v20
	v_exp_f32_e32 v28, v28
	v_exp_f32_e32 v29, v29
	v_mul_f32_e32 v30, 0xc01d265f, v20
	v_mul_f32_e32 v31, 0xc01d265f, v21
	v_exp_f32_e32 v30, v30
	v_exp_f32_e32 v31, v31
	v_pk_add_f32 v[28:29], v[28:29], 1.0 op_sel_hi:[1,0]
	v_med3_f32 v26, v26, s91, v198
	v_rcp_f32_e32 v28, v28
	v_rcp_f32_e32 v29, v29
	v_pk_add_f32 v[30:31], v[30:31], 1.0 op_sel_hi:[1,0]
	v_pk_add_f32 v[24:25], v[76:77], v[16:17]
	v_rcp_f32_e32 v30, v30
	v_rcp_f32_e32 v31, v31
	v_med3_f32 v27, v27, s91, v198
	v_pk_mul_f32 v[22:23], v[22:23], v[28:29]
	v_add_f32_e32 v26, 1.0, v26
	v_med3_f32 v24, v24, s91, v198
	v_mul_f32_e32 v32, v26, v22
	v_add_f32_e32 v22, 1.0, v27
	v_med3_f32 v25, v25, s91, v198
	v_pk_mul_f32 v[20:21], v[20:21], v[30:31]
	v_mul_f32_e32 v33, v22, v23
	v_add_f32_e32 v22, 1.0, v24
	v_mul_f32_e32 v74, v22, v20
	v_add_f32_e32 v20, 1.0, v25
	v_mul_f32_e32 v75, v20, v21
	v_pk_add_f32 v[20:21], v[72:73], v[4:5]
	v_pk_add_f32 v[22:23], v[70:71], v[2:3]
	v_min_f32_e32 v21, 0x40e00000, v21
	v_min_f32_e32 v20, 0x40e00000, v20
	v_min_f32_e32 v23, 0x40e00000, v23
	v_min_f32_e32 v22, 0x40e00000, v22
	v_mul_f32_e32 v28, 0xc01d265f, v22
	v_mul_f32_e32 v29, 0xc01d265f, v23
	v_mul_f32_e32 v30, 0xc01d265f, v20
	v_mul_f32_e32 v31, 0xc01d265f, v21
	v_exp_f32_e32 v28, v28
	v_exp_f32_e32 v29, v29
	v_exp_f32_e32 v30, v30
	v_exp_f32_e32 v31, v31
	v_pk_add_f32 v[24:25], v[68:69], v[8:9]
	v_pk_add_f32 v[28:29], v[28:29], 1.0 op_sel_hi:[1,0]
	v_pk_add_f32 v[26:27], v[66:67], v[6:7]
	v_pk_add_f32 v[30:31], v[30:31], 1.0 op_sel_hi:[1,0]
	v_rcp_f32_e32 v28, v28
	v_rcp_f32_e32 v29, v29
	v_rcp_f32_e32 v30, v30
	v_rcp_f32_e32 v31, v31
	v_med3_f32 v24, v24, s91, v198
	v_med3_f32 v26, v26, s91, v198
	v_med3_f32 v25, v25, s91, v198
	v_med3_f32 v27, v27, s91, v198
	v_pk_mul_f32 v[20:21], v[20:21], v[30:31]
	v_pk_mul_f32 v[22:23], v[22:23], v[28:29]
	v_add_f32_e32 v26, 1.0, v26
	v_add_f32_e32 v24, 1.0, v24
	v_mul_f32_e32 v22, v26, v22
	v_add_f32_e32 v26, 1.0, v27
	v_mul_f32_e32 v24, v24, v20
	v_add_f32_e32 v20, 1.0, v25
	v_mul_f32_e32 v23, v26, v23
	v_mul_f32_e32 v25, v20, v21
	v_mov_b32_e32 v20, v167
	v_mov_b32_e32 v21, v167
	v_cvt_pk_fp8_f32 v20, v32, v33
	v_cvt_pk_fp8_f32 v21, v22, v23
	s_mov_b32 s2, 0x24000
	v_add_co_u32_e32 v22, vcc, s2, v18
	v_cvt_pk_fp8_f32 v20, v74, v75 op_sel:[0,0,1]
	v_cvt_pk_fp8_f32 v21, v24, v25 op_sel:[0,0,1]
	v_addc_co_u32_e32 v23, vcc, 0, v19, vcc
	v_pk_add_f32 v[26:27], v[58:59], v[14:15]
	flat_store_dwordx2 v[22:23], v[20:21]
	v_pk_add_f32 v[22:23], v[62:63], v[10:11]
	v_pk_add_f32 v[20:21], v[64:65], v[12:13]
	v_min_f32_e32 v23, 0x40e00000, v23
	v_min_f32_e32 v22, 0x40e00000, v22
	v_mul_f32_e32 v28, 0xc01d265f, v22
	v_mul_f32_e32 v29, 0xc01d265f, v23
	v_min_f32_e32 v21, 0x40e00000, v21
	v_min_f32_e32 v20, 0x40e00000, v20
	v_exp_f32_e32 v28, v28
	v_exp_f32_e32 v29, v29
	v_mul_f32_e32 v30, 0xc01d265f, v20
	v_mul_f32_e32 v31, 0xc01d265f, v21
	v_exp_f32_e32 v30, v30
	v_exp_f32_e32 v31, v31
	v_pk_add_f32 v[28:29], v[28:29], 1.0 op_sel_hi:[1,0]
	v_med3_f32 v26, v26, s91, v198
	v_rcp_f32_e32 v28, v28
	v_rcp_f32_e32 v29, v29
	v_pk_add_f32 v[30:31], v[30:31], 1.0 op_sel_hi:[1,0]
	v_pk_add_f32 v[24:25], v[60:61], v[16:17]
	v_rcp_f32_e32 v30, v30
	v_rcp_f32_e32 v31, v31
	v_med3_f32 v27, v27, s91, v198
	v_pk_mul_f32 v[22:23], v[22:23], v[28:29]
	v_add_f32_e32 v26, 1.0, v26
	v_med3_f32 v24, v24, s91, v198
	v_mul_f32_e32 v32, v26, v22
	v_add_f32_e32 v22, 1.0, v27
	v_med3_f32 v25, v25, s91, v198
	v_pk_mul_f32 v[20:21], v[20:21], v[30:31]
	v_mul_f32_e32 v33, v22, v23
	v_add_f32_e32 v22, 1.0, v24
	v_mul_f32_e32 v58, v22, v20
	v_add_f32_e32 v20, 1.0, v25
	v_mul_f32_e32 v59, v20, v21
	v_pk_add_f32 v[20:21], v[56:57], v[4:5]
	v_pk_add_f32 v[22:23], v[54:55], v[2:3]
	v_min_f32_e32 v21, 0x40e00000, v21
	v_min_f32_e32 v20, 0x40e00000, v20
	v_min_f32_e32 v23, 0x40e00000, v23
	v_min_f32_e32 v22, 0x40e00000, v22
	v_mul_f32_e32 v28, 0xc01d265f, v22
	v_mul_f32_e32 v29, 0xc01d265f, v23
	v_mul_f32_e32 v30, 0xc01d265f, v20
	v_mul_f32_e32 v31, 0xc01d265f, v21
	v_exp_f32_e32 v28, v28
	v_exp_f32_e32 v29, v29
	v_exp_f32_e32 v30, v30
	v_exp_f32_e32 v31, v31
	v_pk_add_f32 v[24:25], v[52:53], v[8:9]
	v_pk_add_f32 v[28:29], v[28:29], 1.0 op_sel_hi:[1,0]
	v_pk_add_f32 v[26:27], v[50:51], v[6:7]
	v_pk_add_f32 v[30:31], v[30:31], 1.0 op_sel_hi:[1,0]
	v_rcp_f32_e32 v28, v28
	v_rcp_f32_e32 v29, v29
	v_rcp_f32_e32 v30, v30
	v_rcp_f32_e32 v31, v31
	v_med3_f32 v24, v24, s91, v198
	v_med3_f32 v26, v26, s91, v198
	v_med3_f32 v25, v25, s91, v198
	v_med3_f32 v27, v27, s91, v198
	v_pk_mul_f32 v[20:21], v[20:21], v[30:31]
	v_pk_mul_f32 v[22:23], v[22:23], v[28:29]
	v_add_f32_e32 v26, 1.0, v26
	v_add_f32_e32 v24, 1.0, v24
	v_mul_f32_e32 v22, v26, v22
	v_add_f32_e32 v26, 1.0, v27
	v_mul_f32_e32 v24, v24, v20
	v_add_f32_e32 v20, 1.0, v25
	v_mul_f32_e32 v23, v26, v23
	v_mul_f32_e32 v25, v20, v21
	v_mov_b32_e32 v20, v167
	v_mov_b32_e32 v21, v167
	v_cvt_pk_fp8_f32 v20, v32, v33
	v_cvt_pk_fp8_f32 v21, v22, v23
	s_mov_b32 s2, 0x28000
	v_add_co_u32_e32 v22, vcc, s2, v18
	v_cvt_pk_fp8_f32 v20, v58, v59 op_sel:[0,0,1]
	v_cvt_pk_fp8_f32 v21, v24, v25 op_sel:[0,0,1]
	v_pk_add_f32 v[10:11], v[46:47], v[10:11]
	v_addc_co_u32_e32 v23, vcc, 0, v19, vcc
	v_min_f32_e32 v11, 0x40e00000, v11
	v_min_f32_e32 v10, 0x40e00000, v10
	flat_store_dwordx2 v[22:23], v[20:21]
	v_pk_add_f32 v[12:13], v[48:49], v[12:13]
	v_mul_f32_e32 v20, 0xc01d265f, v10
	v_mul_f32_e32 v21, 0xc01d265f, v11
	v_min_f32_e32 v13, 0x40e00000, v13
	v_min_f32_e32 v12, 0x40e00000, v12
	v_exp_f32_e32 v20, v20
	v_exp_f32_e32 v21, v21
	v_mul_f32_e32 v22, 0xc01d265f, v12
	v_mul_f32_e32 v23, 0xc01d265f, v13
	v_exp_f32_e32 v22, v22
	v_exp_f32_e32 v23, v23
	v_pk_add_f32 v[20:21], v[20:21], 1.0 op_sel_hi:[1,0]
	v_pk_add_f32 v[14:15], v[42:43], v[14:15]
	v_rcp_f32_e32 v20, v20
	v_rcp_f32_e32 v21, v21
	v_pk_add_f32 v[22:23], v[22:23], 1.0 op_sel_hi:[1,0]
	v_med3_f32 v14, v14, s91, v198
	v_rcp_f32_e32 v22, v22
	v_rcp_f32_e32 v23, v23
	v_pk_add_f32 v[16:17], v[44:45], v[16:17]
	v_med3_f32 v15, v15, s91, v198
	v_pk_mul_f32 v[10:11], v[10:11], v[20:21]
	v_add_f32_e32 v14, 1.0, v14
	v_med3_f32 v16, v16, s91, v198
	v_mul_f32_e32 v14, v14, v10
	v_add_f32_e32 v10, 1.0, v15
	v_med3_f32 v17, v17, s91, v198
	v_pk_mul_f32 v[12:13], v[12:13], v[22:23]
	v_mul_f32_e32 v15, v10, v11
	v_add_f32_e32 v10, 1.0, v16
	v_pk_add_f32 v[2:3], v[38:39], v[2:3]
	v_mul_f32_e32 v16, v10, v12
	v_add_f32_e32 v10, 1.0, v17
	v_min_f32_e32 v3, 0x40e00000, v3
	v_min_f32_e32 v2, 0x40e00000, v2
	v_mul_f32_e32 v17, v10, v13
	v_pk_add_f32 v[4:5], v[40:41], v[4:5]
	v_mul_f32_e32 v10, 0xc01d265f, v2
	v_mul_f32_e32 v11, 0xc01d265f, v3
	v_min_f32_e32 v5, 0x40e00000, v5
	v_min_f32_e32 v4, 0x40e00000, v4
	v_exp_f32_e32 v10, v10
	v_exp_f32_e32 v11, v11
	v_mul_f32_e32 v12, 0xc01d265f, v4
	v_mul_f32_e32 v13, 0xc01d265f, v5
	v_exp_f32_e32 v12, v12
	v_exp_f32_e32 v13, v13
	v_pk_add_f32 v[10:11], v[10:11], 1.0 op_sel_hi:[1,0]
	v_pk_add_f32 v[6:7], v[34:35], v[6:7]
	v_rcp_f32_e32 v10, v10
	v_rcp_f32_e32 v11, v11
	v_pk_add_f32 v[12:13], v[12:13], 1.0 op_sel_hi:[1,0]
	v_med3_f32 v6, v6, s91, v198
	v_rcp_f32_e32 v12, v12
	v_rcp_f32_e32 v13, v13
	v_pk_add_f32 v[8:9], v[36:37], v[8:9]
	v_med3_f32 v7, v7, s91, v198
	v_pk_mul_f32 v[2:3], v[2:3], v[10:11]
	v_add_f32_e32 v6, 1.0, v6
	v_med3_f32 v8, v8, s91, v198
	v_mul_f32_e32 v6, v6, v2
	v_add_f32_e32 v2, 1.0, v7
	v_med3_f32 v9, v9, s91, v198
	v_pk_mul_f32 v[4:5], v[4:5], v[12:13]
	v_mul_f32_e32 v7, v2, v3
	v_add_f32_e32 v2, 1.0, v8
	v_mul_f32_e32 v4, v2, v4
	v_add_f32_e32 v2, 1.0, v9
	v_mul_f32_e32 v5, v2, v5
	v_mov_b32_e32 v2, v167
	v_mov_b32_e32 v3, v167
	v_cvt_pk_fp8_f32 v2, v14, v15
	v_cvt_pk_fp8_f32 v3, v6, v7
	s_mov_b64 s[2:3], -1
	v_cvt_pk_fp8_f32 v2, v16, v17 op_sel:[0,0,1]
	v_cvt_pk_fp8_f32 v3, v4, v5 op_sel:[0,0,1]
	v_add_co_u32_e32 v4, vcc, 0x2c000, v18
	s_nop 1
	v_addc_co_u32_e32 v5, vcc, 0, v19, vcc
	s_andn2_b64 vcc, exec, s[14:15]
	flat_store_dwordx2 v[4:5], v[2:3]
	s_cbranch_vccnz .LBB0_772
	s_andn2_b64 vcc, exec, s[4:5]
	s_cbranch_vccnz .LBB0_771
	s_barrier
	s_branch .LBB0_771

.LBB0_858:
	s_andn2_b64 vcc, exec, s[8:9]
	s_cbranch_vccnz .LBB0_896
	v_bfe_i32 v5, v2, 27, 1
	v_lshlrev_b32_e32 v3, 4, v2
	v_lshrrev_b32_e32 v5, 22, v5
	v_add_u32_e32 v5, v3, v5
	v_and_b32_e32 v5, 0xfffffc00, v5
	v_sub_u32_e32 v5, v3, v5
	v_ashrrev_i32_e32 v4, 31, v2
	v_lshrrev_b32_e32 v6, 4, v5
	v_lshrrev_b32_e32 v4, 26, v4
	v_bitop3_b32 v6, v6, v5, 32 bitop3:0x6c
	v_ashrrev_i32_e32 v5, 31, v5
	v_add_u32_e32 v4, v2, v4
	v_lshrrev_b32_e32 v5, 26, v5
	v_ashrrev_i32_e32 v4, 6, v4
	v_add_u32_e32 v5, v6, v5
	v_lshlrev_b32_e32 v7, 3, v4
	v_ashrrev_i32_e32 v5, 6, v5
	v_and_b32_e32 v7, -16, v7
	v_mul_i32_i24_e32 v8, 64, v5
	v_add_u32_e32 v7, v5, v7
	v_sub_u32_e32 v6, v6, v8
	s_add_u32 s30, s0, 0x8200000
	v_lshlrev_b32_e32 v4, 5, v4
	v_ashrrev_i16_sdwa v6, v188, sext(v6) dst_sel:DWORD dst_unused:UNUSED_PAD src0_sel:DWORD src1_sel:BYTE_0
	v_lshlrev_b32_e32 v8, 1, v7
	v_lshrrev_b32_e32 v9, 2, v7
	v_and_b32_e32 v5, 3, v5
	s_mov_b32 s0, 0x3fffe0
	v_and_b32_e32 v4, 32, v4
	v_bfe_i32 v6, v6, 0, 16
	v_and_b32_e32 v8, 24, v8
	v_and_b32_e32 v9, 4, v9
	v_and_or_b32 v5, v7, s0, v5
	v_or3_b32 v5, v5, v9, v8
	v_add_lshl_u32 v4, v4, v6, 1
	v_add_u32_e32 v3, 0x2000, v3
	v_lshl_add_u32 v173, v7, 10, v4
	v_lshl_add_u32 v174, v5, 10, v4
	v_ashrrev_i32_e32 v4, 31, v3
	v_lshrrev_b32_e32 v4, 22, v4
	v_add_u32_e32 v4, v3, v4
	v_ashrrev_i32_e32 v4, 10, v4
	v_mul_i32_i24_e32 v5, 0x400, v4
	v_sub_u32_e32 v3, v3, v5
	v_lshrrev_b32_e32 v5, 4, v3
	v_bitop3_b32 v3, v5, v3, 32 bitop3:0x6c
	v_ashrrev_i32_e32 v6, 31, v3
	v_lshrrev_b32_e32 v6, 26, v6
	v_lshlrev_b32_e32 v5, 3, v4
	v_add_u32_e32 v6, v3, v6
	v_and_b32_e32 v5, -16, v5
	v_ashrrev_i32_e32 v7, 6, v6
	v_and_b32_e32 v6, 0xc0, v6
	v_add_u32_e32 v5, v7, v5
	v_sub_u32_e32 v3, v3, v6
	v_lshlrev_b32_e32 v4, 5, v4
	v_ashrrev_i16_sdwa v3, v188, sext(v3) dst_sel:DWORD dst_unused:UNUSED_PAD src0_sel:DWORD src1_sel:BYTE_0
	v_lshlrev_b32_e32 v6, 1, v5
	v_lshrrev_b32_e32 v8, 2, v5
	v_and_b32_e32 v7, 3, v7
	s_addc_u32 s31, s1, 0
	s_ashr_i32 s8, s10, 6
	v_and_b32_e32 v4, 32, v4
	v_bfe_i32 v3, v3, 0, 16
	v_and_b32_e32 v6, 24, v6
	v_and_b32_e32 v8, 4, v8
	v_and_or_b32 v7, v5, s0, v7
	v_or3_b32 v6, v7, v8, v6
	v_add_lshl_u32 v3, v4, v3, 1
	s_lshl_b32 s34, s8, 10
	v_lshl_add_u32 v175, v5, 10, v3
	v_lshl_add_u32 v176, v6, 10, v3
	s_add_i32 s35, s34, 0
	v_mov_b32_e32 v3, v174
	s_add_i32 m0, s35, 0x10000
	s_ashr_i32 s9, s10, 8
	global_load_lds_dwordx4 v3, s[22:23]
	s_add_i32 m0, s35, 0x12000
	s_add_u32 s0, s22, 0x20000
	global_load_lds_dwordx4 v176, s[22:23]
	s_addc_u32 s1, s23, 0
	s_add_i32 m0, s35, 0x14000
	s_nop 0
	global_load_lds_dwordx4 v174, s[0:1]
	s_add_i32 m0, s35, 0x16000
	s_add_u32 s24, s30, s6
	global_load_lds_dwordx4 v176, s[0:1]
	s_addc_u32 s25, s31, s7
	s_mov_b32 m0, s35
	s_add_i32 s36, s35, 0x2000
	global_load_lds_dwordx4 v173, s[24:25]
	s_mov_b32 m0, s36
	s_add_u32 s0, s24, 0x20000
	global_load_lds_dwordx4 v175, s[24:25]
	s_addc_u32 s1, s25, 0
	s_add_i32 s37, s35, 0x4000
	s_mov_b32 m0, s37
	s_add_i32 s38, s35, 0x6000
	global_load_lds_dwordx4 v173, s[0:1]
	v_mov_b32_e32 v3, v175
	s_mov_b32 m0, s38
	s_cmp_eq_u32 s9, 1
	global_load_lds_dwordx4 v3, s[0:1]
	s_cselect_b64 s[0:1], -1, 0
	s_cmp_lg_u32 s9, 1
	s_cbranch_scc1 .LBB0_861
	s_barrier

.Lmy_zjoin_p7_0:
	s_setprio 0
	s_barrier
	v_mov_b32_e32 v166, v174
	s_add_i32 s59, s59, s34
	ds_read_b128 v[204:207], v202 offset:16384
	ds_read_b128 v[208:211], v202 offset:17408
	ds_read_b128 v[212:215], v202 offset:18432
	ds_read_b128 v[216:219], v202 offset:19456
	ds_read_b128 v[220:223], v202 offset:20480
	ds_read_b128 v[224:227], v202 offset:21504
	ds_read_b128 v[228:231], v202 offset:22528
	ds_read_b128 v[232:235], v202 offset:23552
	s_mov_b32 m0, s59
	s_nop 0
	global_load_lds_dwordx4 v166, s[26:27]
	s_add_i32 m0, s59, 0x2000
	s_add_u32 s60, s26, 0x20000
	global_load_lds_dwordx4 v176, s[26:27]
	s_addc_u32 s61, s27, 0
	s_add_i32 s58, s58, s34
	s_mov_b32 m0, s58
	s_nop 0
	global_load_lds_dwordx4 v174, s[60:61]
	s_add_i32 m0, s58, 0x2000
	s_nop 0
	global_load_lds_dwordx4 v176, s[60:61]
	s_mov_b32 m0, s35
	s_nop 0
	global_load_lds_dwordx4 v173, s[24:25]
	v_mov_b32_e32 v166, v175
	s_mov_b32 m0, s36
	s_nop 0
	global_load_lds_dwordx4 v166, s[24:25]
	s_waitcnt vmcnt(8)
	s_waitcnt lgkmcnt(0)
	s_barrier
	s_setprio 1
	s_waitcnt lgkmcnt(0)
	s_cmp_eq_u32 s57, -2
	s_cbranch_scc1 .Lmy_zfirst_p7_1
	s_nop 1
	v_mfma_scale_f32_16x16x128_f8f6f4 v[94:97], v[26:33], v[204:211], v[94:97], v1, v172 op_sel_hi:[0,0,0]
	s_nop 1
	v_mfma_scale_f32_16x16x128_f8f6f4 v[90:93], v[18:25], v[204:211], v[90:93], v1, v172 op_sel_hi:[0,0,0]
	s_nop 1
	v_mfma_scale_f32_16x16x128_f8f6f4 v[78:81], v[26:33], v[212:219], v[78:81], v1, v172 op_sel_hi:[0,0,0]
	s_nop 1
	v_mfma_scale_f32_16x16x128_f8f6f4 v[74:77], v[18:25], v[212:219], v[74:77], v1, v172 op_sel_hi:[0,0,0]
	s_nop 1
	v_mfma_scale_f32_16x16x128_f8f6f4 v[62:65], v[26:33], v[220:227], v[62:65], v1, v172 op_sel_hi:[0,0,0]
	s_nop 1
	v_mfma_scale_f32_16x16x128_f8f6f4 v[58:61], v[18:25], v[220:227], v[58:61], v1, v172 op_sel_hi:[0,0,0]
	s_nop 1
	v_mfma_scale_f32_16x16x128_f8f6f4 v[46:49], v[26:33], v[228:235], v[46:49], v1, v172 op_sel_hi:[0,0,0]
	s_nop 1
	v_mfma_scale_f32_16x16x128_f8f6f4 v[42:45], v[18:25], v[228:235], v[42:45], v1, v172 op_sel_hi:[0,0,0]
	s_setprio 0
	s_setprio 1
	s_nop 1
	v_mfma_scale_f32_16x16x128_f8f6f4 v[86:89], v[10:17], v[204:211], v[86:89], v1, v172 op_sel_hi:[0,0,0]
	s_nop 1
	v_mfma_scale_f32_16x16x128_f8f6f4 v[82:85], v[2:9], v[204:211], v[82:85], v1, v172 op_sel_hi:[0,0,0]
	s_nop 1
	v_mfma_scale_f32_16x16x128_f8f6f4 v[70:73], v[10:17], v[212:219], v[70:73], v1, v172 op_sel_hi:[0,0,0]
	s_nop 1
	v_mfma_scale_f32_16x16x128_f8f6f4 v[66:69], v[2:9], v[212:219], v[66:69], v1, v172 op_sel_hi:[0,0,0]
	s_nop 1
	v_mfma_scale_f32_16x16x128_f8f6f4 v[54:57], v[10:17], v[220:227], v[54:57], v1, v172 op_sel_hi:[0,0,0]
	s_nop 1
	v_mfma_scale_f32_16x16x128_f8f6f4 v[50:53], v[2:9], v[220:227], v[50:53], v1, v172 op_sel_hi:[0,0,0]
	s_nop 1
	v_mfma_scale_f32_16x16x128_f8f6f4 v[38:41], v[10:17], v[228:235], v[38:41], v1, v172 op_sel_hi:[0,0,0]
	s_nop 1
	v_mfma_scale_f32_16x16x128_f8f6f4 v[34:37], v[2:9], v[228:235], v[34:37], v1, v172 op_sel_hi:[0,0,0]
.Lmy_zjoin_p7_1:
	s_setprio 0
	s_barrier
	s_add_i32 s59, 0, 0x18000
	s_add_i32 s58, 0, 0x1c000
	v_add_u32_e32 v2, s59, v178
	v_add_u32_e32 v6, s58, v178
	ds_read_b128 v[26:29], v2
	ds_read_b128 v[30:33], v2 offset:1024
	ds_read_b128 v[18:21], v2 offset:2048
	ds_read_b128 v[22:25], v2 offset:3072
	ds_read_b128 v[10:13], v6
	ds_read_b128 v[14:17], v6 offset:1024
	ds_read_b128 v[2:5], v6 offset:2048
	ds_read_b128 v[6:9], v6 offset:3072
	s_add_u32 s60, s24, 0x20000
	v_mov_b32_e32 v166, v173
	s_mov_b32 m0, s37
	ds_read_b128 v[204:207], v202 offset:32768
	ds_read_b128 v[208:211], v202 offset:33792
	ds_read_b128 v[212:215], v202 offset:34816
	ds_read_b128 v[216:219], v202 offset:35840
	ds_read_b128 v[220:223], v202 offset:36864
	ds_read_b128 v[224:227], v202 offset:37888
	ds_read_b128 v[228:231], v202 offset:38912
	ds_read_b128 v[232:235], v202 offset:39936
	s_addc_u32 s61, s25, 0
	s_nop 0
	global_load_lds_dwordx4 v166, s[60:61]
	s_mov_b32 m0, s38
	s_nop 0
	global_load_lds_dwordx4 v175, s[60:61]
	s_waitcnt vmcnt(8)
	s_waitcnt lgkmcnt(0)
	s_barrier
	s_setprio 1
	s_waitcnt lgkmcnt(0)
	s_nop 1
	v_mfma_scale_f32_16x16x128_f8f6f4 v[158:161], v[26:33], v[204:211], v[158:161], v1, v172 op_sel_hi:[0,0,0]
	s_nop 1
	v_mfma_scale_f32_16x16x128_f8f6f4 v[154:157], v[18:25], v[204:211], v[154:157], v1, v172 op_sel_hi:[0,0,0]
	s_nop 1
	v_mfma_scale_f32_16x16x128_f8f6f4 v[142:145], v[26:33], v[212:219], v[142:145], v1, v172 op_sel_hi:[0,0,0]
	s_nop 1
	v_mfma_scale_f32_16x16x128_f8f6f4 v[138:141], v[18:25], v[212:219], v[138:141], v1, v172 op_sel_hi:[0,0,0]
	s_nop 1
	v_mfma_scale_f32_16x16x128_f8f6f4 v[126:129], v[26:33], v[220:227], v[126:129], v1, v172 op_sel_hi:[0,0,0]
	s_nop 1
	v_mfma_scale_f32_16x16x128_f8f6f4 v[122:125], v[18:25], v[220:227], v[122:125], v1, v172 op_sel_hi:[0,0,0]
	s_nop 1
	v_mfma_scale_f32_16x16x128_f8f6f4 v[110:113], v[26:33], v[228:235], v[110:113], v1, v172 op_sel_hi:[0,0,0]
	s_nop 1
	v_mfma_scale_f32_16x16x128_f8f6f4 v[106:109], v[18:25], v[228:235], v[106:109], v1, v172 op_sel_hi:[0,0,0]
	s_setprio 0
	s_setprio 1
	s_nop 1
	v_mfma_scale_f32_16x16x128_f8f6f4 v[150:153], v[10:17], v[204:211], v[150:153], v1, v172 op_sel_hi:[0,0,0]
	s_nop 1
	v_mfma_scale_f32_16x16x128_f8f6f4 v[146:149], v[2:9], v[204:211], v[146:149], v1, v172 op_sel_hi:[0,0,0]
	s_nop 1
	v_mfma_scale_f32_16x16x128_f8f6f4 v[134:137], v[10:17], v[212:219], v[134:137], v1, v172 op_sel_hi:[0,0,0]
	s_nop 1
	v_mfma_scale_f32_16x16x128_f8f6f4 v[130:133], v[2:9], v[212:219], v[130:133], v1, v172 op_sel_hi:[0,0,0]
	s_nop 1
	v_mfma_scale_f32_16x16x128_f8f6f4 v[118:121], v[10:17], v[220:227], v[118:121], v1, v172 op_sel_hi:[0,0,0]
	s_nop 1
	v_mfma_scale_f32_16x16x128_f8f6f4 v[114:117], v[2:9], v[220:227], v[114:117], v1, v172 op_sel_hi:[0,0,0]
	s_nop 1
	v_mfma_scale_f32_16x16x128_f8f6f4 v[102:105], v[10:17], v[228:235], v[102:105], v1, v172 op_sel_hi:[0,0,0]
	s_nop 1
	v_mfma_scale_f32_16x16x128_f8f6f4 v[98:101], v[2:9], v[228:235], v[98:101], v1, v172 op_sel_hi:[0,0,0]
	s_setprio 0
	s_barrier
	v_mov_b32_e32 v166, v174
	ds_read_b128 v[204:207], v202 offset:49152
	ds_read_b128 v[208:211], v202 offset:50176
	ds_read_b128 v[212:215], v202 offset:51200
	ds_read_b128 v[216:219], v202 offset:52224
	ds_read_b128 v[220:223], v202 offset:53248
	ds_read_b128 v[224:227], v202 offset:54272
	ds_read_b128 v[228:231], v202 offset:55296
	ds_read_b128 v[232:235], v202 offset:56320
	s_add_i32 s59, s59, s34
	v_lshl_add_u64 v[236:237], s[26:27], 0, v[166:167]
	v_lshl_add_u64 v[236:237], v[236:237], 0, s[80:81]
	s_mov_b32 m0, s59
	v_mov_b32_e32 v166, v176
	global_load_lds_dwordx4 v[236:237], off
	s_add_i32 m0, s59, 0x2000
	s_nop 0
	v_lshl_add_u64 v[236:237], s[26:27], 0, v[166:167]
	s_add_u32 s26, s26, 0x20080
	v_lshl_add_u64 v[236:237], v[236:237], 0, s[80:81]
	s_addc_u32 s27, s27, 0
	v_mov_b32_e32 v166, v174
	s_add_i32 s58, s58, s34
	global_load_lds_dwordx4 v[236:237], off
	s_mov_b32 m0, s58
	s_nop 0
	global_load_lds_dwordx4 v166, s[26:27]
	s_add_i32 m0, s58, 0x2000
	s_nop 0
	global_load_lds_dwordx4 v176, s[26:27]
	v_mov_b32_e32 v166, v173
	s_mov_b32 m0, s44
	v_lshl_add_u64 v[236:237], s[24:25], 0, v[166:167]
	v_lshl_add_u64 v[236:237], v[236:237], 0, s[80:81]
	v_mov_b32_e32 v166, v175
	global_load_lds_dwordx4 v[236:237], off
	s_mov_b32 m0, s45
	v_lshl_add_u64 v[236:237], s[24:25], 0, v[166:167]
	v_lshl_add_u64 v[236:237], v[236:237], 0, s[80:81]
	global_load_lds_dwordx4 v[236:237], off
	s_waitcnt vmcnt(8)
	s_waitcnt lgkmcnt(0)
	s_barrier
	s_setprio 1
	s_waitcnt lgkmcnt(0)
	s_nop 1
	v_mfma_scale_f32_16x16x128_f8f6f4 v[94:97], v[26:33], v[204:211], v[94:97], v1, v172 op_sel_hi:[0,0,0]
	s_nop 1
	v_mfma_scale_f32_16x16x128_f8f6f4 v[90:93], v[18:25], v[204:211], v[90:93], v1, v172 op_sel_hi:[0,0,0]
	s_nop 1
	v_mfma_scale_f32_16x16x128_f8f6f4 v[78:81], v[26:33], v[212:219], v[78:81], v1, v172 op_sel_hi:[0,0,0]
	s_nop 1
	v_mfma_scale_f32_16x16x128_f8f6f4 v[74:77], v[18:25], v[212:219], v[74:77], v1, v172 op_sel_hi:[0,0,0]
	s_nop 1
	v_mfma_scale_f32_16x16x128_f8f6f4 v[62:65], v[26:33], v[220:227], v[62:65], v1, v172 op_sel_hi:[0,0,0]
	s_nop 1
	v_mfma_scale_f32_16x16x128_f8f6f4 v[58:61], v[18:25], v[220:227], v[58:61], v1, v172 op_sel_hi:[0,0,0]
	s_nop 1
	v_mfma_scale_f32_16x16x128_f8f6f4 v[46:49], v[26:33], v[228:235], v[46:49], v1, v172 op_sel_hi:[0,0,0]
	s_nop 1
	v_mfma_scale_f32_16x16x128_f8f6f4 v[42:45], v[18:25], v[228:235], v[42:45], v1, v172 op_sel_hi:[0,0,0]
	s_setprio 0
	s_setprio 1
	s_nop 1
	v_mfma_scale_f32_16x16x128_f8f6f4 v[86:89], v[10:17], v[204:211], v[86:89], v1, v172 op_sel_hi:[0,0,0]
	s_nop 1
	v_mfma_scale_f32_16x16x128_f8f6f4 v[82:85], v[2:9], v[204:211], v[82:85], v1, v172 op_sel_hi:[0,0,0]
	s_nop 1
	v_mfma_scale_f32_16x16x128_f8f6f4 v[70:73], v[10:17], v[212:219], v[70:73], v1, v172 op_sel_hi:[0,0,0]
	s_nop 1
	v_mfma_scale_f32_16x16x128_f8f6f4 v[66:69], v[2:9], v[212:219], v[66:69], v1, v172 op_sel_hi:[0,0,0]
	s_nop 1
	v_mfma_scale_f32_16x16x128_f8f6f4 v[54:57], v[10:17], v[220:227], v[54:57], v1, v172 op_sel_hi:[0,0,0]
	s_nop 1
	v_mfma_scale_f32_16x16x128_f8f6f4 v[50:53], v[2:9], v[220:227], v[50:53], v1, v172 op_sel_hi:[0,0,0]
	s_nop 1
	v_mfma_scale_f32_16x16x128_f8f6f4 v[38:41], v[10:17], v[228:235], v[38:41], v1, v172 op_sel_hi:[0,0,0]
	s_nop 1
	v_mfma_scale_f32_16x16x128_f8f6f4 v[34:37], v[2:9], v[228:235], v[34:37], v1, v172 op_sel_hi:[0,0,0]
	s_setprio 0
	s_barrier
	s_add_i32 s57, s57, 2
	s_add_u32 s19, s19, 0x100
	s_addc_u32 s56, s56, 0
	s_add_u32 s22, s22, 0x100
	s_addc_u32 s23, s23, 0
	s_cmp_gt_u32 s57, 5
	s_cbranch_scc1 .LBB0_874

.LBB0_876:
	s_add_i32 s11, 0, 0x20400
	s_nop 11
	v_add_u32_e32 v18, s11, v182
	s_add_i32 s19, 0, 0x20800
	ds_read_b128 v[14:17], v203
	ds_read_b128 v[10:13], v203 offset:16
	ds_read_b128 v[6:9], v203 offset:512
	ds_read_b128 v[2:5], v203 offset:528
	v_add_u32_e32 v19, s19, v182
	v_add_u32_e32 v20, s11, v183
	v_add_u32_e32 v21, s19, v183
	v_add_u32_e32 v22, s11, v184
	v_add_u32_e32 v23, s19, v184
	ds_read_b32 v33, v18
	ds_read_b32 v32, v19
	ds_read_b32 v31, v20
	ds_read_b32 v30, v21
	ds_read_b32 v29, v22
	ds_read_b32 v28, v23
	v_add_u32_e32 v18, s11, v181
	v_add_u32_e32 v20, s19, v181
	ds_read2_b32 v[24:25], v18 offset0:128 offset1:144
	ds_read2_b32 v[26:27], v20 offset0:128 offset1:144
	ds_read2_b32 v[18:19], v18 offset0:160 offset1:176
	ds_read2_b32 v[22:23], v20 offset0:160 offset1:176
	v_add_u32_e32 v20, s18, v185
	v_add_u32_e32 v162, s54, v177
	v_ashrrev_i32_e32 v21, 31, v20
	v_cmp_gt_i32_e32 vcc, s39, v162
	s_and_saveexec_b64 s[18:19], vcc
	s_cbranch_execz .LBB0_878
	v_add_u32_e32 v163, 0, v181
	v_add_u32_e32 v164, 0x20800, v163
	v_add_u32_e32 v163, 0x20400, v163
	ds_read_b32 v166, v164
	ds_read_b32 v165, v163
	s_waitcnt lgkmcnt(0)
	v_pk_add_f32 v[154:155], v[154:155], v[10:11]
	v_mov_b32_e32 v205, v167
	v_pk_add_f32 v[158:159], v[158:159], v[14:15]
	v_mul_f32_e32 v166, 0x41800000, v166
	v_pk_mul_f32 v[154:155], v[154:155], v[166:167] op_sel_hi:[1,0]
	v_pk_mul_f32 v[158:159], v[158:159], v[166:167] op_sel_hi:[1,0]
	v_cvt_pk_fp8_f32 v205, v154, v155
	v_pk_add_f32 v[154:155], v[156:157], v[12:13]
	v_mov_b32_e32 v204, v167
	v_pk_mul_f32 v[154:155], v[154:155], v[166:167] op_sel_hi:[1,0]
	v_pk_add_f32 v[150:151], v[150:151], v[6:7]
	v_pk_add_f32 v[146:147], v[146:147], v[2:3]
	v_cvt_pk_fp8_f32 v204, v158, v159
	v_cvt_pk_fp8_f32 v205, v154, v155 op_sel:[0,0,1]
	v_pk_mul_f32 v[150:151], v[150:151], v[166:167] op_sel_hi:[1,0]
	v_pk_mul_f32 v[146:147], v[146:147], v[166:167] op_sel_hi:[1,0]
	v_mov_b32_e32 v154, v167
	v_mov_b32_e32 v155, v167
	v_cvt_pk_fp8_f32 v154, v150, v151
	v_cvt_pk_fp8_f32 v155, v146, v147
	v_pk_add_f32 v[160:161], v[160:161], v[16:17]
	v_pk_add_f32 v[152:153], v[152:153], v[8:9]
	v_pk_mul_f32 v[160:161], v[160:161], v[166:167] op_sel_hi:[1,0]
	v_pk_add_f32 v[146:147], v[148:149], v[4:5]
	v_mov_b32_e32 v164, v167
	v_cvt_pk_fp8_f32 v204, v160, v161 op_sel:[0,0,1]
	v_pk_mul_f32 v[152:153], v[152:153], v[166:167] op_sel_hi:[1,0]
	v_pk_mul_f32 v[146:147], v[146:147], v[166:167] op_sel_hi:[1,0]
	v_ashrrev_i64 v[164:165], 22, v[164:165]
	v_cvt_pk_fp8_f32 v154, v152, v153 op_sel:[0,0,1]
	v_cvt_pk_fp8_f32 v155, v146, v147 op_sel:[0,0,1]
	v_lshl_add_u64 v[146:147], s[2:3], 0, v[164:165]
	v_lshl_add_u64 v[146:147], v[146:147], 0, v[20:21]
	flat_store_dwordx2 v[146:147], v[204:205]
	flat_store_dwordx2 v[146:147], v[154:155] offset:128
